# baseline (speedup 1.0000x reference)
.LBB7_26:
	v_add_u32_e32 v254, 0x18000, v166
	v_add_u32_e32 v255, 0x1c000, v166
	s_lshl_b32 s34, s70, 8
	s_add_i32 s34, s34, s48
	v_or_b32_e32 v250, s34, v165
	v_ashrrev_i32_e32 v251, 31, v250
	v_lshl_add_u64 v[250:251], v[250:251], 3, s[12:13]
	s_lshl_b32 s35, s67, 8
	s_or_b32 s35, s35, s51
	v_or_b32_e32 v252, s35, v164
	v_ashrrev_i32_e32 v253, 31, v252
	v_lshl_add_u64 v[252:253], v[252:253], 2, s[14:15]
	global_load_dword v226, v[250:251], off offset:4
	global_load_dword v227, v[250:251], off offset:132
	global_load_dword v228, v[250:251], off offset:260
	global_load_dword v229, v[250:251], off offset:388
	global_load_dword v230, v[250:251], off offset:1028
	global_load_dword v231, v[250:251], off offset:1156
	global_load_dword v232, v[250:251], off offset:1284
	global_load_dword v233, v[250:251], off offset:1412
	global_load_dwordx4 v[234:237], v[252:253], off
	global_load_dwordx4 v[238:241], v[252:253], off offset:16
	global_load_dwordx4 v[242:245], v[252:253], off offset:128
	global_load_dwordx4 v[246:249], v[252:253], off offset:144
	s_add_u32 s28, s28, 0x30080
	s_addc_u32 s29, s29, 0
	s_add_u32 s71, s30, 0x100
	v_mov_b32_e32 v0, 0
	s_addc_u32 s72, s31, 0
	s_mov_b32 s73, -2
	v_mov_b32_e32 v1, v0
	v_mov_b32_e32 v2, v0
	v_mov_b32_e32 v3, v0
	v_mov_b32_e32 v4, v0
	v_mov_b32_e32 v5, v0
	v_mov_b32_e32 v6, v0
	v_mov_b32_e32 v7, v0
	v_mov_b32_e32 v12, v0
	v_mov_b32_e32 v13, v0
	v_mov_b32_e32 v14, v0
	v_mov_b32_e32 v15, v0
	v_mov_b32_e32 v20, v0
	v_mov_b32_e32 v21, v0
	v_mov_b32_e32 v22, v0
	v_mov_b32_e32 v23, v0
	v_mov_b32_e32 v28, v0
	v_mov_b32_e32 v29, v0
	v_mov_b32_e32 v30, v0
	v_mov_b32_e32 v31, v0
	v_mov_b32_e32 v36, v0
	v_mov_b32_e32 v37, v0
	v_mov_b32_e32 v38, v0
	v_mov_b32_e32 v39, v0
	v_mov_b32_e32 v44, v0
	v_mov_b32_e32 v45, v0
	v_mov_b32_e32 v46, v0
	v_mov_b32_e32 v47, v0
	v_mov_b32_e32 v52, v0
	v_mov_b32_e32 v53, v0
	v_mov_b32_e32 v54, v0
	v_mov_b32_e32 v55, v0
	v_mov_b32_e32 v8, v0
	v_mov_b32_e32 v9, v0
	v_mov_b32_e32 v10, v0
	v_mov_b32_e32 v11, v0
	v_mov_b32_e32 v16, v0
	v_mov_b32_e32 v17, v0
	v_mov_b32_e32 v18, v0
	v_mov_b32_e32 v19, v0
	v_mov_b32_e32 v24, v0
	v_mov_b32_e32 v25, v0
	v_mov_b32_e32 v26, v0
	v_mov_b32_e32 v27, v0
	v_mov_b32_e32 v32, v0
	v_mov_b32_e32 v33, v0
	v_mov_b32_e32 v34, v0
	v_mov_b32_e32 v35, v0
	v_mov_b32_e32 v40, v0
	v_mov_b32_e32 v41, v0
	v_mov_b32_e32 v42, v0
	v_mov_b32_e32 v43, v0
	v_mov_b32_e32 v48, v0
	v_mov_b32_e32 v49, v0
	v_mov_b32_e32 v50, v0
	v_mov_b32_e32 v51, v0
	v_mov_b32_e32 v56, v0
	v_mov_b32_e32 v57, v0
	v_mov_b32_e32 v58, v0
	v_mov_b32_e32 v59, v0
	v_mov_b32_e32 v60, v0
	v_mov_b32_e32 v61, v0
	v_mov_b32_e32 v62, v0
	v_mov_b32_e32 v63, v0
	v_mov_b32_e32 v64, v0
	v_mov_b32_e32 v65, v0
	v_mov_b32_e32 v66, v0
	v_mov_b32_e32 v67, v0
	v_mov_b32_e32 v68, v0
	v_mov_b32_e32 v69, v0
	v_mov_b32_e32 v70, v0
	v_mov_b32_e32 v71, v0
	v_mov_b32_e32 v76, v0
	v_mov_b32_e32 v77, v0
	v_mov_b32_e32 v78, v0
	v_mov_b32_e32 v79, v0
	v_mov_b32_e32 v84, v0
	v_mov_b32_e32 v85, v0
	v_mov_b32_e32 v86, v0
	v_mov_b32_e32 v87, v0
	v_mov_b32_e32 v92, v0
	v_mov_b32_e32 v93, v0
	v_mov_b32_e32 v94, v0
	v_mov_b32_e32 v95, v0
	v_mov_b32_e32 v100, v0
	v_mov_b32_e32 v101, v0
	v_mov_b32_e32 v102, v0
	v_mov_b32_e32 v103, v0
	v_mov_b32_e32 v112, v0
	v_mov_b32_e32 v113, v0
	v_mov_b32_e32 v114, v0
	v_mov_b32_e32 v115, v0
	v_mov_b32_e32 v116, v0
	v_mov_b32_e32 v117, v0
	v_mov_b32_e32 v118, v0
	v_mov_b32_e32 v119, v0
	v_mov_b32_e32 v72, v0
	v_mov_b32_e32 v73, v0
	v_mov_b32_e32 v74, v0
	v_mov_b32_e32 v75, v0
	v_mov_b32_e32 v80, v0
	v_mov_b32_e32 v81, v0
	v_mov_b32_e32 v82, v0
	v_mov_b32_e32 v83, v0
	v_mov_b32_e32 v88, v0
	v_mov_b32_e32 v89, v0
	v_mov_b32_e32 v90, v0
	v_mov_b32_e32 v91, v0
	v_mov_b32_e32 v96, v0
	v_mov_b32_e32 v97, v0
	v_mov_b32_e32 v98, v0
	v_mov_b32_e32 v99, v0
	v_mov_b32_e32 v104, v0
	v_mov_b32_e32 v105, v0
	v_mov_b32_e32 v106, v0
	v_mov_b32_e32 v107, v0
	v_mov_b32_e32 v108, v0
	v_mov_b32_e32 v109, v0
	v_mov_b32_e32 v110, v0
	v_mov_b32_e32 v111, v0
	v_mov_b32_e32 v120, v0
	v_mov_b32_e32 v121, v0
	v_mov_b32_e32 v122, v0
	v_mov_b32_e32 v123, v0
	v_mov_b32_e32 v124, v0
	v_mov_b32_e32 v125, v0
	v_mov_b32_e32 v126, v0
	v_mov_b32_e32 v127, v0
	ds_read_b128 v[128:131], v170
	ds_read_b128 v[132:135], v170 offset:1024
	ds_read_b128 v[136:139], v170 offset:2048
	ds_read_b128 v[140:143], v170 offset:3072
.LBB7_27:
	s_add_u32 s30, s28, 0xfffd0080
	s_addc_u32 s31, s29, -1
	s_cmp_eq_u32 s73, 8
	s_cselect_b32 s35, s9, s31
	s_cselect_b32 s34, s8, s30
	s_cselect_b32 s31, s1, s72
	s_cselect_b32 s30, s0, s71
	s_add_i32 m0, s43, 0xc000
	ds_read_b128 v[158:161], v171
	ds_read_b128 v[176:179], v171 offset:1024
	ds_read_b128 v[180:183], v171 offset:2048
	ds_read_b128 v[184:187], v171 offset:3072
	ds_read_b128 v[188:191], v171 offset:4096
	ds_read_b128 v[192:195], v171 offset:5120
	ds_read_b128 v[196:199], v171 offset:6144
	ds_read_b128 v[200:203], v171 offset:7168
	global_load_lds_dwordx4 v152, s[28:29]
	s_add_i32 m0, s43, 0xe000
	s_nop 0
	global_load_lds_dwordx4 v154, s[28:29]
	s_waitcnt lgkmcnt(8)
	s_barrier
	s_waitcnt lgkmcnt(0)
	v_mfma_f32_16x16x32_f16 v[124:127], v[128:131], v[158:161], v[124:127]
	v_mfma_f32_16x16x32_f16 v[120:123], v[136:139], v[158:161], v[120:123]
	v_mfma_f32_16x16x32_f16 v[108:111], v[128:131], v[180:183], v[108:111]
	v_mfma_f32_16x16x32_f16 v[104:107], v[136:139], v[180:183], v[104:107]
	v_mfma_f32_16x16x32_f16 v[96:99], v[128:131], v[188:191], v[96:99]
	v_mfma_f32_16x16x32_f16 v[88:91], v[136:139], v[188:191], v[88:91]
	v_mfma_f32_16x16x32_f16 v[80:83], v[128:131], v[196:199], v[80:83]
	v_mfma_f32_16x16x32_f16 v[72:75], v[136:139], v[196:199], v[72:75]
	v_mfma_f32_16x16x32_f16 v[124:127], v[132:135], v[176:179], v[124:127]
	v_mfma_f32_16x16x32_f16 v[120:123], v[140:143], v[176:179], v[120:123]
	v_mfma_f32_16x16x32_f16 v[108:111], v[132:135], v[184:187], v[108:111]
	v_mfma_f32_16x16x32_f16 v[104:107], v[140:143], v[184:187], v[104:107]
	v_mfma_f32_16x16x32_f16 v[96:99], v[132:135], v[192:195], v[96:99]
	v_mfma_f32_16x16x32_f16 v[88:91], v[140:143], v[192:195], v[88:91]
	v_mfma_f32_16x16x32_f16 v[80:83], v[132:135], v[200:203], v[80:83]
	v_mfma_f32_16x16x32_f16 v[72:75], v[140:143], v[200:203], v[72:75]
	s_barrier
	s_add_i32 s74, s65, s42
	s_mov_b32 m0, s74
	ds_read_b128 v[204:207], v172
	ds_read_b128 v[208:211], v172 offset:1024
	ds_read_b128 v[212:215], v172 offset:2048
	ds_read_b128 v[216:219], v172 offset:3072
	global_load_lds_dwordx4 v146, s[30:31]
	s_add_i32 m0, s74, 0x2000
	s_add_u32 s78, s30, 0x80
	s_addc_u32 s79, s31, 0
	global_load_lds_dwordx4 v150, s[30:31]
	s_barrier
	s_waitcnt lgkmcnt(0)
	v_mfma_f32_16x16x32_f16 v[116:119], v[204:207], v[158:161], v[116:119]
	v_mfma_f32_16x16x32_f16 v[112:115], v[212:215], v[158:161], v[112:115]
	v_mfma_f32_16x16x32_f16 v[100:103], v[204:207], v[180:183], v[100:103]
	v_mfma_f32_16x16x32_f16 v[92:95], v[212:215], v[180:183], v[92:95]
	v_mfma_f32_16x16x32_f16 v[84:87], v[204:207], v[188:191], v[84:87]
	v_mfma_f32_16x16x32_f16 v[76:79], v[212:215], v[188:191], v[76:79]
	v_mfma_f32_16x16x32_f16 v[68:71], v[204:207], v[196:199], v[68:71]
	v_mfma_f32_16x16x32_f16 v[64:67], v[212:215], v[196:199], v[64:67]
	v_mfma_f32_16x16x32_f16 v[116:119], v[208:211], v[176:179], v[116:119]
	v_mfma_f32_16x16x32_f16 v[112:115], v[216:219], v[176:179], v[112:115]
	v_mfma_f32_16x16x32_f16 v[100:103], v[208:211], v[184:187], v[100:103]
	v_mfma_f32_16x16x32_f16 v[92:95], v[216:219], v[184:187], v[92:95]
	v_mfma_f32_16x16x32_f16 v[84:87], v[208:211], v[192:195], v[84:87]
	v_mfma_f32_16x16x32_f16 v[76:79], v[216:219], v[192:195], v[76:79]
	v_mfma_f32_16x16x32_f16 v[68:71], v[208:211], v[200:203], v[68:71]
	v_mfma_f32_16x16x32_f16 v[64:67], v[216:219], v[200:203], v[64:67]
	s_barrier
	s_mov_b32 m0, s43
	ds_read_b128 v[158:161], v171 offset:16384
	ds_read_b128 v[176:179], v171 offset:17408
	ds_read_b128 v[180:183], v171 offset:18432
	ds_read_b128 v[184:187], v171 offset:19456
	ds_read_b128 v[188:191], v171 offset:20480
	ds_read_b128 v[192:195], v171 offset:21504
	ds_read_b128 v[196:199], v171 offset:22528
	ds_read_b128 v[200:203], v171 offset:23552
	global_load_lds_dwordx4 v144, s[34:35]
	s_mov_b32 m0, s44
	s_add_u32 s80, s34, 0x80
	s_addc_u32 s81, s35, 0
	global_load_lds_dwordx4 v148, s[34:35]
	s_waitcnt vmcnt(10)
	s_barrier
	s_waitcnt lgkmcnt(0)
	v_mfma_f32_16x16x32_f16 v[60:63], v[128:131], v[158:161], v[60:63]
	v_mfma_f32_16x16x32_f16 v[56:59], v[136:139], v[158:161], v[56:59]
	v_mfma_f32_16x16x32_f16 v[48:51], v[128:131], v[180:183], v[48:51]
	v_mfma_f32_16x16x32_f16 v[40:43], v[136:139], v[180:183], v[40:43]
	v_mfma_f32_16x16x32_f16 v[32:35], v[128:131], v[188:191], v[32:35]
	v_mfma_f32_16x16x32_f16 v[24:27], v[136:139], v[188:191], v[24:27]
	v_mfma_f32_16x16x32_f16 v[16:19], v[128:131], v[196:199], v[16:19]
	v_mfma_f32_16x16x32_f16 v[8:11], v[136:139], v[196:199], v[8:11]
	v_mfma_f32_16x16x32_f16 v[60:63], v[132:135], v[176:179], v[60:63]
	v_mfma_f32_16x16x32_f16 v[56:59], v[140:143], v[176:179], v[56:59]
	v_mfma_f32_16x16x32_f16 v[48:51], v[132:135], v[184:187], v[48:51]
	v_mfma_f32_16x16x32_f16 v[40:43], v[140:143], v[184:187], v[40:43]
	v_mfma_f32_16x16x32_f16 v[32:35], v[132:135], v[192:195], v[32:35]
	v_mfma_f32_16x16x32_f16 v[24:27], v[140:143], v[192:195], v[24:27]
	v_mfma_f32_16x16x32_f16 v[16:19], v[132:135], v[200:203], v[16:19]
	v_mfma_f32_16x16x32_f16 v[8:11], v[140:143], v[200:203], v[8:11]
	s_barrier
	s_add_i32 s76, s66, s42
	s_mov_b32 m0, s76
	s_add_u32 s74, s30, 0xc000
	s_addc_u32 s75, s31, 0
	global_load_lds_dwordx4 v146, s[74:75]
	s_add_i32 m0, s76, 0x2000
	s_nop 0
	global_load_lds_dwordx4 v150, s[74:75]
	s_add_i32 s74, 0, 0x18000
	ds_read_b128 v[128:131], v254
	ds_read_b128 v[132:135], v254 offset:1024
	ds_read_b128 v[136:139], v254 offset:2048
	ds_read_b128 v[140:143], v254 offset:3072
	s_waitcnt vmcnt(6)
	s_barrier
	v_mfma_f32_16x16x32_f16 v[52:55], v[204:207], v[158:161], v[52:55]
	v_mfma_f32_16x16x32_f16 v[44:47], v[212:215], v[158:161], v[44:47]
	v_mfma_f32_16x16x32_f16 v[36:39], v[204:207], v[180:183], v[36:39]
	v_mfma_f32_16x16x32_f16 v[28:31], v[212:215], v[180:183], v[28:31]
	v_mfma_f32_16x16x32_f16 v[20:23], v[204:207], v[188:191], v[20:23]
	v_mfma_f32_16x16x32_f16 v[12:15], v[212:215], v[188:191], v[12:15]
	v_mfma_f32_16x16x32_f16 v[4:7], v[204:207], v[196:199], v[4:7]
	v_mfma_f32_16x16x32_f16 v[0:3], v[212:215], v[196:199], v[0:3]
	v_mfma_f32_16x16x32_f16 v[52:55], v[208:211], v[176:179], v[52:55]
	v_mfma_f32_16x16x32_f16 v[44:47], v[216:219], v[176:179], v[44:47]
	v_mfma_f32_16x16x32_f16 v[36:39], v[208:211], v[184:187], v[36:39]
	v_mfma_f32_16x16x32_f16 v[28:31], v[216:219], v[184:187], v[28:31]
	v_mfma_f32_16x16x32_f16 v[20:23], v[208:211], v[192:195], v[20:23]
	v_mfma_f32_16x16x32_f16 v[12:15], v[216:219], v[192:195], v[12:15]
	v_mfma_f32_16x16x32_f16 v[4:7], v[208:211], v[200:203], v[4:7]
	v_mfma_f32_16x16x32_f16 v[0:3], v[216:219], v[200:203], v[0:3]
	s_barrier
	s_add_u32 s34, s34, 0x30000
	s_addc_u32 s35, s35, 0
	s_mov_b32 m0, s45
	ds_read_b128 v[158:161], v171 offset:32768
	ds_read_b128 v[176:179], v171 offset:33792
	ds_read_b128 v[180:183], v171 offset:34816
	ds_read_b128 v[184:187], v171 offset:35840
	ds_read_b128 v[188:191], v171 offset:36864
	ds_read_b128 v[192:195], v171 offset:37888
	ds_read_b128 v[196:199], v171 offset:38912
	ds_read_b128 v[200:203], v171 offset:39936
	global_load_lds_dwordx4 v144, s[34:35]
	s_mov_b32 m0, s46
	s_nop 0
	global_load_lds_dwordx4 v148, s[34:35]
	s_waitcnt lgkmcnt(8)
	s_barrier
	s_waitcnt lgkmcnt(0)
	v_mfma_f32_16x16x32_f16 v[124:127], v[128:131], v[158:161], v[124:127]
	v_mfma_f32_16x16x32_f16 v[120:123], v[136:139], v[158:161], v[120:123]
	v_mfma_f32_16x16x32_f16 v[108:111], v[128:131], v[180:183], v[108:111]
	v_mfma_f32_16x16x32_f16 v[104:107], v[136:139], v[180:183], v[104:107]
	v_mfma_f32_16x16x32_f16 v[96:99], v[128:131], v[188:191], v[96:99]
	v_mfma_f32_16x16x32_f16 v[88:91], v[136:139], v[188:191], v[88:91]
	v_mfma_f32_16x16x32_f16 v[80:83], v[128:131], v[196:199], v[80:83]
	v_mfma_f32_16x16x32_f16 v[72:75], v[136:139], v[196:199], v[72:75]
	v_mfma_f32_16x16x32_f16 v[124:127], v[132:135], v[176:179], v[124:127]
	v_mfma_f32_16x16x32_f16 v[120:123], v[140:143], v[176:179], v[120:123]
	v_mfma_f32_16x16x32_f16 v[108:111], v[132:135], v[184:187], v[108:111]
	v_mfma_f32_16x16x32_f16 v[104:107], v[140:143], v[184:187], v[104:107]
	v_mfma_f32_16x16x32_f16 v[96:99], v[132:135], v[192:195], v[96:99]
	v_mfma_f32_16x16x32_f16 v[88:91], v[140:143], v[192:195], v[88:91]
	v_mfma_f32_16x16x32_f16 v[80:83], v[132:135], v[200:203], v[80:83]
	v_mfma_f32_16x16x32_f16 v[72:75], v[140:143], v[200:203], v[72:75]
	s_barrier
	s_add_i32 s34, 0, 0x1c000
	s_add_i32 s35, s74, s42
	s_mov_b32 m0, s35
	ds_read_b128 v[204:207], v255
	ds_read_b128 v[208:211], v255 offset:1024
	ds_read_b128 v[212:215], v255 offset:2048
	ds_read_b128 v[216:219], v255 offset:3072
	global_load_lds_dwordx4 v146, s[78:79]
	s_add_i32 m0, s35, 0x2000
	s_nop 0
	global_load_lds_dwordx4 v150, s[78:79]
	s_barrier
	s_waitcnt lgkmcnt(0)
	v_mfma_f32_16x16x32_f16 v[116:119], v[204:207], v[158:161], v[116:119]
	v_mfma_f32_16x16x32_f16 v[112:115], v[212:215], v[158:161], v[112:115]
	v_mfma_f32_16x16x32_f16 v[100:103], v[204:207], v[180:183], v[100:103]
	v_mfma_f32_16x16x32_f16 v[92:95], v[212:215], v[180:183], v[92:95]
	v_mfma_f32_16x16x32_f16 v[84:87], v[204:207], v[188:191], v[84:87]
	v_mfma_f32_16x16x32_f16 v[76:79], v[212:215], v[188:191], v[76:79]
	v_mfma_f32_16x16x32_f16 v[68:71], v[204:207], v[196:199], v[68:71]
	v_mfma_f32_16x16x32_f16 v[64:67], v[212:215], v[196:199], v[64:67]
	v_mfma_f32_16x16x32_f16 v[116:119], v[208:211], v[176:179], v[116:119]
	v_mfma_f32_16x16x32_f16 v[112:115], v[216:219], v[176:179], v[112:115]
	v_mfma_f32_16x16x32_f16 v[100:103], v[208:211], v[184:187], v[100:103]
	v_mfma_f32_16x16x32_f16 v[92:95], v[216:219], v[184:187], v[92:95]
	v_mfma_f32_16x16x32_f16 v[84:87], v[208:211], v[192:195], v[84:87]
	v_mfma_f32_16x16x32_f16 v[76:79], v[216:219], v[192:195], v[76:79]
	v_mfma_f32_16x16x32_f16 v[68:71], v[208:211], v[200:203], v[68:71]
	v_mfma_f32_16x16x32_f16 v[64:67], v[216:219], v[200:203], v[64:67]
	s_barrier
	s_mov_b32 m0, s49
	ds_read_b128 v[158:161], v171 offset:49152
	ds_read_b128 v[176:179], v171 offset:50176
	ds_read_b128 v[180:183], v171 offset:51200
	ds_read_b128 v[184:187], v171 offset:52224
	ds_read_b128 v[188:191], v171 offset:53248
	ds_read_b128 v[192:195], v171 offset:54272
	ds_read_b128 v[196:199], v171 offset:55296
	ds_read_b128 v[200:203], v171 offset:56320
	global_load_lds_dwordx4 v144, s[80:81]
	s_mov_b32 m0, s50
	s_nop 0
	global_load_lds_dwordx4 v148, s[80:81]
	s_waitcnt vmcnt(10)
	s_barrier
	s_waitcnt lgkmcnt(0)
	v_mfma_f32_16x16x32_f16 v[60:63], v[128:131], v[158:161], v[60:63]
	v_mfma_f32_16x16x32_f16 v[56:59], v[136:139], v[158:161], v[56:59]
	v_mfma_f32_16x16x32_f16 v[48:51], v[128:131], v[180:183], v[48:51]
	v_mfma_f32_16x16x32_f16 v[40:43], v[136:139], v[180:183], v[40:43]
	v_mfma_f32_16x16x32_f16 v[32:35], v[128:131], v[188:191], v[32:35]
	v_mfma_f32_16x16x32_f16 v[24:27], v[136:139], v[188:191], v[24:27]
	v_mfma_f32_16x16x32_f16 v[16:19], v[128:131], v[196:199], v[16:19]
	v_mfma_f32_16x16x32_f16 v[8:11], v[136:139], v[196:199], v[8:11]
	v_mfma_f32_16x16x32_f16 v[60:63], v[132:135], v[176:179], v[60:63]
	v_mfma_f32_16x16x32_f16 v[56:59], v[140:143], v[176:179], v[56:59]
	v_mfma_f32_16x16x32_f16 v[48:51], v[132:135], v[184:187], v[48:51]
	v_mfma_f32_16x16x32_f16 v[40:43], v[140:143], v[184:187], v[40:43]
	v_mfma_f32_16x16x32_f16 v[32:35], v[132:135], v[192:195], v[32:35]
	v_mfma_f32_16x16x32_f16 v[24:27], v[140:143], v[192:195], v[24:27]
	v_mfma_f32_16x16x32_f16 v[16:19], v[132:135], v[200:203], v[16:19]
	v_mfma_f32_16x16x32_f16 v[8:11], v[140:143], v[200:203], v[8:11]
	s_barrier
	s_add_i32 s34, s34, s42
	s_mov_b32 m0, s34
	s_add_u32 s30, s30, 0xc080
	s_addc_u32 s31, s31, 0
	global_load_lds_dwordx4 v146, s[30:31]
	s_add_i32 m0, s34, 0x2000
	s_nop 0
	global_load_lds_dwordx4 v150, s[30:31]
	ds_read_b128 v[128:131], v170
	ds_read_b128 v[132:135], v170 offset:1024
	ds_read_b128 v[136:139], v170 offset:2048
	ds_read_b128 v[140:143], v170 offset:3072
	s_waitcnt vmcnt(6)
	s_barrier
	v_mfma_f32_16x16x32_f16 v[52:55], v[204:207], v[158:161], v[52:55]
	v_mfma_f32_16x16x32_f16 v[44:47], v[212:215], v[158:161], v[44:47]
	v_mfma_f32_16x16x32_f16 v[36:39], v[204:207], v[180:183], v[36:39]
	v_mfma_f32_16x16x32_f16 v[28:31], v[212:215], v[180:183], v[28:31]
	v_mfma_f32_16x16x32_f16 v[20:23], v[204:207], v[188:191], v[20:23]
	v_mfma_f32_16x16x32_f16 v[12:15], v[212:215], v[188:191], v[12:15]
	v_mfma_f32_16x16x32_f16 v[4:7], v[204:207], v[196:199], v[4:7]
	v_mfma_f32_16x16x32_f16 v[0:3], v[212:215], v[196:199], v[0:3]
	v_mfma_f32_16x16x32_f16 v[52:55], v[208:211], v[176:179], v[52:55]
	v_mfma_f32_16x16x32_f16 v[44:47], v[216:219], v[176:179], v[44:47]
	v_mfma_f32_16x16x32_f16 v[36:39], v[208:211], v[184:187], v[36:39]
	v_mfma_f32_16x16x32_f16 v[28:31], v[216:219], v[184:187], v[28:31]
	v_mfma_f32_16x16x32_f16 v[20:23], v[208:211], v[192:195], v[20:23]
	v_mfma_f32_16x16x32_f16 v[12:15], v[216:219], v[192:195], v[12:15]
	v_mfma_f32_16x16x32_f16 v[4:7], v[208:211], v[200:203], v[4:7]
	v_mfma_f32_16x16x32_f16 v[0:3], v[216:219], v[200:203], v[0:3]
	s_barrier
	s_add_i32 s73, s73, 2
	s_add_u32 s28, s28, 0x100
	s_addc_u32 s29, s29, 0
	s_add_u32 s71, s71, 0x100
	s_addc_u32 s72, s72, 0
	s_cmp_gt_u32 s73, 9
	s_cbranch_scc0 .LBB7_27
	s_lshl_b32 s28, s70, 8
	s_add_i32 s28, s28, s48
	s_lshl_b32 s29, s67, 8
	s_or_b32 s29, s29, s51
	s_waitcnt vmcnt(6)
	v_pk_fma_f32 v[126:127], v[126:127], v[226:227], v[236:237] op_sel_hi:[1,0,1]
	v_pk_fma_f32 v[124:125], v[124:125], v[226:227], v[234:235] op_sel_hi:[1,0,1]
	v_pk_fma_f32 v[186:187], v[122:123], v[226:227], v[240:241] op_sel_hi:[1,0,1]
	v_pk_fma_f32 v[122:123], v[120:121], v[226:227], v[238:239] op_sel_hi:[1,0,1]
	v_cvt_pk_f16_f32 v120, v124, v125
	v_cvt_pk_f16_f32 v121, v126, v127
	v_cvt_pk_f16_f32 v122, v122, v123
	v_cvt_pk_f16_f32 v123, v186, v187
	ds_write_b128 v173, v[120:123]
	v_pk_fma_f32 v[118:119], v[118:119], v[226:227], v[244:245] op_sel_hi:[1,0,1]
	v_pk_fma_f32 v[116:117], v[116:117], v[226:227], v[242:243] op_sel_hi:[1,0,1]
	v_pk_fma_f32 v[120:121], v[114:115], v[226:227], v[248:249] op_sel_hi:[1,0,1]
	v_pk_fma_f32 v[114:115], v[112:113], v[226:227], v[246:247] op_sel_hi:[1,0,1]
	v_cvt_pk_f16_f32 v112, v116, v117
	v_cvt_pk_f16_f32 v113, v118, v119
	v_cvt_pk_f16_f32 v114, v114, v115
	v_cvt_pk_f16_f32 v115, v120, v121
	ds_write_b128 v173, v[112:115] offset:64
	v_or_b32_e32 v116, s28, v167
	ds_read_b128 v[112:115], v174
	v_mul_lo_u32 v116, v116, s10
	v_add_u32_e32 v120, s29, v116
	v_lshlrev_b32_e32 v121, 1, v120
	v_add_u32_e32 v122, v121, v168
	ds_read_b128 v[116:119], v174 offset:1152
	s_waitcnt lgkmcnt(0)
	buffer_store_dwordx4 v[112:115], v122, s[20:23], 0 offen nt
	v_pk_fma_f32 v[110:111], v[110:111], v[226:227], v[236:237] op_sel:[0,1,0]
	v_pk_fma_f32 v[108:109], v[108:109], v[226:227], v[234:235] op_sel:[0,1,0]
	v_pk_fma_f32 v[112:113], v[106:107], v[226:227], v[240:241] op_sel:[0,1,0]
	v_pk_fma_f32 v[106:107], v[104:105], v[226:227], v[238:239] op_sel:[0,1,0]
	v_cvt_pk_f16_f32 v104, v108, v109
	v_cvt_pk_f16_f32 v105, v110, v111
	v_cvt_pk_f16_f32 v106, v106, v107
	v_cvt_pk_f16_f32 v107, v112, v113
	ds_write_b128 v173, v[104:107]
	v_pk_fma_f32 v[102:103], v[102:103], v[226:227], v[244:245] op_sel:[0,1,0]
	v_pk_fma_f32 v[100:101], v[100:101], v[226:227], v[242:243] op_sel:[0,1,0]
	v_pk_fma_f32 v[104:105], v[94:95], v[226:227], v[248:249] op_sel:[0,1,0]
	v_pk_fma_f32 v[94:95], v[92:93], v[226:227], v[246:247] op_sel:[0,1,0]
	v_cvt_pk_f16_f32 v92, v100, v101
	v_cvt_pk_f16_f32 v93, v102, v103
	v_cvt_pk_f16_f32 v94, v94, v95
	v_cvt_pk_f16_f32 v95, v104, v105
	ds_write_b128 v173, v[92:95] offset:64
	ds_read_b128 v[92:95], v174
	ds_read_b128 v[100:103], v174 offset:1152
	v_add_u32_e32 v104, s55, v121
	v_add_u32_e32 v114, v121, v169
	v_add_u32_e32 v105, v104, v168
	buffer_store_dwordx4 v[116:119], v114, s[20:23], 0 offen nt
	s_waitcnt lgkmcnt(1)
	buffer_store_dwordx4 v[92:95], v105, s[20:23], 0 offen nt
	v_pk_fma_f32 v[86:87], v[86:87], v[228:229], v[244:245] op_sel_hi:[1,0,1]
	v_pk_fma_f32 v[84:85], v[84:85], v[228:229], v[242:243] op_sel_hi:[1,0,1]
	v_pk_fma_f32 v[92:93], v[98:99], v[228:229], v[236:237] op_sel_hi:[1,0,1]
	v_pk_fma_f32 v[94:95], v[96:97], v[228:229], v[234:235] op_sel_hi:[1,0,1]
	v_pk_fma_f32 v[96:97], v[90:91], v[228:229], v[240:241] op_sel_hi:[1,0,1]
	v_pk_fma_f32 v[90:91], v[88:89], v[228:229], v[238:239] op_sel_hi:[1,0,1]
	v_cvt_pk_f16_f32 v88, v94, v95
	v_cvt_pk_f16_f32 v89, v92, v93
	v_cvt_pk_f16_f32 v90, v90, v91
	v_cvt_pk_f16_f32 v91, v96, v97
	ds_write_b128 v173, v[88:91]
	v_pk_fma_f32 v[88:89], v[78:79], v[228:229], v[248:249] op_sel_hi:[1,0,1]
	v_pk_fma_f32 v[78:79], v[76:77], v[228:229], v[246:247] op_sel_hi:[1,0,1]
	v_cvt_pk_f16_f32 v76, v84, v85
	v_cvt_pk_f16_f32 v77, v86, v87
	v_cvt_pk_f16_f32 v78, v78, v79
	v_cvt_pk_f16_f32 v79, v88, v89
	ds_write_b128 v173, v[76:79] offset:64
	ds_read_b128 v[76:79], v174
	ds_read_b128 v[84:87], v174 offset:1152
	v_add_u32_e32 v88, s55, v104
	v_add_u32_e32 v105, v104, v169
	v_add_u32_e32 v89, v88, v168
	s_waitcnt lgkmcnt(4)
	buffer_store_dwordx4 v[100:103], v105, s[20:23], 0 offen nt
	s_waitcnt lgkmcnt(1)
	buffer_store_dwordx4 v[76:79], v89, s[20:23], 0 offen nt
	v_pk_fma_f32 v[70:71], v[70:71], v[228:229], v[244:245] op_sel:[0,1,0]
	v_pk_fma_f32 v[68:69], v[68:69], v[228:229], v[242:243] op_sel:[0,1,0]
	v_add_u32_e32 v76, v88, v169
	s_waitcnt lgkmcnt(0)
	buffer_store_dwordx4 v[84:87], v76, s[20:23], 0 offen nt
	v_pk_fma_f32 v[76:77], v[82:83], v[228:229], v[236:237] op_sel:[0,1,0]
	v_pk_fma_f32 v[78:79], v[80:81], v[228:229], v[234:235] op_sel:[0,1,0]
	v_pk_fma_f32 v[80:81], v[74:75], v[228:229], v[240:241] op_sel:[0,1,0]
	v_pk_fma_f32 v[74:75], v[72:73], v[228:229], v[238:239] op_sel:[0,1,0]
	v_cvt_pk_f16_f32 v72, v78, v79
	v_cvt_pk_f16_f32 v73, v76, v77
	v_cvt_pk_f16_f32 v74, v74, v75
	v_cvt_pk_f16_f32 v75, v80, v81
	ds_write_b128 v173, v[72:75]
	v_pk_fma_f32 v[72:73], v[66:67], v[228:229], v[248:249] op_sel:[0,1,0]
	v_pk_fma_f32 v[66:67], v[64:65], v[228:229], v[246:247] op_sel:[0,1,0]
	v_cvt_pk_f16_f32 v64, v68, v69
	v_cvt_pk_f16_f32 v65, v70, v71
	v_cvt_pk_f16_f32 v66, v66, v67
	v_cvt_pk_f16_f32 v67, v72, v73
	ds_write_b128 v173, v[64:67] offset:64
	ds_read_b128 v[64:67], v174
	ds_read_b128 v[68:71], v174 offset:1152
	v_add_u32_e32 v72, s56, v120
	v_lshlrev_b32_e32 v73, 1, v72
	v_add_u32_e32 v74, v73, v168
	s_waitcnt lgkmcnt(1)
	buffer_store_dwordx4 v[64:67], v74, s[20:23], 0 offen nt
	v_pk_fma_f32 v[62:63], v[62:63], v[230:231], v[236:237] op_sel_hi:[1,0,1]
	v_pk_fma_f32 v[60:61], v[60:61], v[230:231], v[234:235] op_sel_hi:[1,0,1]
	v_pk_fma_f32 v[64:65], v[58:59], v[230:231], v[240:241] op_sel_hi:[1,0,1]
	v_pk_fma_f32 v[58:59], v[56:57], v[230:231], v[238:239] op_sel_hi:[1,0,1]
	v_cvt_pk_f16_f32 v56, v60, v61
	v_cvt_pk_f16_f32 v57, v62, v63
	v_cvt_pk_f16_f32 v58, v58, v59
	v_cvt_pk_f16_f32 v59, v64, v65
	ds_write_b128 v173, v[56:59]
	v_pk_fma_f32 v[54:55], v[54:55], v[230:231], v[244:245] op_sel_hi:[1,0,1]
	v_pk_fma_f32 v[52:53], v[52:53], v[230:231], v[242:243] op_sel_hi:[1,0,1]
	v_pk_fma_f32 v[56:57], v[46:47], v[230:231], v[248:249] op_sel_hi:[1,0,1]
	v_pk_fma_f32 v[46:47], v[44:45], v[230:231], v[246:247] op_sel_hi:[1,0,1]
	v_cvt_pk_f16_f32 v44, v52, v53
	v_cvt_pk_f16_f32 v45, v54, v55
	v_cvt_pk_f16_f32 v46, v46, v47
	v_cvt_pk_f16_f32 v47, v56, v57
	ds_write_b128 v173, v[44:47] offset:64
	ds_read_b128 v[44:47], v174
	ds_read_b128 v[52:55], v174 offset:1152
	v_add_u32_e32 v56, s62, v88
	v_add_u32_e32 v66, v73, v169
	v_add_u32_e32 v57, v56, v168
	s_waitcnt lgkmcnt(4)
	buffer_store_dwordx4 v[68:71], v66, s[20:23], 0 offen nt
	s_waitcnt lgkmcnt(1)
	buffer_store_dwordx4 v[44:47], v57, s[20:23], 0 offen nt
	v_pk_fma_f32 v[38:39], v[38:39], v[230:231], v[244:245] op_sel:[0,1,0]
	v_pk_fma_f32 v[36:37], v[36:37], v[230:231], v[242:243] op_sel:[0,1,0]
	v_add_u32_e32 v44, v56, v169
	s_waitcnt lgkmcnt(0)
	buffer_store_dwordx4 v[52:55], v44, s[20:23], 0 offen nt
	v_pk_fma_f32 v[44:45], v[50:51], v[230:231], v[236:237] op_sel:[0,1,0]
	v_pk_fma_f32 v[46:47], v[48:49], v[230:231], v[234:235] op_sel:[0,1,0]
	v_pk_fma_f32 v[48:49], v[42:43], v[230:231], v[240:241] op_sel:[0,1,0]
	v_pk_fma_f32 v[42:43], v[40:41], v[230:231], v[238:239] op_sel:[0,1,0]
	v_cvt_pk_f16_f32 v40, v46, v47
	v_cvt_pk_f16_f32 v41, v44, v45
	v_cvt_pk_f16_f32 v42, v42, v43
	v_cvt_pk_f16_f32 v43, v48, v49
	ds_write_b128 v173, v[40:43]
	v_pk_fma_f32 v[40:41], v[30:31], v[230:231], v[248:249] op_sel:[0,1,0]
	v_pk_fma_f32 v[30:31], v[28:29], v[230:231], v[246:247] op_sel:[0,1,0]
	v_cvt_pk_f16_f32 v28, v36, v37
	v_cvt_pk_f16_f32 v29, v38, v39
	v_cvt_pk_f16_f32 v30, v30, v31
	v_cvt_pk_f16_f32 v31, v40, v41
	ds_write_b128 v173, v[28:31] offset:64
	ds_read_b128 v[28:31], v174
	ds_read_b128 v[36:39], v174 offset:1152
	v_add_u32_e32 v40, s63, v72
	v_lshlrev_b32_e32 v41, 1, v40
	v_add_u32_e32 v42, v41, v168
	s_waitcnt lgkmcnt(1)
	buffer_store_dwordx4 v[28:31], v42, s[20:23], 0 offen nt
	v_pk_fma_f32 v[22:23], v[22:23], v[232:233], v[244:245] op_sel_hi:[1,0,1]
	v_pk_fma_f32 v[20:21], v[20:21], v[232:233], v[242:243] op_sel_hi:[1,0,1]
	v_add_u32_e32 v28, v41, v169
	s_waitcnt lgkmcnt(0)
	buffer_store_dwordx4 v[36:39], v28, s[20:23], 0 offen nt
	v_pk_fma_f32 v[28:29], v[34:35], v[232:233], v[236:237] op_sel_hi:[1,0,1]
	v_pk_fma_f32 v[30:31], v[32:33], v[232:233], v[234:235] op_sel_hi:[1,0,1]
	v_pk_fma_f32 v[32:33], v[26:27], v[232:233], v[240:241] op_sel_hi:[1,0,1]
	v_pk_fma_f32 v[26:27], v[24:25], v[232:233], v[238:239] op_sel_hi:[1,0,1]
	v_cvt_pk_f16_f32 v24, v30, v31
	v_cvt_pk_f16_f32 v25, v28, v29
	v_cvt_pk_f16_f32 v26, v26, v27
	v_cvt_pk_f16_f32 v27, v32, v33
	ds_write_b128 v173, v[24:27]
	v_pk_fma_f32 v[24:25], v[14:15], v[232:233], v[248:249] op_sel_hi:[1,0,1]
	v_pk_fma_f32 v[14:15], v[12:13], v[232:233], v[246:247] op_sel_hi:[1,0,1]
	v_cvt_pk_f16_f32 v12, v20, v21
	v_cvt_pk_f16_f32 v13, v22, v23
	v_cvt_pk_f16_f32 v14, v14, v15
	v_cvt_pk_f16_f32 v15, v24, v25
	ds_write_b128 v173, v[12:15] offset:64
	ds_read_b128 v[12:15], v174
	ds_read_b128 v[20:23], v174 offset:1152
	v_add_u32_e32 v24, s64, v40
	v_lshlrev_b32_e32 v25, 1, v24
	v_add_u32_e32 v26, v25, v168
	s_waitcnt lgkmcnt(1)
	buffer_store_dwordx4 v[12:15], v26, s[20:23], 0 offen nt
	v_pk_fma_f32 v[6:7], v[6:7], v[232:233], v[244:245] op_sel:[0,1,0]
	v_pk_fma_f32 v[4:5], v[4:5], v[232:233], v[242:243] op_sel:[0,1,0]
	v_pk_fma_f32 v[12:13], v[18:19], v[232:233], v[236:237] op_sel:[0,1,0]
	v_pk_fma_f32 v[14:15], v[16:17], v[232:233], v[234:235] op_sel:[0,1,0]
	v_pk_fma_f32 v[16:17], v[10:11], v[232:233], v[240:241] op_sel:[0,1,0]
	v_pk_fma_f32 v[10:11], v[8:9], v[232:233], v[238:239] op_sel:[0,1,0]
	v_cvt_pk_f16_f32 v8, v14, v15
	v_cvt_pk_f16_f32 v9, v12, v13
	v_cvt_pk_f16_f32 v10, v10, v11
	v_cvt_pk_f16_f32 v11, v16, v17
	ds_write_b128 v173, v[8:11]
	v_pk_fma_f32 v[8:9], v[2:3], v[232:233], v[248:249] op_sel:[0,1,0]
	v_pk_fma_f32 v[2:3], v[0:1], v[232:233], v[246:247] op_sel:[0,1,0]
	v_cvt_pk_f16_f32 v0, v4, v5
	v_cvt_pk_f16_f32 v1, v6, v7
	v_cvt_pk_f16_f32 v2, v2, v3
	v_cvt_pk_f16_f32 v3, v8, v9
	ds_write_b128 v173, v[0:3] offset:64
	ds_read_b128 v[0:3], v174
	ds_read_b128 v[4:7], v174 offset:1152
	v_add_lshl_u32 v8, v24, s64, 1
	v_add_u32_e32 v25, v25, v169
	v_add_u32_e32 v9, v8, v168
	s_waitcnt lgkmcnt(4)
	buffer_store_dwordx4 v[20:23], v25, s[20:23], 0 offen nt
	s_waitcnt lgkmcnt(1)
	buffer_store_dwordx4 v[0:3], v9, s[20:23], 0 offen nt
	s_mov_b32 s67, s68
	s_mov_b32 s70, s69
	v_add_u32_e32 v0, v8, v169
	s_mov_b64 s[30:31], s[0:1]
	s_mov_b64 s[28:29], s[8:9]
	s_mov_b64 vcc, s[6:7]
	s_waitcnt lgkmcnt(0)
	buffer_store_dwordx4 v[4:7], v0, s[20:23], 0 offen nt
	s_cbranch_vccz .LBB7_12
	s_waitcnt vmcnt(0)
	s_cmpk_gt_u32 s36, 0xff
	s_cbranch_scc1 .LBB7_31
	s_barrier

	.amdhsa_kernel _Z6k_gemmIN2pg6EpiLinILi0EEELi768EEvNS0_4GemmET_
		.amdhsa_group_segment_fixed_size 0
		.amdhsa_private_segment_fixed_size 0
		.amdhsa_kernarg_size 320
		.amdhsa_user_sgpr_count 2
		.amdhsa_user_sgpr_dispatch_ptr 0
		.amdhsa_user_sgpr_queue_ptr 0
		.amdhsa_user_sgpr_kernarg_segment_ptr 1
		.amdhsa_user_sgpr_dispatch_id 0
		.amdhsa_user_sgpr_kernarg_preload_length 0
		.amdhsa_user_sgpr_kernarg_preload_offset 0
		.amdhsa_user_sgpr_private_segment_size 0
		.amdhsa_uses_dynamic_stack 0
		.amdhsa_enable_private_segment 0
		.amdhsa_system_sgpr_workgroup_id_x 1
		.amdhsa_system_sgpr_workgroup_id_y 0
		.amdhsa_system_sgpr_workgroup_id_z 0
		.amdhsa_system_sgpr_workgroup_info 0
		.amdhsa_system_vgpr_workitem_id 0
		.amdhsa_next_free_vgpr 256
		.amdhsa_next_free_sgpr 82
		.amdhsa_accum_offset 256
		.amdhsa_reserve_vcc 1
		.amdhsa_float_round_mode_32 0
		.amdhsa_float_round_mode_16_64 0
		.amdhsa_float_denorm_mode_32 3
		.amdhsa_float_denorm_mode_16_64 3
		.amdhsa_dx10_clamp 1
		.amdhsa_ieee_mode 1
		.amdhsa_fp16_overflow 0
		.amdhsa_tg_split 0
		.amdhsa_exception_fp_ieee_invalid_op 0
		.amdhsa_exception_fp_denorm_src 0
		.amdhsa_exception_fp_ieee_div_zero 0
		.amdhsa_exception_fp_ieee_overflow 0
		.amdhsa_exception_fp_ieee_underflow 0
		.amdhsa_exception_fp_ieee_inexact 0
		.amdhsa_exception_int_div_zero 0
	.end_amdhsa_kernel

.LBB8_26:
	v_add_u32_e32 v254, 0x18000, v228
	v_add_u32_e32 v255, 0x1c000, v228
	s_add_u32 s38, s38, 0x30080
	s_addc_u32 s39, s39, 0
	s_add_u32 s85, s40, 0x100
	v_mov_b32_e32 v0, 0
	s_addc_u32 s86, s41, 0
	s_mov_b32 s87, -2
	v_mov_b32_e32 v1, v0
	v_mov_b32_e32 v2, v0
	v_mov_b32_e32 v3, v0
	v_mov_b32_e32 v4, v0
	v_mov_b32_e32 v5, v0
	v_mov_b32_e32 v6, v0
	v_mov_b32_e32 v7, v0
	v_mov_b32_e32 v16, v0
	v_mov_b32_e32 v17, v0
	v_mov_b32_e32 v18, v0
	v_mov_b32_e32 v19, v0
	v_mov_b32_e32 v20, v0
	v_mov_b32_e32 v21, v0
	v_mov_b32_e32 v22, v0
	v_mov_b32_e32 v23, v0
	v_mov_b32_e32 v32, v0
	v_mov_b32_e32 v33, v0
	v_mov_b32_e32 v34, v0
	v_mov_b32_e32 v35, v0
	v_mov_b32_e32 v36, v0
	v_mov_b32_e32 v37, v0
	v_mov_b32_e32 v38, v0
	v_mov_b32_e32 v39, v0
	v_mov_b32_e32 v48, v0
	v_mov_b32_e32 v49, v0
	v_mov_b32_e32 v50, v0
	v_mov_b32_e32 v51, v0
	v_mov_b32_e32 v52, v0
	v_mov_b32_e32 v53, v0
	v_mov_b32_e32 v54, v0
	v_mov_b32_e32 v55, v0
	v_mov_b32_e32 v8, v0
	v_mov_b32_e32 v9, v0
	v_mov_b32_e32 v10, v0
	v_mov_b32_e32 v11, v0
	v_mov_b32_e32 v12, v0
	v_mov_b32_e32 v13, v0
	v_mov_b32_e32 v14, v0
	v_mov_b32_e32 v15, v0
	v_mov_b32_e32 v24, v0
	v_mov_b32_e32 v25, v0
	v_mov_b32_e32 v26, v0
	v_mov_b32_e32 v27, v0
	v_mov_b32_e32 v28, v0
	v_mov_b32_e32 v29, v0
	v_mov_b32_e32 v30, v0
	v_mov_b32_e32 v31, v0
	v_mov_b32_e32 v40, v0
	v_mov_b32_e32 v41, v0
	v_mov_b32_e32 v42, v0
	v_mov_b32_e32 v43, v0
	v_mov_b32_e32 v44, v0
	v_mov_b32_e32 v45, v0
	v_mov_b32_e32 v46, v0
	v_mov_b32_e32 v47, v0
	v_mov_b32_e32 v56, v0
	v_mov_b32_e32 v57, v0
	v_mov_b32_e32 v58, v0
	v_mov_b32_e32 v59, v0
	v_mov_b32_e32 v60, v0
	v_mov_b32_e32 v61, v0
	v_mov_b32_e32 v62, v0
	v_mov_b32_e32 v63, v0
	v_mov_b32_e32 v64, v0
	v_mov_b32_e32 v65, v0
	v_mov_b32_e32 v66, v0
	v_mov_b32_e32 v67, v0
	v_mov_b32_e32 v68, v0
	v_mov_b32_e32 v69, v0
	v_mov_b32_e32 v70, v0
	v_mov_b32_e32 v71, v0
	v_mov_b32_e32 v96, v0
	v_mov_b32_e32 v97, v0
	v_mov_b32_e32 v98, v0
	v_mov_b32_e32 v99, v0
	v_mov_b32_e32 v100, v0
	v_mov_b32_e32 v101, v0
	v_mov_b32_e32 v102, v0
	v_mov_b32_e32 v103, v0
	v_mov_b32_e32 v112, v0
	v_mov_b32_e32 v113, v0
	v_mov_b32_e32 v114, v0
	v_mov_b32_e32 v115, v0
	v_mov_b32_e32 v116, v0
	v_mov_b32_e32 v117, v0
	v_mov_b32_e32 v118, v0
	v_mov_b32_e32 v119, v0
	v_mov_b32_e32 v128, v0
	v_mov_b32_e32 v129, v0
	v_mov_b32_e32 v130, v0
	v_mov_b32_e32 v131, v0
	v_mov_b32_e32 v132, v0
	v_mov_b32_e32 v133, v0
	v_mov_b32_e32 v134, v0
	v_mov_b32_e32 v135, v0
	v_mov_b32_e32 v76, v0
	v_mov_b32_e32 v77, v0
	v_mov_b32_e32 v78, v0
	v_mov_b32_e32 v79, v0
	v_mov_b32_e32 v84, v0
	v_mov_b32_e32 v85, v0
	v_mov_b32_e32 v86, v0
	v_mov_b32_e32 v87, v0
	v_mov_b32_e32 v104, v0
	v_mov_b32_e32 v105, v0
	v_mov_b32_e32 v106, v0
	v_mov_b32_e32 v107, v0
	v_mov_b32_e32 v108, v0
	v_mov_b32_e32 v109, v0
	v_mov_b32_e32 v110, v0
	v_mov_b32_e32 v111, v0
	v_mov_b32_e32 v120, v0
	v_mov_b32_e32 v121, v0
	v_mov_b32_e32 v122, v0
	v_mov_b32_e32 v123, v0
	v_mov_b32_e32 v124, v0
	v_mov_b32_e32 v125, v0
	v_mov_b32_e32 v126, v0
	v_mov_b32_e32 v127, v0
	v_mov_b32_e32 v140, v0
	v_mov_b32_e32 v141, v0
	v_mov_b32_e32 v142, v0
	v_mov_b32_e32 v143, v0
	v_mov_b32_e32 v144, v0
	v_mov_b32_e32 v145, v0
	v_mov_b32_e32 v146, v0
	v_mov_b32_e32 v147, v0
	ds_read_b128 v[72:75], v231
	ds_read_b128 v[80:83], v231 offset:1024
	ds_read_b128 v[88:91], v231 offset:2048
	ds_read_b128 v[92:95], v231 offset:3072
.LBB8_27:
	s_add_u32 s40, s38, 0xfffd0080
	s_addc_u32 s41, s39, -1
	s_cmp_eq_u32 s87, 8
	s_cselect_b32 s43, s9, s41
	s_cselect_b32 s42, s8, s40
	s_cselect_b32 s41, s1, s86
	s_cselect_b32 s40, s0, s85
	s_add_i32 m0, s51, 0xc000
	ds_read_b128 v[136:139], v232
	ds_read_b128 v[148:151], v232 offset:1024
	ds_read_b128 v[152:155], v232 offset:2048
	ds_read_b128 v[156:159], v232 offset:3072
	ds_read_b128 v[160:163], v232 offset:4096
	ds_read_b128 v[164:167], v232 offset:5120
	ds_read_b128 v[168:171], v232 offset:6144
	ds_read_b128 v[172:175], v232 offset:7168
	global_load_lds_dwordx4 v184, s[38:39]
	s_add_i32 m0, s51, 0xe000
	s_nop 0
	global_load_lds_dwordx4 v186, s[38:39]
	s_waitcnt lgkmcnt(8)
	s_barrier
	s_waitcnt lgkmcnt(0)
	v_mfma_f32_16x16x32_f16 v[144:147], v[72:75], v[136:139], v[144:147]
	v_mfma_f32_16x16x32_f16 v[140:143], v[88:91], v[136:139], v[140:143]
	v_mfma_f32_16x16x32_f16 v[124:127], v[72:75], v[152:155], v[124:127]
	v_mfma_f32_16x16x32_f16 v[120:123], v[88:91], v[152:155], v[120:123]
	v_mfma_f32_16x16x32_f16 v[108:111], v[72:75], v[160:163], v[108:111]
	v_mfma_f32_16x16x32_f16 v[104:107], v[88:91], v[160:163], v[104:107]
	v_mfma_f32_16x16x32_f16 v[84:87], v[72:75], v[168:171], v[84:87]
	v_mfma_f32_16x16x32_f16 v[76:79], v[88:91], v[168:171], v[76:79]
	v_mfma_f32_16x16x32_f16 v[144:147], v[80:83], v[148:151], v[144:147]
	v_mfma_f32_16x16x32_f16 v[140:143], v[92:95], v[148:151], v[140:143]
	v_mfma_f32_16x16x32_f16 v[124:127], v[80:83], v[156:159], v[124:127]
	v_mfma_f32_16x16x32_f16 v[120:123], v[92:95], v[156:159], v[120:123]
	v_mfma_f32_16x16x32_f16 v[108:111], v[80:83], v[164:167], v[108:111]
	v_mfma_f32_16x16x32_f16 v[104:107], v[92:95], v[164:167], v[104:107]
	v_mfma_f32_16x16x32_f16 v[84:87], v[80:83], v[172:175], v[84:87]
	v_mfma_f32_16x16x32_f16 v[76:79], v[92:95], v[172:175], v[76:79]
	s_barrier
	s_add_i32 s88, s70, s50
	s_mov_b32 m0, s88
	ds_read_b128 v[190:193], v233
	ds_read_b128 v[194:197], v233 offset:1024
	ds_read_b128 v[198:201], v233 offset:2048
	ds_read_b128 v[202:205], v233 offset:3072
	global_load_lds_dwordx4 v178, s[40:41]
	s_add_i32 m0, s88, 0x2000
	s_add_u32 s92, s40, 0x80
	s_addc_u32 s93, s41, 0
	global_load_lds_dwordx4 v182, s[40:41]
	s_barrier
	s_waitcnt lgkmcnt(0)
	v_mfma_f32_16x16x32_f16 v[132:135], v[190:193], v[136:139], v[132:135]
	v_mfma_f32_16x16x32_f16 v[128:131], v[198:201], v[136:139], v[128:131]
	v_mfma_f32_16x16x32_f16 v[116:119], v[190:193], v[152:155], v[116:119]
	v_mfma_f32_16x16x32_f16 v[112:115], v[198:201], v[152:155], v[112:115]
	v_mfma_f32_16x16x32_f16 v[100:103], v[190:193], v[160:163], v[100:103]
	v_mfma_f32_16x16x32_f16 v[96:99], v[198:201], v[160:163], v[96:99]
	v_mfma_f32_16x16x32_f16 v[68:71], v[190:193], v[168:171], v[68:71]
	v_mfma_f32_16x16x32_f16 v[64:67], v[198:201], v[168:171], v[64:67]
	v_mfma_f32_16x16x32_f16 v[132:135], v[194:197], v[148:151], v[132:135]
	v_mfma_f32_16x16x32_f16 v[128:131], v[202:205], v[148:151], v[128:131]
	v_mfma_f32_16x16x32_f16 v[116:119], v[194:197], v[156:159], v[116:119]
	v_mfma_f32_16x16x32_f16 v[112:115], v[202:205], v[156:159], v[112:115]
	v_mfma_f32_16x16x32_f16 v[100:103], v[194:197], v[164:167], v[100:103]
	v_mfma_f32_16x16x32_f16 v[96:99], v[202:205], v[164:167], v[96:99]
	v_mfma_f32_16x16x32_f16 v[68:71], v[194:197], v[172:175], v[68:71]
	v_mfma_f32_16x16x32_f16 v[64:67], v[202:205], v[172:175], v[64:67]
	s_barrier
	s_mov_b32 m0, s51
	ds_read_b128 v[136:139], v232 offset:16384
	ds_read_b128 v[148:151], v232 offset:17408
	ds_read_b128 v[152:155], v232 offset:18432
	ds_read_b128 v[156:159], v232 offset:19456
	ds_read_b128 v[160:163], v232 offset:20480
	ds_read_b128 v[164:167], v232 offset:21504
	ds_read_b128 v[168:171], v232 offset:22528
	ds_read_b128 v[172:175], v232 offset:23552
	global_load_lds_dwordx4 v176, s[42:43]
	s_mov_b32 m0, s52
	s_add_u32 s94, s42, 0x80
	s_addc_u32 s95, s43, 0
	global_load_lds_dwordx4 v180, s[42:43]
	s_waitcnt vmcnt(10)
	s_barrier
	s_waitcnt lgkmcnt(0)
	v_mfma_f32_16x16x32_f16 v[60:63], v[72:75], v[136:139], v[60:63]
	v_mfma_f32_16x16x32_f16 v[56:59], v[88:91], v[136:139], v[56:59]
	v_mfma_f32_16x16x32_f16 v[44:47], v[72:75], v[152:155], v[44:47]
	v_mfma_f32_16x16x32_f16 v[40:43], v[88:91], v[152:155], v[40:43]
	v_mfma_f32_16x16x32_f16 v[28:31], v[72:75], v[160:163], v[28:31]
	v_mfma_f32_16x16x32_f16 v[24:27], v[88:91], v[160:163], v[24:27]
	v_mfma_f32_16x16x32_f16 v[12:15], v[72:75], v[168:171], v[12:15]
	v_mfma_f32_16x16x32_f16 v[8:11], v[88:91], v[168:171], v[8:11]
	v_mfma_f32_16x16x32_f16 v[60:63], v[80:83], v[148:151], v[60:63]
	v_mfma_f32_16x16x32_f16 v[56:59], v[92:95], v[148:151], v[56:59]
	v_mfma_f32_16x16x32_f16 v[44:47], v[80:83], v[156:159], v[44:47]
	v_mfma_f32_16x16x32_f16 v[40:43], v[92:95], v[156:159], v[40:43]
	v_mfma_f32_16x16x32_f16 v[28:31], v[80:83], v[164:167], v[28:31]
	v_mfma_f32_16x16x32_f16 v[24:27], v[92:95], v[164:167], v[24:27]
	v_mfma_f32_16x16x32_f16 v[12:15], v[80:83], v[172:175], v[12:15]
	v_mfma_f32_16x16x32_f16 v[8:11], v[92:95], v[172:175], v[8:11]
	s_barrier
	s_add_i32 s90, s71, s50
	s_mov_b32 m0, s90
	s_add_u32 s88, s40, 0xc000
	s_addc_u32 s89, s41, 0
	global_load_lds_dwordx4 v178, s[88:89]
	s_add_i32 m0, s90, 0x2000
	s_nop 0
	global_load_lds_dwordx4 v182, s[88:89]
	s_add_i32 s88, 0, 0x18000
	ds_read_b128 v[72:75], v254
	ds_read_b128 v[80:83], v254 offset:1024
	ds_read_b128 v[88:91], v254 offset:2048
	ds_read_b128 v[92:95], v254 offset:3072
	s_waitcnt vmcnt(6)
	s_barrier
	v_mfma_f32_16x16x32_f16 v[52:55], v[190:193], v[136:139], v[52:55]
	v_mfma_f32_16x16x32_f16 v[48:51], v[198:201], v[136:139], v[48:51]
	v_mfma_f32_16x16x32_f16 v[36:39], v[190:193], v[152:155], v[36:39]
	v_mfma_f32_16x16x32_f16 v[32:35], v[198:201], v[152:155], v[32:35]
	v_mfma_f32_16x16x32_f16 v[20:23], v[190:193], v[160:163], v[20:23]
	v_mfma_f32_16x16x32_f16 v[16:19], v[198:201], v[160:163], v[16:19]
	v_mfma_f32_16x16x32_f16 v[4:7], v[190:193], v[168:171], v[4:7]
	v_mfma_f32_16x16x32_f16 v[0:3], v[198:201], v[168:171], v[0:3]
	v_mfma_f32_16x16x32_f16 v[52:55], v[194:197], v[148:151], v[52:55]
	v_mfma_f32_16x16x32_f16 v[48:51], v[202:205], v[148:151], v[48:51]
	v_mfma_f32_16x16x32_f16 v[36:39], v[194:197], v[156:159], v[36:39]
	v_mfma_f32_16x16x32_f16 v[32:35], v[202:205], v[156:159], v[32:35]
	v_mfma_f32_16x16x32_f16 v[20:23], v[194:197], v[164:167], v[20:23]
	v_mfma_f32_16x16x32_f16 v[16:19], v[202:205], v[164:167], v[16:19]
	v_mfma_f32_16x16x32_f16 v[4:7], v[194:197], v[172:175], v[4:7]
	v_mfma_f32_16x16x32_f16 v[0:3], v[202:205], v[172:175], v[0:3]
	s_barrier
	s_add_u32 s42, s42, 0x30000
	s_addc_u32 s43, s43, 0
	s_mov_b32 m0, s53
	ds_read_b128 v[136:139], v232 offset:32768
	ds_read_b128 v[148:151], v232 offset:33792
	ds_read_b128 v[152:155], v232 offset:34816
	ds_read_b128 v[156:159], v232 offset:35840
	ds_read_b128 v[160:163], v232 offset:36864
	ds_read_b128 v[164:167], v232 offset:37888
	ds_read_b128 v[168:171], v232 offset:38912
	ds_read_b128 v[172:175], v232 offset:39936
	global_load_lds_dwordx4 v176, s[42:43]
	s_mov_b32 m0, s54
	s_nop 0
	global_load_lds_dwordx4 v180, s[42:43]
	s_waitcnt lgkmcnt(8)
	s_barrier
	s_waitcnt lgkmcnt(0)
	v_mfma_f32_16x16x32_f16 v[144:147], v[72:75], v[136:139], v[144:147]
	v_mfma_f32_16x16x32_f16 v[140:143], v[88:91], v[136:139], v[140:143]
	v_mfma_f32_16x16x32_f16 v[124:127], v[72:75], v[152:155], v[124:127]
	v_mfma_f32_16x16x32_f16 v[120:123], v[88:91], v[152:155], v[120:123]
	v_mfma_f32_16x16x32_f16 v[108:111], v[72:75], v[160:163], v[108:111]
	v_mfma_f32_16x16x32_f16 v[104:107], v[88:91], v[160:163], v[104:107]
	v_mfma_f32_16x16x32_f16 v[84:87], v[72:75], v[168:171], v[84:87]
	v_mfma_f32_16x16x32_f16 v[76:79], v[88:91], v[168:171], v[76:79]
	v_mfma_f32_16x16x32_f16 v[144:147], v[80:83], v[148:151], v[144:147]
	v_mfma_f32_16x16x32_f16 v[140:143], v[92:95], v[148:151], v[140:143]
	v_mfma_f32_16x16x32_f16 v[124:127], v[80:83], v[156:159], v[124:127]
	v_mfma_f32_16x16x32_f16 v[120:123], v[92:95], v[156:159], v[120:123]
	v_mfma_f32_16x16x32_f16 v[108:111], v[80:83], v[164:167], v[108:111]
	v_mfma_f32_16x16x32_f16 v[104:107], v[92:95], v[164:167], v[104:107]
	v_mfma_f32_16x16x32_f16 v[84:87], v[80:83], v[172:175], v[84:87]
	v_mfma_f32_16x16x32_f16 v[76:79], v[92:95], v[172:175], v[76:79]
	s_barrier
	s_add_i32 s42, 0, 0x1c000
	s_add_i32 s43, s88, s50
	s_mov_b32 m0, s43
	ds_read_b128 v[190:193], v255
	ds_read_b128 v[194:197], v255 offset:1024
	ds_read_b128 v[198:201], v255 offset:2048
	ds_read_b128 v[202:205], v255 offset:3072
	global_load_lds_dwordx4 v178, s[92:93]
	s_add_i32 m0, s43, 0x2000
	s_nop 0
	global_load_lds_dwordx4 v182, s[92:93]
	s_barrier
	s_waitcnt lgkmcnt(0)
	v_mfma_f32_16x16x32_f16 v[132:135], v[190:193], v[136:139], v[132:135]
	v_mfma_f32_16x16x32_f16 v[128:131], v[198:201], v[136:139], v[128:131]
	v_mfma_f32_16x16x32_f16 v[116:119], v[190:193], v[152:155], v[116:119]
	v_mfma_f32_16x16x32_f16 v[112:115], v[198:201], v[152:155], v[112:115]
	v_mfma_f32_16x16x32_f16 v[100:103], v[190:193], v[160:163], v[100:103]
	v_mfma_f32_16x16x32_f16 v[96:99], v[198:201], v[160:163], v[96:99]
	v_mfma_f32_16x16x32_f16 v[68:71], v[190:193], v[168:171], v[68:71]
	v_mfma_f32_16x16x32_f16 v[64:67], v[198:201], v[168:171], v[64:67]
	v_mfma_f32_16x16x32_f16 v[132:135], v[194:197], v[148:151], v[132:135]
	v_mfma_f32_16x16x32_f16 v[128:131], v[202:205], v[148:151], v[128:131]
	v_mfma_f32_16x16x32_f16 v[116:119], v[194:197], v[156:159], v[116:119]
	v_mfma_f32_16x16x32_f16 v[112:115], v[202:205], v[156:159], v[112:115]
	v_mfma_f32_16x16x32_f16 v[100:103], v[194:197], v[164:167], v[100:103]
	v_mfma_f32_16x16x32_f16 v[96:99], v[202:205], v[164:167], v[96:99]
	v_mfma_f32_16x16x32_f16 v[68:71], v[194:197], v[172:175], v[68:71]
	v_mfma_f32_16x16x32_f16 v[64:67], v[202:205], v[172:175], v[64:67]
	s_barrier
	s_mov_b32 m0, s59
	ds_read_b128 v[136:139], v232 offset:49152
	ds_read_b128 v[148:151], v232 offset:50176
	ds_read_b128 v[152:155], v232 offset:51200
	ds_read_b128 v[156:159], v232 offset:52224
	ds_read_b128 v[160:163], v232 offset:53248
	ds_read_b128 v[164:167], v232 offset:54272
	ds_read_b128 v[168:171], v232 offset:55296
	ds_read_b128 v[172:175], v232 offset:56320
	global_load_lds_dwordx4 v176, s[94:95]
	s_mov_b32 m0, s60
	s_nop 0
	global_load_lds_dwordx4 v180, s[94:95]
	s_waitcnt vmcnt(10)
	s_barrier
	s_waitcnt lgkmcnt(0)
	v_mfma_f32_16x16x32_f16 v[60:63], v[72:75], v[136:139], v[60:63]
	v_mfma_f32_16x16x32_f16 v[56:59], v[88:91], v[136:139], v[56:59]
	v_mfma_f32_16x16x32_f16 v[44:47], v[72:75], v[152:155], v[44:47]
	v_mfma_f32_16x16x32_f16 v[40:43], v[88:91], v[152:155], v[40:43]
	v_mfma_f32_16x16x32_f16 v[28:31], v[72:75], v[160:163], v[28:31]
	v_mfma_f32_16x16x32_f16 v[24:27], v[88:91], v[160:163], v[24:27]
	v_mfma_f32_16x16x32_f16 v[12:15], v[72:75], v[168:171], v[12:15]
	v_mfma_f32_16x16x32_f16 v[8:11], v[88:91], v[168:171], v[8:11]
	v_mfma_f32_16x16x32_f16 v[60:63], v[80:83], v[148:151], v[60:63]
	v_mfma_f32_16x16x32_f16 v[56:59], v[92:95], v[148:151], v[56:59]
	v_mfma_f32_16x16x32_f16 v[44:47], v[80:83], v[156:159], v[44:47]
	v_mfma_f32_16x16x32_f16 v[40:43], v[92:95], v[156:159], v[40:43]
	v_mfma_f32_16x16x32_f16 v[28:31], v[80:83], v[164:167], v[28:31]
	v_mfma_f32_16x16x32_f16 v[24:27], v[92:95], v[164:167], v[24:27]
	v_mfma_f32_16x16x32_f16 v[12:15], v[80:83], v[172:175], v[12:15]
	v_mfma_f32_16x16x32_f16 v[8:11], v[92:95], v[172:175], v[8:11]
	s_barrier
	s_add_i32 s42, s42, s50
	s_mov_b32 m0, s42
	s_add_u32 s40, s40, 0xc080
	s_addc_u32 s41, s41, 0
	global_load_lds_dwordx4 v178, s[40:41]
	s_add_i32 m0, s42, 0x2000
	s_nop 0
	global_load_lds_dwordx4 v182, s[40:41]
	ds_read_b128 v[72:75], v231
	ds_read_b128 v[80:83], v231 offset:1024
	ds_read_b128 v[88:91], v231 offset:2048
	ds_read_b128 v[92:95], v231 offset:3072
	s_waitcnt vmcnt(6)
	s_barrier
	v_mfma_f32_16x16x32_f16 v[52:55], v[190:193], v[136:139], v[52:55]
	v_mfma_f32_16x16x32_f16 v[48:51], v[198:201], v[136:139], v[48:51]
	v_mfma_f32_16x16x32_f16 v[36:39], v[190:193], v[152:155], v[36:39]
	v_mfma_f32_16x16x32_f16 v[32:35], v[198:201], v[152:155], v[32:35]
	v_mfma_f32_16x16x32_f16 v[20:23], v[190:193], v[160:163], v[20:23]
	v_mfma_f32_16x16x32_f16 v[16:19], v[198:201], v[160:163], v[16:19]
	v_mfma_f32_16x16x32_f16 v[4:7], v[190:193], v[168:171], v[4:7]
	v_mfma_f32_16x16x32_f16 v[0:3], v[198:201], v[168:171], v[0:3]
	v_mfma_f32_16x16x32_f16 v[52:55], v[194:197], v[148:151], v[52:55]
	v_mfma_f32_16x16x32_f16 v[48:51], v[202:205], v[148:151], v[48:51]
	v_mfma_f32_16x16x32_f16 v[36:39], v[194:197], v[156:159], v[36:39]
	v_mfma_f32_16x16x32_f16 v[32:35], v[202:205], v[156:159], v[32:35]
	v_mfma_f32_16x16x32_f16 v[20:23], v[194:197], v[164:167], v[20:23]
	v_mfma_f32_16x16x32_f16 v[16:19], v[202:205], v[164:167], v[16:19]
	v_mfma_f32_16x16x32_f16 v[4:7], v[194:197], v[172:175], v[4:7]
	v_mfma_f32_16x16x32_f16 v[0:3], v[202:205], v[172:175], v[0:3]
	s_barrier
	s_add_i32 s87, s87, 2
	s_add_u32 s38, s38, 0x100
	s_addc_u32 s39, s39, 0
	s_add_u32 s85, s85, 0x100
	s_addc_u32 s86, s86, 0
	s_cmp_gt_u32 s87, 9
	s_cbranch_scc0 .LBB8_27
	s_lshl_b32 s92, s84, 8
	s_add_i32 s92, s92, s58
	s_lshl_b32 s93, s83, 8
	s_or_b32 s93, s93, s61
	v_lshlrev_b32_e32 v237, 2, v226
	s_lshl_b32 s96, s93, 2
	s_add_u32 s94, s16, s96
	s_addc_u32 s95, s17, 0
	global_load_dwordx4 v[72:75], v237, s[94:95] offset:0
	global_load_dwordx4 v[80:83], v237, s[94:95] offset:16
	global_load_dwordx4 v[88:91], v237, s[94:95] offset:128
	global_load_dwordx4 v[92:95], v237, s[94:95] offset:144
	s_add_u32 s94, s18, s96
	s_addc_u32 s95, s19, 0
	global_load_dwordx4 v[136:139], v237, s[94:95] offset:0
	global_load_dwordx4 v[148:151], v237, s[94:95] offset:16
	global_load_dwordx4 v[152:155], v237, s[94:95] offset:128
	global_load_dwordx4 v[156:159], v237, s[94:95] offset:144
	s_add_u32 s94, s14, s96
	s_addc_u32 s95, s15, 0
	global_load_dwordx4 v[160:163], v237, s[94:95] offset:0
	global_load_dwordx4 v[164:167], v237, s[94:95] offset:16
	global_load_dwordx4 v[168:171], v237, s[94:95] offset:128
	global_load_dwordx4 v[172:175], v237, s[94:95] offset:144
	v_lshlrev_b32_e32 v190, 3, v227
	s_lshl_b32 s96, s92, 3
	s_add_u32 s94, s12, s96
	s_addc_u32 s95, s13, 0
	global_load_dwordx2 v[238:239], v190, s[94:95] offset:0
	global_load_dwordx2 v[192:193], v190, s[94:95] offset:128
	global_load_dwordx2 v[194:195], v190, s[94:95] offset:256
	global_load_dwordx2 v[196:197], v190, s[94:95] offset:384
	global_load_dwordx2 v[198:199], v190, s[94:95] offset:1024
	global_load_dwordx2 v[200:201], v190, s[94:95] offset:1152
	global_load_dwordx2 v[202:203], v190, s[94:95] offset:1280
	global_load_dwordx2 v[204:205], v190, s[94:95] offset:1408
	v_mul_u32_u24_e32 v191, 0x600, v227
	v_lshl_add_u32 v191, v226, 1, v191
	s_mul_i32 s96, s92, 0x600
	s_lshl_b32 s97, s93, 1
	s_add_u32 s96, s96, s97
	s_add_u32 s98, s10, s96
	s_addc_u32 s99, s11, 0
	s_add_u32 s94, s98, 0x0
	s_addc_u32 s95, s99, 0
	global_load_dwordx4 v[208:211], v191, s[94:95] offset:0 nt
	global_load_dwordx4 v[212:215], v191, s[94:95] offset:64 nt
	s_add_u32 s94, s98, 0x6000
	s_addc_u32 s95, s99, 0
	global_load_dwordx4 v[216:219], v191, s[94:95] offset:0 nt
	global_load_dwordx4 v[220:223], v191, s[94:95] offset:64 nt
	v_add_u32_e32 v224, s92, v229
	v_mul_u32_u24_e32 v224, 0x600, v224
	s_lshl_b32 s97, s93, 1
	v_add3_u32 v224, v224, v230, s97
	s_lshl_b32 s96, s83, 2
	s_lshr_b32 s97, s61, 6
	s_add_u32 s96, s96, s97
	s_lshl_b32 s96, s96, 19
	s_lshl_b32 s97, s92, 3
	s_add_u32 s96, s96, s97
	s_add_u32 s100, s28, s96
	s_addc_u32 s101, s29, 0
	s_waitcnt vmcnt(19)
	v_pk_add_f32 v[72:73], v[72:73], v[136:137]
	v_pk_add_f32 v[74:75], v[74:75], v[138:139]
	s_waitcnt vmcnt(18)
	v_pk_add_f32 v[80:81], v[80:81], v[148:149]
	v_pk_add_f32 v[82:83], v[82:83], v[150:151]
	s_waitcnt vmcnt(17)
	v_pk_add_f32 v[88:89], v[88:89], v[152:153]
	v_pk_add_f32 v[90:91], v[90:91], v[154:155]
	s_waitcnt vmcnt(16)
	v_pk_add_f32 v[92:93], v[92:93], v[156:157]
	v_pk_add_f32 v[94:95], v[94:95], v[158:159]
	v_pk_add_f32 v[144:145], v[144:145], v[72:73]
	v_pk_add_f32 v[146:147], v[146:147], v[74:75]
	v_pk_add_f32 v[124:125], v[124:125], v[72:73]
	v_pk_add_f32 v[126:127], v[126:127], v[74:75]
	v_pk_add_f32 v[108:109], v[108:109], v[72:73]
	v_pk_add_f32 v[110:111], v[110:111], v[74:75]
	v_pk_add_f32 v[84:85], v[84:85], v[72:73]
	v_pk_add_f32 v[86:87], v[86:87], v[74:75]
	v_pk_add_f32 v[60:61], v[60:61], v[72:73]
	v_pk_add_f32 v[62:63], v[62:63], v[74:75]
	v_pk_add_f32 v[44:45], v[44:45], v[72:73]
	v_pk_add_f32 v[46:47], v[46:47], v[74:75]
	v_pk_add_f32 v[28:29], v[28:29], v[72:73]
	v_pk_add_f32 v[30:31], v[30:31], v[74:75]
	v_pk_add_f32 v[12:13], v[12:13], v[72:73]
	v_pk_add_f32 v[14:15], v[14:15], v[74:75]
	v_pk_add_f32 v[140:141], v[140:141], v[80:81]
	v_pk_add_f32 v[142:143], v[142:143], v[82:83]
	v_pk_add_f32 v[120:121], v[120:121], v[80:81]
	v_pk_add_f32 v[122:123], v[122:123], v[82:83]
	v_pk_add_f32 v[104:105], v[104:105], v[80:81]
	v_pk_add_f32 v[106:107], v[106:107], v[82:83]
	v_pk_add_f32 v[76:77], v[76:77], v[80:81]
	v_pk_add_f32 v[78:79], v[78:79], v[82:83]
	v_pk_add_f32 v[56:57], v[56:57], v[80:81]
	v_pk_add_f32 v[58:59], v[58:59], v[82:83]
	v_pk_add_f32 v[40:41], v[40:41], v[80:81]
	v_pk_add_f32 v[42:43], v[42:43], v[82:83]
	v_pk_add_f32 v[24:25], v[24:25], v[80:81]
	v_pk_add_f32 v[26:27], v[26:27], v[82:83]
	v_pk_add_f32 v[8:9], v[8:9], v[80:81]
	v_pk_add_f32 v[10:11], v[10:11], v[82:83]
	v_pk_add_f32 v[132:133], v[132:133], v[88:89]
	v_pk_add_f32 v[134:135], v[134:135], v[90:91]
	v_pk_add_f32 v[116:117], v[116:117], v[88:89]
	v_pk_add_f32 v[118:119], v[118:119], v[90:91]
	v_pk_add_f32 v[100:101], v[100:101], v[88:89]
	v_pk_add_f32 v[102:103], v[102:103], v[90:91]
	v_pk_add_f32 v[68:69], v[68:69], v[88:89]
	v_pk_add_f32 v[70:71], v[70:71], v[90:91]
	v_pk_add_f32 v[52:53], v[52:53], v[88:89]
	v_pk_add_f32 v[54:55], v[54:55], v[90:91]
	v_pk_add_f32 v[36:37], v[36:37], v[88:89]
	v_pk_add_f32 v[38:39], v[38:39], v[90:91]
	v_pk_add_f32 v[20:21], v[20:21], v[88:89]
	v_pk_add_f32 v[22:23], v[22:23], v[90:91]
	v_pk_add_f32 v[4:5], v[4:5], v[88:89]
	v_pk_add_f32 v[6:7], v[6:7], v[90:91]
	v_pk_add_f32 v[128:129], v[128:129], v[92:93]
	v_pk_add_f32 v[130:131], v[130:131], v[94:95]
	v_pk_add_f32 v[112:113], v[112:113], v[92:93]
	v_pk_add_f32 v[114:115], v[114:115], v[94:95]
	v_pk_add_f32 v[96:97], v[96:97], v[92:93]
	v_pk_add_f32 v[98:99], v[98:99], v[94:95]
	v_pk_add_f32 v[64:65], v[64:65], v[92:93]
	v_pk_add_f32 v[66:67], v[66:67], v[94:95]
	v_pk_add_f32 v[48:49], v[48:49], v[92:93]
	v_pk_add_f32 v[50:51], v[50:51], v[94:95]
	v_pk_add_f32 v[32:33], v[32:33], v[92:93]
	v_pk_add_f32 v[34:35], v[34:35], v[94:95]
	v_pk_add_f32 v[16:17], v[16:17], v[92:93]
	v_pk_add_f32 v[18:19], v[18:19], v[94:95]
	v_pk_add_f32 v[0:1], v[0:1], v[92:93]
	v_pk_add_f32 v[2:3], v[2:3], v[94:95]
	s_add_u32 s94, s98, 0xc000
	s_addc_u32 s95, s99, 0
	global_load_dwordx4 v[240:243], v191, s[94:95] offset:0 nt
	global_load_dwordx4 v[244:247], v191, s[94:95] offset:64 nt
	s_add_u32 s94, s98, 0x12000
	s_addc_u32 s95, s99, 0
	global_load_dwordx4 v[248:251], v191, s[94:95] offset:0 nt
	global_load_dwordx4 v[252:255], v191, s[94:95] offset:64 nt
	s_add_u32 s94, s98, 0x30000
	s_addc_u32 s95, s99, 0
	global_load_dwordx4 v[136:139], v191, s[94:95] offset:0 nt
	global_load_dwordx4 v[148:151], v191, s[94:95] offset:64 nt
	s_add_u32 s94, s98, 0x36000
	s_addc_u32 s95, s99, 0
	global_load_dwordx4 v[152:155], v191, s[94:95] offset:0 nt
	global_load_dwordx4 v[156:159], v191, s[94:95] offset:64 nt
	s_waitcnt vmcnt(19)
	s_waitcnt vmcnt(11)
	v_cvt_f32_f16_e32 v72, v208
	v_cvt_f32_f16_sdwa v73, v208 dst_sel:DWORD dst_unused:UNUSED_PAD src0_sel:WORD_1
	v_cvt_f32_f16_e32 v74, v209
	v_cvt_f32_f16_sdwa v75, v209 dst_sel:DWORD dst_unused:UNUSED_PAD src0_sel:WORD_1
	v_cvt_f32_f16_e32 v80, v210
	v_cvt_f32_f16_sdwa v81, v210 dst_sel:DWORD dst_unused:UNUSED_PAD src0_sel:WORD_1
	v_cvt_f32_f16_e32 v82, v211
	v_cvt_f32_f16_sdwa v83, v211 dst_sel:DWORD dst_unused:UNUSED_PAD src0_sel:WORD_1
	v_sub_f32_e32 v72, v72, v238
	v_sub_f32_e32 v73, v73, v238
	v_sub_f32_e32 v74, v74, v238
	v_sub_f32_e32 v75, v75, v238
	v_sub_f32_e32 v80, v80, v238
	v_sub_f32_e32 v81, v81, v238
	v_sub_f32_e32 v82, v82, v238
	v_sub_f32_e32 v83, v83, v238
	v_pk_mul_f32 v[72:73], v[238:239], v[72:73] op_sel:[1,0]
	v_pk_mul_f32 v[74:75], v[238:239], v[74:75] op_sel:[1,0]
	v_pk_mul_f32 v[80:81], v[238:239], v[80:81] op_sel:[1,0]
	v_pk_mul_f32 v[82:83], v[238:239], v[82:83] op_sel:[1,0]
	v_pk_fma_f32 v[144:145], v[72:73], v[160:161], v[144:145]
	v_pk_fma_f32 v[146:147], v[74:75], v[162:163], v[146:147]
	v_pk_fma_f32 v[140:141], v[80:81], v[164:165], v[140:141]
	v_pk_fma_f32 v[142:143], v[82:83], v[166:167], v[142:143]
	v_cvt_pk_f16_f32 v144, v144, v145
	v_cvt_pk_f16_f32 v145, v146, v147
	v_cvt_pk_f16_f32 v146, v140, v141
	v_cvt_pk_f16_f32 v147, v142, v143
	ds_write_b128 v235, v[144:147]
	v_fma_mix_f32 v206, v144, 1.0, 0 op_sel_hi:[1,0,0]
	v_fma_mix_f32 v207, v144, v144, 0 op_sel_hi:[1,1,0]
	v_fma_mix_f32 v206, v144, 1.0, v206 op_sel:[1,0,0] op_sel_hi:[1,0,0]
	v_fma_mix_f32 v207, v144, v144, v207 op_sel:[1,1,0] op_sel_hi:[1,1,0]
	v_fma_mix_f32 v206, v145, 1.0, v206 op_sel_hi:[1,0,0]
	v_fma_mix_f32 v207, v145, v145, v207 op_sel_hi:[1,1,0]
	v_fma_mix_f32 v206, v145, 1.0, v206 op_sel:[1,0,0] op_sel_hi:[1,0,0]
	v_fma_mix_f32 v207, v145, v145, v207 op_sel:[1,1,0] op_sel_hi:[1,1,0]
	v_fma_mix_f32 v206, v146, 1.0, v206 op_sel_hi:[1,0,0]
	v_fma_mix_f32 v207, v146, v146, v207 op_sel_hi:[1,1,0]
	v_fma_mix_f32 v206, v146, 1.0, v206 op_sel:[1,0,0] op_sel_hi:[1,0,0]
	v_fma_mix_f32 v207, v146, v146, v207 op_sel:[1,1,0] op_sel_hi:[1,1,0]
	v_fma_mix_f32 v206, v147, 1.0, v206 op_sel_hi:[1,0,0]
	v_fma_mix_f32 v207, v147, v147, v207 op_sel_hi:[1,1,0]
	v_fma_mix_f32 v206, v147, 1.0, v206 op_sel:[1,0,0] op_sel_hi:[1,0,0]
	v_fma_mix_f32 v207, v147, v147, v207 op_sel:[1,1,0] op_sel_hi:[1,1,0]
	s_waitcnt vmcnt(10)
	v_cvt_f32_f16_e32 v72, v212
	v_cvt_f32_f16_sdwa v73, v212 dst_sel:DWORD dst_unused:UNUSED_PAD src0_sel:WORD_1
	v_cvt_f32_f16_e32 v74, v213
	v_cvt_f32_f16_sdwa v75, v213 dst_sel:DWORD dst_unused:UNUSED_PAD src0_sel:WORD_1
	v_cvt_f32_f16_e32 v80, v214
	v_cvt_f32_f16_sdwa v81, v214 dst_sel:DWORD dst_unused:UNUSED_PAD src0_sel:WORD_1
	v_cvt_f32_f16_e32 v82, v215
	v_cvt_f32_f16_sdwa v83, v215 dst_sel:DWORD dst_unused:UNUSED_PAD src0_sel:WORD_1
	v_sub_f32_e32 v72, v72, v238
	v_sub_f32_e32 v73, v73, v238
	v_sub_f32_e32 v74, v74, v238
	v_sub_f32_e32 v75, v75, v238
	v_sub_f32_e32 v80, v80, v238
	v_sub_f32_e32 v81, v81, v238
	v_sub_f32_e32 v82, v82, v238
	v_sub_f32_e32 v83, v83, v238
	v_pk_mul_f32 v[72:73], v[238:239], v[72:73] op_sel:[1,0]
	v_pk_mul_f32 v[74:75], v[238:239], v[74:75] op_sel:[1,0]
	v_pk_mul_f32 v[80:81], v[238:239], v[80:81] op_sel:[1,0]
	v_pk_mul_f32 v[82:83], v[238:239], v[82:83] op_sel:[1,0]
	v_pk_fma_f32 v[132:133], v[72:73], v[168:169], v[132:133]
	v_pk_fma_f32 v[134:135], v[74:75], v[170:171], v[134:135]
	v_pk_fma_f32 v[128:129], v[80:81], v[172:173], v[128:129]
	v_pk_fma_f32 v[130:131], v[82:83], v[174:175], v[130:131]
	v_cvt_pk_f16_f32 v132, v132, v133
	v_cvt_pk_f16_f32 v133, v134, v135
	v_cvt_pk_f16_f32 v134, v128, v129
	v_cvt_pk_f16_f32 v135, v130, v131
	ds_write_b128 v235, v[132:135] offset:64
	v_fma_mix_f32 v206, v132, 1.0, v206 op_sel_hi:[1,0,0]
	v_fma_mix_f32 v207, v132, v132, v207 op_sel_hi:[1,1,0]
	v_fma_mix_f32 v206, v132, 1.0, v206 op_sel:[1,0,0] op_sel_hi:[1,0,0]
	v_fma_mix_f32 v207, v132, v132, v207 op_sel:[1,1,0] op_sel_hi:[1,1,0]
	v_fma_mix_f32 v206, v133, 1.0, v206 op_sel_hi:[1,0,0]
	v_fma_mix_f32 v207, v133, v133, v207 op_sel_hi:[1,1,0]
	v_fma_mix_f32 v206, v133, 1.0, v206 op_sel:[1,0,0] op_sel_hi:[1,0,0]
	v_fma_mix_f32 v207, v133, v133, v207 op_sel:[1,1,0] op_sel_hi:[1,1,0]
	v_fma_mix_f32 v206, v134, 1.0, v206 op_sel_hi:[1,0,0]
	v_fma_mix_f32 v207, v134, v134, v207 op_sel_hi:[1,1,0]
	v_fma_mix_f32 v206, v134, 1.0, v206 op_sel:[1,0,0] op_sel_hi:[1,0,0]
	v_fma_mix_f32 v207, v134, v134, v207 op_sel:[1,1,0] op_sel_hi:[1,1,0]
	v_fma_mix_f32 v206, v135, 1.0, v206 op_sel_hi:[1,0,0]
	v_fma_mix_f32 v207, v135, v135, v207 op_sel_hi:[1,1,0]
	v_fma_mix_f32 v206, v135, 1.0, v206 op_sel:[1,0,0] op_sel_hi:[1,0,0]
	v_fma_mix_f32 v207, v135, v135, v207 op_sel:[1,1,0] op_sel_hi:[1,1,0]
	ds_read_b128 v[88:91], v236
	ds_read_b128 v[92:95], v236 offset:1152
	s_waitcnt vmcnt(9)
	v_cvt_f32_f16_e32 v72, v216
	v_cvt_f32_f16_sdwa v73, v216 dst_sel:DWORD dst_unused:UNUSED_PAD src0_sel:WORD_1
	v_cvt_f32_f16_e32 v74, v217
	v_cvt_f32_f16_sdwa v75, v217 dst_sel:DWORD dst_unused:UNUSED_PAD src0_sel:WORD_1
	v_cvt_f32_f16_e32 v80, v218
	v_cvt_f32_f16_sdwa v81, v218 dst_sel:DWORD dst_unused:UNUSED_PAD src0_sel:WORD_1
	v_cvt_f32_f16_e32 v82, v219
	v_cvt_f32_f16_sdwa v83, v219 dst_sel:DWORD dst_unused:UNUSED_PAD src0_sel:WORD_1
	v_sub_f32_e32 v72, v72, v192
	v_sub_f32_e32 v73, v73, v192
	v_sub_f32_e32 v74, v74, v192
	v_sub_f32_e32 v75, v75, v192
	v_sub_f32_e32 v80, v80, v192
	v_sub_f32_e32 v81, v81, v192
	v_sub_f32_e32 v82, v82, v192
	v_sub_f32_e32 v83, v83, v192
	v_pk_mul_f32 v[72:73], v[192:193], v[72:73] op_sel:[1,0]
	v_pk_mul_f32 v[74:75], v[192:193], v[74:75] op_sel:[1,0]
	v_pk_mul_f32 v[80:81], v[192:193], v[80:81] op_sel:[1,0]
	v_pk_mul_f32 v[82:83], v[192:193], v[82:83] op_sel:[1,0]
	v_pk_fma_f32 v[124:125], v[72:73], v[160:161], v[124:125]
	v_pk_fma_f32 v[126:127], v[74:75], v[162:163], v[126:127]
	v_pk_fma_f32 v[120:121], v[80:81], v[164:165], v[120:121]
	v_pk_fma_f32 v[122:123], v[82:83], v[166:167], v[122:123]
	v_cvt_pk_f16_f32 v124, v124, v125
	v_cvt_pk_f16_f32 v125, v126, v127
	v_cvt_pk_f16_f32 v126, v120, v121
	v_cvt_pk_f16_f32 v127, v122, v123
	s_waitcnt lgkmcnt(0)
	buffer_store_dwordx4 v[88:91], v224, s[24:27], 0 offen nt
	v_add_u32_e32 v82, 0x3000, v224
	buffer_store_dwordx4 v[92:95], v82, s[24:27], 0 offen nt
	ds_write_b128 v235, v[124:127]
	v_fma_mix_f32 v140, v124, 1.0, 0 op_sel_hi:[1,0,0]
	v_fma_mix_f32 v141, v124, v124, 0 op_sel_hi:[1,1,0]
	v_fma_mix_f32 v140, v124, 1.0, v140 op_sel:[1,0,0] op_sel_hi:[1,0,0]
	v_fma_mix_f32 v141, v124, v124, v141 op_sel:[1,1,0] op_sel_hi:[1,1,0]
	v_fma_mix_f32 v140, v125, 1.0, v140 op_sel_hi:[1,0,0]
	v_fma_mix_f32 v141, v125, v125, v141 op_sel_hi:[1,1,0]
	v_fma_mix_f32 v140, v125, 1.0, v140 op_sel:[1,0,0] op_sel_hi:[1,0,0]
	v_fma_mix_f32 v141, v125, v125, v141 op_sel:[1,1,0] op_sel_hi:[1,1,0]
	v_fma_mix_f32 v140, v126, 1.0, v140 op_sel_hi:[1,0,0]
	v_fma_mix_f32 v141, v126, v126, v141 op_sel_hi:[1,1,0]
	v_fma_mix_f32 v140, v126, 1.0, v140 op_sel:[1,0,0] op_sel_hi:[1,0,0]
	v_fma_mix_f32 v141, v126, v126, v141 op_sel:[1,1,0] op_sel_hi:[1,1,0]
	v_fma_mix_f32 v140, v127, 1.0, v140 op_sel_hi:[1,0,0]
	v_fma_mix_f32 v141, v127, v127, v141 op_sel_hi:[1,1,0]
	v_fma_mix_f32 v140, v127, 1.0, v140 op_sel:[1,0,0] op_sel_hi:[1,0,0]
	v_fma_mix_f32 v141, v127, v127, v141 op_sel:[1,1,0] op_sel_hi:[1,1,0]
	s_waitcnt vmcnt(10)
	v_cvt_f32_f16_e32 v72, v220
	v_cvt_f32_f16_sdwa v73, v220 dst_sel:DWORD dst_unused:UNUSED_PAD src0_sel:WORD_1
	v_cvt_f32_f16_e32 v74, v221
	v_cvt_f32_f16_sdwa v75, v221 dst_sel:DWORD dst_unused:UNUSED_PAD src0_sel:WORD_1
	v_cvt_f32_f16_e32 v80, v222
	v_cvt_f32_f16_sdwa v81, v222 dst_sel:DWORD dst_unused:UNUSED_PAD src0_sel:WORD_1
	v_cvt_f32_f16_e32 v82, v223
	v_cvt_f32_f16_sdwa v83, v223 dst_sel:DWORD dst_unused:UNUSED_PAD src0_sel:WORD_1
	v_sub_f32_e32 v72, v72, v192
	v_sub_f32_e32 v73, v73, v192
	v_sub_f32_e32 v74, v74, v192
	v_sub_f32_e32 v75, v75, v192
	v_sub_f32_e32 v80, v80, v192
	v_sub_f32_e32 v81, v81, v192
	v_sub_f32_e32 v82, v82, v192
	v_sub_f32_e32 v83, v83, v192
	v_pk_mul_f32 v[72:73], v[192:193], v[72:73] op_sel:[1,0]
	v_pk_mul_f32 v[74:75], v[192:193], v[74:75] op_sel:[1,0]
	v_pk_mul_f32 v[80:81], v[192:193], v[80:81] op_sel:[1,0]
	v_pk_mul_f32 v[82:83], v[192:193], v[82:83] op_sel:[1,0]
	v_pk_fma_f32 v[116:117], v[72:73], v[168:169], v[116:117]
	v_pk_fma_f32 v[118:119], v[74:75], v[170:171], v[118:119]
	v_pk_fma_f32 v[112:113], v[80:81], v[172:173], v[112:113]
	v_pk_fma_f32 v[114:115], v[82:83], v[174:175], v[114:115]
	v_cvt_pk_f16_f32 v116, v116, v117
	v_cvt_pk_f16_f32 v117, v118, v119
	v_cvt_pk_f16_f32 v118, v112, v113
	v_cvt_pk_f16_f32 v119, v114, v115
	ds_write_b128 v235, v[116:119] offset:64
	v_fma_mix_f32 v140, v116, 1.0, v140 op_sel_hi:[1,0,0]
	v_fma_mix_f32 v141, v116, v116, v141 op_sel_hi:[1,1,0]
	v_fma_mix_f32 v140, v116, 1.0, v140 op_sel:[1,0,0] op_sel_hi:[1,0,0]
	v_fma_mix_f32 v141, v116, v116, v141 op_sel:[1,1,0] op_sel_hi:[1,1,0]
	v_fma_mix_f32 v140, v117, 1.0, v140 op_sel_hi:[1,0,0]
	v_fma_mix_f32 v141, v117, v117, v141 op_sel_hi:[1,1,0]
	v_fma_mix_f32 v140, v117, 1.0, v140 op_sel:[1,0,0] op_sel_hi:[1,0,0]
	v_fma_mix_f32 v141, v117, v117, v141 op_sel:[1,1,0] op_sel_hi:[1,1,0]
	v_fma_mix_f32 v140, v118, 1.0, v140 op_sel_hi:[1,0,0]
	v_fma_mix_f32 v141, v118, v118, v141 op_sel_hi:[1,1,0]
	v_fma_mix_f32 v140, v118, 1.0, v140 op_sel:[1,0,0] op_sel_hi:[1,0,0]
	v_fma_mix_f32 v141, v118, v118, v141 op_sel:[1,1,0] op_sel_hi:[1,1,0]
	v_fma_mix_f32 v140, v119, 1.0, v140 op_sel_hi:[1,0,0]
	v_fma_mix_f32 v141, v119, v119, v141 op_sel_hi:[1,1,0]
	v_fma_mix_f32 v140, v119, 1.0, v140 op_sel:[1,0,0] op_sel_hi:[1,0,0]
	v_fma_mix_f32 v141, v119, v119, v141 op_sel:[1,1,0] op_sel_hi:[1,1,0]
	ds_read_b128 v[208:211], v236
	ds_read_b128 v[128:131], v236 offset:1152
	s_add_u32 s94, s98, 0x3c000
	s_addc_u32 s95, s99, 0
	global_load_dwordx4 v[212:215], v191, s[94:95] offset:0 nt
	global_load_dwordx4 v[144:147], v191, s[94:95] offset:64 nt
	s_add_u32 s94, s98, 0x42000
	s_addc_u32 s95, s99, 0
	global_load_dwordx4 v[132:135], v191, s[94:95] offset:0 nt
	global_load_dwordx4 v[88:91], v191, s[94:95] offset:64 nt
	s_waitcnt vmcnt(13)
	v_cvt_f32_f16_e32 v72, v240
	v_cvt_f32_f16_sdwa v73, v240 dst_sel:DWORD dst_unused:UNUSED_PAD src0_sel:WORD_1
	v_cvt_f32_f16_e32 v74, v241
	v_cvt_f32_f16_sdwa v75, v241 dst_sel:DWORD dst_unused:UNUSED_PAD src0_sel:WORD_1
	v_cvt_f32_f16_e32 v80, v242
	v_cvt_f32_f16_sdwa v81, v242 dst_sel:DWORD dst_unused:UNUSED_PAD src0_sel:WORD_1
	v_cvt_f32_f16_e32 v82, v243
	v_cvt_f32_f16_sdwa v83, v243 dst_sel:DWORD dst_unused:UNUSED_PAD src0_sel:WORD_1
	v_sub_f32_e32 v72, v72, v194
	v_sub_f32_e32 v73, v73, v194
	v_sub_f32_e32 v74, v74, v194
	v_sub_f32_e32 v75, v75, v194
	v_sub_f32_e32 v80, v80, v194
	v_sub_f32_e32 v81, v81, v194
	v_sub_f32_e32 v82, v82, v194
	v_sub_f32_e32 v83, v83, v194
	v_pk_mul_f32 v[72:73], v[194:195], v[72:73] op_sel:[1,0]
	v_pk_mul_f32 v[74:75], v[194:195], v[74:75] op_sel:[1,0]
	v_pk_mul_f32 v[80:81], v[194:195], v[80:81] op_sel:[1,0]
	v_pk_mul_f32 v[82:83], v[194:195], v[82:83] op_sel:[1,0]
	v_pk_fma_f32 v[108:109], v[72:73], v[160:161], v[108:109]
	v_pk_fma_f32 v[110:111], v[74:75], v[162:163], v[110:111]
	v_pk_fma_f32 v[104:105], v[80:81], v[164:165], v[104:105]
	v_pk_fma_f32 v[106:107], v[82:83], v[166:167], v[106:107]
	v_cvt_pk_f16_f32 v108, v108, v109
	v_cvt_pk_f16_f32 v109, v110, v111
	v_cvt_pk_f16_f32 v110, v104, v105
	v_cvt_pk_f16_f32 v111, v106, v107
	s_waitcnt lgkmcnt(0)
	v_add_u32_e32 v83, 0x6000, v224
	buffer_store_dwordx4 v[208:211], v83, s[24:27], 0 offen nt
	v_add_u32_e32 v82, 0x9000, v224
	buffer_store_dwordx4 v[128:131], v82, s[24:27], 0 offen nt
	ds_write_b128 v235, v[108:111]
	v_fma_mix_f32 v142, v108, 1.0, 0 op_sel_hi:[1,0,0]
	v_fma_mix_f32 v143, v108, v108, 0 op_sel_hi:[1,1,0]
	v_fma_mix_f32 v142, v108, 1.0, v142 op_sel:[1,0,0] op_sel_hi:[1,0,0]
	v_fma_mix_f32 v143, v108, v108, v143 op_sel:[1,1,0] op_sel_hi:[1,1,0]
	v_fma_mix_f32 v142, v109, 1.0, v142 op_sel_hi:[1,0,0]
	v_fma_mix_f32 v143, v109, v109, v143 op_sel_hi:[1,1,0]
	v_fma_mix_f32 v142, v109, 1.0, v142 op_sel:[1,0,0] op_sel_hi:[1,0,0]
	v_fma_mix_f32 v143, v109, v109, v143 op_sel:[1,1,0] op_sel_hi:[1,1,0]
	v_fma_mix_f32 v142, v110, 1.0, v142 op_sel_hi:[1,0,0]
	v_fma_mix_f32 v143, v110, v110, v143 op_sel_hi:[1,1,0]
	v_fma_mix_f32 v142, v110, 1.0, v142 op_sel:[1,0,0] op_sel_hi:[1,0,0]
	v_fma_mix_f32 v143, v110, v110, v143 op_sel:[1,1,0] op_sel_hi:[1,1,0]
	v_fma_mix_f32 v142, v111, 1.0, v142 op_sel_hi:[1,0,0]
	v_fma_mix_f32 v143, v111, v111, v143 op_sel_hi:[1,1,0]
	v_fma_mix_f32 v142, v111, 1.0, v142 op_sel:[1,0,0] op_sel_hi:[1,0,0]
	v_fma_mix_f32 v143, v111, v111, v143 op_sel:[1,1,0] op_sel_hi:[1,1,0]
	s_waitcnt vmcnt(14)
	v_cvt_f32_f16_e32 v72, v244
	v_cvt_f32_f16_sdwa v73, v244 dst_sel:DWORD dst_unused:UNUSED_PAD src0_sel:WORD_1
	v_cvt_f32_f16_e32 v74, v245
	v_cvt_f32_f16_sdwa v75, v245 dst_sel:DWORD dst_unused:UNUSED_PAD src0_sel:WORD_1
	v_cvt_f32_f16_e32 v80, v246
	v_cvt_f32_f16_sdwa v81, v246 dst_sel:DWORD dst_unused:UNUSED_PAD src0_sel:WORD_1
	v_cvt_f32_f16_e32 v82, v247
	v_cvt_f32_f16_sdwa v83, v247 dst_sel:DWORD dst_unused:UNUSED_PAD src0_sel:WORD_1
	v_sub_f32_e32 v72, v72, v194
	v_sub_f32_e32 v73, v73, v194
	v_sub_f32_e32 v74, v74, v194
	v_sub_f32_e32 v75, v75, v194
	v_sub_f32_e32 v80, v80, v194
	v_sub_f32_e32 v81, v81, v194
	v_sub_f32_e32 v82, v82, v194
	v_sub_f32_e32 v83, v83, v194
	v_pk_mul_f32 v[72:73], v[194:195], v[72:73] op_sel:[1,0]
	v_pk_mul_f32 v[74:75], v[194:195], v[74:75] op_sel:[1,0]
	v_pk_mul_f32 v[80:81], v[194:195], v[80:81] op_sel:[1,0]
	v_pk_mul_f32 v[82:83], v[194:195], v[82:83] op_sel:[1,0]
	v_pk_fma_f32 v[100:101], v[72:73], v[168:169], v[100:101]
	v_pk_fma_f32 v[102:103], v[74:75], v[170:171], v[102:103]
	v_pk_fma_f32 v[96:97], v[80:81], v[172:173], v[96:97]
	v_pk_fma_f32 v[98:99], v[82:83], v[174:175], v[98:99]
	v_cvt_pk_f16_f32 v100, v100, v101
	v_cvt_pk_f16_f32 v101, v102, v103
	v_cvt_pk_f16_f32 v102, v96, v97
	v_cvt_pk_f16_f32 v103, v98, v99
	ds_write_b128 v235, v[100:103] offset:64
	v_fma_mix_f32 v142, v100, 1.0, v142 op_sel_hi:[1,0,0]
	v_fma_mix_f32 v143, v100, v100, v143 op_sel_hi:[1,1,0]
	v_fma_mix_f32 v142, v100, 1.0, v142 op_sel:[1,0,0] op_sel_hi:[1,0,0]
	v_fma_mix_f32 v143, v100, v100, v143 op_sel:[1,1,0] op_sel_hi:[1,1,0]
	v_fma_mix_f32 v142, v101, 1.0, v142 op_sel_hi:[1,0,0]
	v_fma_mix_f32 v143, v101, v101, v143 op_sel_hi:[1,1,0]
	v_fma_mix_f32 v142, v101, 1.0, v142 op_sel:[1,0,0] op_sel_hi:[1,0,0]
	v_fma_mix_f32 v143, v101, v101, v143 op_sel:[1,1,0] op_sel_hi:[1,1,0]
	v_fma_mix_f32 v142, v102, 1.0, v142 op_sel_hi:[1,0,0]
	v_fma_mix_f32 v143, v102, v102, v143 op_sel_hi:[1,1,0]
	v_fma_mix_f32 v142, v102, 1.0, v142 op_sel:[1,0,0] op_sel_hi:[1,0,0]
	v_fma_mix_f32 v143, v102, v102, v143 op_sel:[1,1,0] op_sel_hi:[1,1,0]
	v_fma_mix_f32 v142, v103, 1.0, v142 op_sel_hi:[1,0,0]
	v_fma_mix_f32 v143, v103, v103, v143 op_sel_hi:[1,1,0]
	v_fma_mix_f32 v142, v103, 1.0, v142 op_sel:[1,0,0] op_sel_hi:[1,0,0]
	v_fma_mix_f32 v143, v103, v103, v143 op_sel:[1,1,0] op_sel_hi:[1,1,0]
	ds_read_b128 v[92:95], v236
	ds_read_b128 v[120:123], v236 offset:1152
	s_waitcnt vmcnt(13)
	v_cvt_f32_f16_e32 v72, v248
	v_cvt_f32_f16_sdwa v73, v248 dst_sel:DWORD dst_unused:UNUSED_PAD src0_sel:WORD_1
	v_cvt_f32_f16_e32 v74, v249
	v_cvt_f32_f16_sdwa v75, v249 dst_sel:DWORD dst_unused:UNUSED_PAD src0_sel:WORD_1
	v_cvt_f32_f16_e32 v80, v250
	v_cvt_f32_f16_sdwa v81, v250 dst_sel:DWORD dst_unused:UNUSED_PAD src0_sel:WORD_1
	v_cvt_f32_f16_e32 v82, v251
	v_cvt_f32_f16_sdwa v83, v251 dst_sel:DWORD dst_unused:UNUSED_PAD src0_sel:WORD_1
	v_sub_f32_e32 v72, v72, v196
	v_sub_f32_e32 v73, v73, v196
	v_sub_f32_e32 v74, v74, v196
	v_sub_f32_e32 v75, v75, v196
	v_sub_f32_e32 v80, v80, v196
	v_sub_f32_e32 v81, v81, v196
	v_sub_f32_e32 v82, v82, v196
	v_sub_f32_e32 v83, v83, v196
	v_pk_mul_f32 v[72:73], v[196:197], v[72:73] op_sel:[1,0]
	v_pk_mul_f32 v[74:75], v[196:197], v[74:75] op_sel:[1,0]
	v_pk_mul_f32 v[80:81], v[196:197], v[80:81] op_sel:[1,0]
	v_pk_mul_f32 v[82:83], v[196:197], v[82:83] op_sel:[1,0]
	v_pk_fma_f32 v[84:85], v[72:73], v[160:161], v[84:85]
	v_pk_fma_f32 v[86:87], v[74:75], v[162:163], v[86:87]
	v_pk_fma_f32 v[76:77], v[80:81], v[164:165], v[76:77]
	v_pk_fma_f32 v[78:79], v[82:83], v[166:167], v[78:79]
	v_cvt_pk_f16_f32 v84, v84, v85
	v_cvt_pk_f16_f32 v85, v86, v87
	v_cvt_pk_f16_f32 v86, v76, v77
	v_cvt_pk_f16_f32 v87, v78, v79
	s_waitcnt lgkmcnt(0)
	v_add_u32_e32 v83, 0xc000, v224
	buffer_store_dwordx4 v[92:95], v83, s[24:27], 0 offen nt
	v_add_u32_e32 v82, 0xf000, v224
	buffer_store_dwordx4 v[120:123], v82, s[24:27], 0 offen nt
	ds_write_b128 v235, v[84:87]
	v_fma_mix_f32 v216, v84, 1.0, 0 op_sel_hi:[1,0,0]
	v_fma_mix_f32 v217, v84, v84, 0 op_sel_hi:[1,1,0]
	v_fma_mix_f32 v216, v84, 1.0, v216 op_sel:[1,0,0] op_sel_hi:[1,0,0]
	v_fma_mix_f32 v217, v84, v84, v217 op_sel:[1,1,0] op_sel_hi:[1,1,0]
	v_fma_mix_f32 v216, v85, 1.0, v216 op_sel_hi:[1,0,0]
	v_fma_mix_f32 v217, v85, v85, v217 op_sel_hi:[1,1,0]
	v_fma_mix_f32 v216, v85, 1.0, v216 op_sel:[1,0,0] op_sel_hi:[1,0,0]
	v_fma_mix_f32 v217, v85, v85, v217 op_sel:[1,1,0] op_sel_hi:[1,1,0]
	v_fma_mix_f32 v216, v86, 1.0, v216 op_sel_hi:[1,0,0]
	v_fma_mix_f32 v217, v86, v86, v217 op_sel_hi:[1,1,0]
	v_fma_mix_f32 v216, v86, 1.0, v216 op_sel:[1,0,0] op_sel_hi:[1,0,0]
	v_fma_mix_f32 v217, v86, v86, v217 op_sel:[1,1,0] op_sel_hi:[1,1,0]
	v_fma_mix_f32 v216, v87, 1.0, v216 op_sel_hi:[1,0,0]
	v_fma_mix_f32 v217, v87, v87, v217 op_sel_hi:[1,1,0]
	v_fma_mix_f32 v216, v87, 1.0, v216 op_sel:[1,0,0] op_sel_hi:[1,0,0]
	v_fma_mix_f32 v217, v87, v87, v217 op_sel:[1,1,0] op_sel_hi:[1,1,0]
	s_waitcnt vmcnt(14)
	v_cvt_f32_f16_e32 v72, v252
	v_cvt_f32_f16_sdwa v73, v252 dst_sel:DWORD dst_unused:UNUSED_PAD src0_sel:WORD_1
	v_cvt_f32_f16_e32 v74, v253
	v_cvt_f32_f16_sdwa v75, v253 dst_sel:DWORD dst_unused:UNUSED_PAD src0_sel:WORD_1
	v_cvt_f32_f16_e32 v80, v254
	v_cvt_f32_f16_sdwa v81, v254 dst_sel:DWORD dst_unused:UNUSED_PAD src0_sel:WORD_1
	v_cvt_f32_f16_e32 v82, v255
	v_cvt_f32_f16_sdwa v83, v255 dst_sel:DWORD dst_unused:UNUSED_PAD src0_sel:WORD_1
	v_sub_f32_e32 v72, v72, v196
	v_sub_f32_e32 v73, v73, v196
	v_sub_f32_e32 v74, v74, v196
	v_sub_f32_e32 v75, v75, v196
	v_sub_f32_e32 v80, v80, v196
	v_sub_f32_e32 v81, v81, v196
	v_sub_f32_e32 v82, v82, v196
	v_sub_f32_e32 v83, v83, v196
	v_pk_mul_f32 v[72:73], v[196:197], v[72:73] op_sel:[1,0]
	v_pk_mul_f32 v[74:75], v[196:197], v[74:75] op_sel:[1,0]
	v_pk_mul_f32 v[80:81], v[196:197], v[80:81] op_sel:[1,0]
	v_pk_mul_f32 v[82:83], v[196:197], v[82:83] op_sel:[1,0]
	v_pk_fma_f32 v[68:69], v[72:73], v[168:169], v[68:69]
	v_pk_fma_f32 v[70:71], v[74:75], v[170:171], v[70:71]
	v_pk_fma_f32 v[64:65], v[80:81], v[172:173], v[64:65]
	v_pk_fma_f32 v[66:67], v[82:83], v[174:175], v[66:67]
	v_cvt_pk_f16_f32 v68, v68, v69
	v_cvt_pk_f16_f32 v69, v70, v71
	v_cvt_pk_f16_f32 v70, v64, v65
	v_cvt_pk_f16_f32 v71, v66, v67
	ds_write_b128 v235, v[68:71] offset:64
	v_fma_mix_f32 v216, v68, 1.0, v216 op_sel_hi:[1,0,0]
	v_fma_mix_f32 v217, v68, v68, v217 op_sel_hi:[1,1,0]
	v_fma_mix_f32 v216, v68, 1.0, v216 op_sel:[1,0,0] op_sel_hi:[1,0,0]
	v_fma_mix_f32 v217, v68, v68, v217 op_sel:[1,1,0] op_sel_hi:[1,1,0]
	v_fma_mix_f32 v216, v69, 1.0, v216 op_sel_hi:[1,0,0]
	v_fma_mix_f32 v217, v69, v69, v217 op_sel_hi:[1,1,0]
	v_fma_mix_f32 v216, v69, 1.0, v216 op_sel:[1,0,0] op_sel_hi:[1,0,0]
	v_fma_mix_f32 v217, v69, v69, v217 op_sel:[1,1,0] op_sel_hi:[1,1,0]
	v_fma_mix_f32 v216, v70, 1.0, v216 op_sel_hi:[1,0,0]
	v_fma_mix_f32 v217, v70, v70, v217 op_sel_hi:[1,1,0]
	v_fma_mix_f32 v216, v70, 1.0, v216 op_sel:[1,0,0] op_sel_hi:[1,0,0]
	v_fma_mix_f32 v217, v70, v70, v217 op_sel:[1,1,0] op_sel_hi:[1,1,0]
	v_fma_mix_f32 v216, v71, 1.0, v216 op_sel_hi:[1,0,0]
	v_fma_mix_f32 v217, v71, v71, v217 op_sel_hi:[1,1,0]
	v_fma_mix_f32 v216, v71, 1.0, v216 op_sel:[1,0,0] op_sel_hi:[1,0,0]
	v_fma_mix_f32 v217, v71, v71, v217 op_sel:[1,1,0] op_sel_hi:[1,1,0]
	ds_read_b128 v[112:115], v236
	ds_read_b128 v[220:223], v236 offset:1152
	s_waitcnt vmcnt(13)
	v_cvt_f32_f16_e32 v72, v136
	v_cvt_f32_f16_sdwa v73, v136 dst_sel:DWORD dst_unused:UNUSED_PAD src0_sel:WORD_1
	v_cvt_f32_f16_e32 v74, v137
	v_cvt_f32_f16_sdwa v75, v137 dst_sel:DWORD dst_unused:UNUSED_PAD src0_sel:WORD_1
	v_cvt_f32_f16_e32 v80, v138
	v_cvt_f32_f16_sdwa v81, v138 dst_sel:DWORD dst_unused:UNUSED_PAD src0_sel:WORD_1
	v_cvt_f32_f16_e32 v82, v139
	v_cvt_f32_f16_sdwa v83, v139 dst_sel:DWORD dst_unused:UNUSED_PAD src0_sel:WORD_1
	v_sub_f32_e32 v72, v72, v198
	v_sub_f32_e32 v73, v73, v198
	v_sub_f32_e32 v74, v74, v198
	v_sub_f32_e32 v75, v75, v198
	v_sub_f32_e32 v80, v80, v198
	v_sub_f32_e32 v81, v81, v198
	v_sub_f32_e32 v82, v82, v198
	v_sub_f32_e32 v83, v83, v198
	v_pk_mul_f32 v[72:73], v[198:199], v[72:73] op_sel:[1,0]
	v_pk_mul_f32 v[74:75], v[198:199], v[74:75] op_sel:[1,0]
	v_pk_mul_f32 v[80:81], v[198:199], v[80:81] op_sel:[1,0]
	v_pk_mul_f32 v[82:83], v[198:199], v[82:83] op_sel:[1,0]
	v_pk_fma_f32 v[60:61], v[72:73], v[160:161], v[60:61]
	v_pk_fma_f32 v[62:63], v[74:75], v[162:163], v[62:63]
	v_pk_fma_f32 v[56:57], v[80:81], v[164:165], v[56:57]
	v_pk_fma_f32 v[58:59], v[82:83], v[166:167], v[58:59]
	v_cvt_pk_f16_f32 v60, v60, v61
	v_cvt_pk_f16_f32 v61, v62, v63
	v_cvt_pk_f16_f32 v62, v56, v57
	v_cvt_pk_f16_f32 v63, v58, v59
	s_waitcnt lgkmcnt(0)
	v_add_u32_e32 v83, 0x12000, v224
	buffer_store_dwordx4 v[112:115], v83, s[24:27], 0 offen nt
	v_add_u32_e32 v82, 0x15000, v224
	buffer_store_dwordx4 v[220:223], v82, s[24:27], 0 offen nt
	ds_write_b128 v235, v[60:63]
	v_fma_mix_f32 v218, v60, 1.0, 0 op_sel_hi:[1,0,0]
	v_fma_mix_f32 v219, v60, v60, 0 op_sel_hi:[1,1,0]
	v_fma_mix_f32 v218, v60, 1.0, v218 op_sel:[1,0,0] op_sel_hi:[1,0,0]
	v_fma_mix_f32 v219, v60, v60, v219 op_sel:[1,1,0] op_sel_hi:[1,1,0]
	v_fma_mix_f32 v218, v61, 1.0, v218 op_sel_hi:[1,0,0]
	v_fma_mix_f32 v219, v61, v61, v219 op_sel_hi:[1,1,0]
	v_fma_mix_f32 v218, v61, 1.0, v218 op_sel:[1,0,0] op_sel_hi:[1,0,0]
	v_fma_mix_f32 v219, v61, v61, v219 op_sel:[1,1,0] op_sel_hi:[1,1,0]
	v_fma_mix_f32 v218, v62, 1.0, v218 op_sel_hi:[1,0,0]
	v_fma_mix_f32 v219, v62, v62, v219 op_sel_hi:[1,1,0]
	v_fma_mix_f32 v218, v62, 1.0, v218 op_sel:[1,0,0] op_sel_hi:[1,0,0]
	v_fma_mix_f32 v219, v62, v62, v219 op_sel:[1,1,0] op_sel_hi:[1,1,0]
	v_fma_mix_f32 v218, v63, 1.0, v218 op_sel_hi:[1,0,0]
	v_fma_mix_f32 v219, v63, v63, v219 op_sel_hi:[1,1,0]
	v_fma_mix_f32 v218, v63, 1.0, v218 op_sel:[1,0,0] op_sel_hi:[1,0,0]
	v_fma_mix_f32 v219, v63, v63, v219 op_sel:[1,1,0] op_sel_hi:[1,1,0]
	s_waitcnt vmcnt(14)
	v_cvt_f32_f16_e32 v72, v148
	v_cvt_f32_f16_sdwa v73, v148 dst_sel:DWORD dst_unused:UNUSED_PAD src0_sel:WORD_1
	v_cvt_f32_f16_e32 v74, v149
	v_cvt_f32_f16_sdwa v75, v149 dst_sel:DWORD dst_unused:UNUSED_PAD src0_sel:WORD_1
	v_cvt_f32_f16_e32 v80, v150
	v_cvt_f32_f16_sdwa v81, v150 dst_sel:DWORD dst_unused:UNUSED_PAD src0_sel:WORD_1
	v_cvt_f32_f16_e32 v82, v151
	v_cvt_f32_f16_sdwa v83, v151 dst_sel:DWORD dst_unused:UNUSED_PAD src0_sel:WORD_1
	v_sub_f32_e32 v72, v72, v198
	v_sub_f32_e32 v73, v73, v198
	v_sub_f32_e32 v74, v74, v198
	v_sub_f32_e32 v75, v75, v198
	v_sub_f32_e32 v80, v80, v198
	v_sub_f32_e32 v81, v81, v198
	v_sub_f32_e32 v82, v82, v198
	v_sub_f32_e32 v83, v83, v198
	v_pk_mul_f32 v[72:73], v[198:199], v[72:73] op_sel:[1,0]
	v_pk_mul_f32 v[74:75], v[198:199], v[74:75] op_sel:[1,0]
	v_pk_mul_f32 v[80:81], v[198:199], v[80:81] op_sel:[1,0]
	v_pk_mul_f32 v[82:83], v[198:199], v[82:83] op_sel:[1,0]
	v_pk_fma_f32 v[52:53], v[72:73], v[168:169], v[52:53]
	v_pk_fma_f32 v[54:55], v[74:75], v[170:171], v[54:55]
	v_pk_fma_f32 v[48:49], v[80:81], v[172:173], v[48:49]
	v_pk_fma_f32 v[50:51], v[82:83], v[174:175], v[50:51]
	v_cvt_pk_f16_f32 v52, v52, v53
	v_cvt_pk_f16_f32 v53, v54, v55
	v_cvt_pk_f16_f32 v54, v48, v49
	v_cvt_pk_f16_f32 v55, v50, v51
	ds_write_b128 v235, v[52:55] offset:64
	v_fma_mix_f32 v218, v52, 1.0, v218 op_sel_hi:[1,0,0]
	v_fma_mix_f32 v219, v52, v52, v219 op_sel_hi:[1,1,0]
	v_fma_mix_f32 v218, v52, 1.0, v218 op_sel:[1,0,0] op_sel_hi:[1,0,0]
	v_fma_mix_f32 v219, v52, v52, v219 op_sel:[1,1,0] op_sel_hi:[1,1,0]
	v_fma_mix_f32 v218, v53, 1.0, v218 op_sel_hi:[1,0,0]
	v_fma_mix_f32 v219, v53, v53, v219 op_sel_hi:[1,1,0]
	v_fma_mix_f32 v218, v53, 1.0, v218 op_sel:[1,0,0] op_sel_hi:[1,0,0]
	v_fma_mix_f32 v219, v53, v53, v219 op_sel:[1,1,0] op_sel_hi:[1,1,0]
	v_fma_mix_f32 v218, v54, 1.0, v218 op_sel_hi:[1,0,0]
	v_fma_mix_f32 v219, v54, v54, v219 op_sel_hi:[1,1,0]
	v_fma_mix_f32 v218, v54, 1.0, v218 op_sel:[1,0,0] op_sel_hi:[1,0,0]
	v_fma_mix_f32 v219, v54, v54, v219 op_sel:[1,1,0] op_sel_hi:[1,1,0]
	v_fma_mix_f32 v218, v55, 1.0, v218 op_sel_hi:[1,0,0]
	v_fma_mix_f32 v219, v55, v55, v219 op_sel_hi:[1,1,0]
	v_fma_mix_f32 v218, v55, 1.0, v218 op_sel:[1,0,0] op_sel_hi:[1,0,0]
	v_fma_mix_f32 v219, v55, v55, v219 op_sel:[1,1,0] op_sel_hi:[1,1,0]
	ds_read_b128 v[124:127], v236
	ds_read_b128 v[116:119], v236 offset:1152
	s_waitcnt vmcnt(13)
	v_cvt_f32_f16_e32 v72, v152
	v_cvt_f32_f16_sdwa v73, v152 dst_sel:DWORD dst_unused:UNUSED_PAD src0_sel:WORD_1
	v_cvt_f32_f16_e32 v74, v153
	v_cvt_f32_f16_sdwa v75, v153 dst_sel:DWORD dst_unused:UNUSED_PAD src0_sel:WORD_1
	v_cvt_f32_f16_e32 v80, v154
	v_cvt_f32_f16_sdwa v81, v154 dst_sel:DWORD dst_unused:UNUSED_PAD src0_sel:WORD_1
	v_cvt_f32_f16_e32 v82, v155
	v_cvt_f32_f16_sdwa v83, v155 dst_sel:DWORD dst_unused:UNUSED_PAD src0_sel:WORD_1
	v_sub_f32_e32 v72, v72, v200
	v_sub_f32_e32 v73, v73, v200
	v_sub_f32_e32 v74, v74, v200
	v_sub_f32_e32 v75, v75, v200
	v_sub_f32_e32 v80, v80, v200
	v_sub_f32_e32 v81, v81, v200
	v_sub_f32_e32 v82, v82, v200
	v_sub_f32_e32 v83, v83, v200
	v_pk_mul_f32 v[72:73], v[200:201], v[72:73] op_sel:[1,0]
	v_pk_mul_f32 v[74:75], v[200:201], v[74:75] op_sel:[1,0]
	v_pk_mul_f32 v[80:81], v[200:201], v[80:81] op_sel:[1,0]
	v_pk_mul_f32 v[82:83], v[200:201], v[82:83] op_sel:[1,0]
	v_pk_fma_f32 v[44:45], v[72:73], v[160:161], v[44:45]
	v_pk_fma_f32 v[46:47], v[74:75], v[162:163], v[46:47]
	v_pk_fma_f32 v[40:41], v[80:81], v[164:165], v[40:41]
	v_pk_fma_f32 v[42:43], v[82:83], v[166:167], v[42:43]
	v_cvt_pk_f16_f32 v44, v44, v45
	v_cvt_pk_f16_f32 v45, v46, v47
	v_cvt_pk_f16_f32 v46, v40, v41
	v_cvt_pk_f16_f32 v47, v42, v43
	s_waitcnt lgkmcnt(0)
	v_add_u32_e32 v83, 0x30000, v224
	buffer_store_dwordx4 v[124:127], v83, s[24:27], 0 offen nt
	v_add_u32_e32 v82, 0x33000, v224
	buffer_store_dwordx4 v[116:119], v82, s[24:27], 0 offen nt
	ds_write_b128 v235, v[44:47]
	v_fma_mix_f32 v208, v44, 1.0, 0 op_sel_hi:[1,0,0]
	v_fma_mix_f32 v209, v44, v44, 0 op_sel_hi:[1,1,0]
	v_fma_mix_f32 v208, v44, 1.0, v208 op_sel:[1,0,0] op_sel_hi:[1,0,0]
	v_fma_mix_f32 v209, v44, v44, v209 op_sel:[1,1,0] op_sel_hi:[1,1,0]
	v_fma_mix_f32 v208, v45, 1.0, v208 op_sel_hi:[1,0,0]
	v_fma_mix_f32 v209, v45, v45, v209 op_sel_hi:[1,1,0]
	v_fma_mix_f32 v208, v45, 1.0, v208 op_sel:[1,0,0] op_sel_hi:[1,0,0]
	v_fma_mix_f32 v209, v45, v45, v209 op_sel:[1,1,0] op_sel_hi:[1,1,0]
	v_fma_mix_f32 v208, v46, 1.0, v208 op_sel_hi:[1,0,0]
	v_fma_mix_f32 v209, v46, v46, v209 op_sel_hi:[1,1,0]
	v_fma_mix_f32 v208, v46, 1.0, v208 op_sel:[1,0,0] op_sel_hi:[1,0,0]
	v_fma_mix_f32 v209, v46, v46, v209 op_sel:[1,1,0] op_sel_hi:[1,1,0]
	v_fma_mix_f32 v208, v47, 1.0, v208 op_sel_hi:[1,0,0]
	v_fma_mix_f32 v209, v47, v47, v209 op_sel_hi:[1,1,0]
	v_fma_mix_f32 v208, v47, 1.0, v208 op_sel:[1,0,0] op_sel_hi:[1,0,0]
	v_fma_mix_f32 v209, v47, v47, v209 op_sel:[1,1,0] op_sel_hi:[1,1,0]
	s_waitcnt vmcnt(14)
	v_cvt_f32_f16_e32 v72, v156
	v_cvt_f32_f16_sdwa v73, v156 dst_sel:DWORD dst_unused:UNUSED_PAD src0_sel:WORD_1
	v_cvt_f32_f16_e32 v74, v157
	v_cvt_f32_f16_sdwa v75, v157 dst_sel:DWORD dst_unused:UNUSED_PAD src0_sel:WORD_1
	v_cvt_f32_f16_e32 v80, v158
	v_cvt_f32_f16_sdwa v81, v158 dst_sel:DWORD dst_unused:UNUSED_PAD src0_sel:WORD_1
	v_cvt_f32_f16_e32 v82, v159
	v_cvt_f32_f16_sdwa v83, v159 dst_sel:DWORD dst_unused:UNUSED_PAD src0_sel:WORD_1
	v_sub_f32_e32 v72, v72, v200
	v_sub_f32_e32 v73, v73, v200
	v_sub_f32_e32 v74, v74, v200
	v_sub_f32_e32 v75, v75, v200
	v_sub_f32_e32 v80, v80, v200
	v_sub_f32_e32 v81, v81, v200
	v_sub_f32_e32 v82, v82, v200
	v_sub_f32_e32 v83, v83, v200
	v_pk_mul_f32 v[72:73], v[200:201], v[72:73] op_sel:[1,0]
	v_pk_mul_f32 v[74:75], v[200:201], v[74:75] op_sel:[1,0]
	v_pk_mul_f32 v[80:81], v[200:201], v[80:81] op_sel:[1,0]
	v_pk_mul_f32 v[82:83], v[200:201], v[82:83] op_sel:[1,0]
	v_pk_fma_f32 v[36:37], v[72:73], v[168:169], v[36:37]
	v_pk_fma_f32 v[38:39], v[74:75], v[170:171], v[38:39]
	v_pk_fma_f32 v[32:33], v[80:81], v[172:173], v[32:33]
	v_pk_fma_f32 v[34:35], v[82:83], v[174:175], v[34:35]
	v_cvt_pk_f16_f32 v36, v36, v37
	v_cvt_pk_f16_f32 v37, v38, v39
	v_cvt_pk_f16_f32 v38, v32, v33
	v_cvt_pk_f16_f32 v39, v34, v35
	ds_write_b128 v235, v[36:39] offset:64
	v_fma_mix_f32 v208, v36, 1.0, v208 op_sel_hi:[1,0,0]
	v_fma_mix_f32 v209, v36, v36, v209 op_sel_hi:[1,1,0]
	v_fma_mix_f32 v208, v36, 1.0, v208 op_sel:[1,0,0] op_sel_hi:[1,0,0]
	v_fma_mix_f32 v209, v36, v36, v209 op_sel:[1,1,0] op_sel_hi:[1,1,0]
	v_fma_mix_f32 v208, v37, 1.0, v208 op_sel_hi:[1,0,0]
	v_fma_mix_f32 v209, v37, v37, v209 op_sel_hi:[1,1,0]
	v_fma_mix_f32 v208, v37, 1.0, v208 op_sel:[1,0,0] op_sel_hi:[1,0,0]
	v_fma_mix_f32 v209, v37, v37, v209 op_sel:[1,1,0] op_sel_hi:[1,1,0]
	v_fma_mix_f32 v208, v38, 1.0, v208 op_sel_hi:[1,0,0]
	v_fma_mix_f32 v209, v38, v38, v209 op_sel_hi:[1,1,0]
	v_fma_mix_f32 v208, v38, 1.0, v208 op_sel:[1,0,0] op_sel_hi:[1,0,0]
	v_fma_mix_f32 v209, v38, v38, v209 op_sel:[1,1,0] op_sel_hi:[1,1,0]
	v_fma_mix_f32 v208, v39, 1.0, v208 op_sel_hi:[1,0,0]
	v_fma_mix_f32 v209, v39, v39, v209 op_sel_hi:[1,1,0]
	v_fma_mix_f32 v208, v39, 1.0, v208 op_sel:[1,0,0] op_sel_hi:[1,0,0]
	v_fma_mix_f32 v209, v39, v39, v209 op_sel:[1,1,0] op_sel_hi:[1,1,0]
	ds_read_b128 v[128:131], v236
	ds_read_b128 v[104:107], v236 offset:1152
	s_waitcnt vmcnt(11)
	v_cvt_f32_f16_e32 v72, v212
	v_cvt_f32_f16_sdwa v73, v212 dst_sel:DWORD dst_unused:UNUSED_PAD src0_sel:WORD_1
	v_cvt_f32_f16_e32 v74, v213
	v_cvt_f32_f16_sdwa v75, v213 dst_sel:DWORD dst_unused:UNUSED_PAD src0_sel:WORD_1
	v_cvt_f32_f16_e32 v80, v214
	v_cvt_f32_f16_sdwa v81, v214 dst_sel:DWORD dst_unused:UNUSED_PAD src0_sel:WORD_1
	v_cvt_f32_f16_e32 v82, v215
	v_cvt_f32_f16_sdwa v83, v215 dst_sel:DWORD dst_unused:UNUSED_PAD src0_sel:WORD_1
	v_sub_f32_e32 v72, v72, v202
	v_sub_f32_e32 v73, v73, v202
	v_sub_f32_e32 v74, v74, v202
	v_sub_f32_e32 v75, v75, v202
	v_sub_f32_e32 v80, v80, v202
	v_sub_f32_e32 v81, v81, v202
	v_sub_f32_e32 v82, v82, v202
	v_sub_f32_e32 v83, v83, v202
	v_pk_mul_f32 v[72:73], v[202:203], v[72:73] op_sel:[1,0]
	v_pk_mul_f32 v[74:75], v[202:203], v[74:75] op_sel:[1,0]
	v_pk_mul_f32 v[80:81], v[202:203], v[80:81] op_sel:[1,0]
	v_pk_mul_f32 v[82:83], v[202:203], v[82:83] op_sel:[1,0]
	v_pk_fma_f32 v[28:29], v[72:73], v[160:161], v[28:29]
	v_pk_fma_f32 v[30:31], v[74:75], v[162:163], v[30:31]
	v_pk_fma_f32 v[24:25], v[80:81], v[164:165], v[24:25]
	v_pk_fma_f32 v[26:27], v[82:83], v[166:167], v[26:27]
	v_cvt_pk_f16_f32 v28, v28, v29
	v_cvt_pk_f16_f32 v29, v30, v31
	v_cvt_pk_f16_f32 v30, v24, v25
	v_cvt_pk_f16_f32 v31, v26, v27
	s_waitcnt lgkmcnt(0)
	v_add_u32_e32 v83, 0x36000, v224
	buffer_store_dwordx4 v[128:131], v83, s[24:27], 0 offen nt
	v_add_u32_e32 v82, 0x39000, v224
	buffer_store_dwordx4 v[104:107], v82, s[24:27], 0 offen nt
	ds_write_b128 v235, v[28:31]
	v_fma_mix_f32 v210, v28, 1.0, 0 op_sel_hi:[1,0,0]
	v_fma_mix_f32 v211, v28, v28, 0 op_sel_hi:[1,1,0]
	v_fma_mix_f32 v210, v28, 1.0, v210 op_sel:[1,0,0] op_sel_hi:[1,0,0]
	v_fma_mix_f32 v211, v28, v28, v211 op_sel:[1,1,0] op_sel_hi:[1,1,0]
	v_fma_mix_f32 v210, v29, 1.0, v210 op_sel_hi:[1,0,0]
	v_fma_mix_f32 v211, v29, v29, v211 op_sel_hi:[1,1,0]
	v_fma_mix_f32 v210, v29, 1.0, v210 op_sel:[1,0,0] op_sel_hi:[1,0,0]
	v_fma_mix_f32 v211, v29, v29, v211 op_sel:[1,1,0] op_sel_hi:[1,1,0]
	v_fma_mix_f32 v210, v30, 1.0, v210 op_sel_hi:[1,0,0]
	v_fma_mix_f32 v211, v30, v30, v211 op_sel_hi:[1,1,0]
	v_fma_mix_f32 v210, v30, 1.0, v210 op_sel:[1,0,0] op_sel_hi:[1,0,0]
	v_fma_mix_f32 v211, v30, v30, v211 op_sel:[1,1,0] op_sel_hi:[1,1,0]
	v_fma_mix_f32 v210, v31, 1.0, v210 op_sel_hi:[1,0,0]
	v_fma_mix_f32 v211, v31, v31, v211 op_sel_hi:[1,1,0]
	v_fma_mix_f32 v210, v31, 1.0, v210 op_sel:[1,0,0] op_sel_hi:[1,0,0]
	v_fma_mix_f32 v211, v31, v31, v211 op_sel:[1,1,0] op_sel_hi:[1,1,0]
	s_waitcnt vmcnt(12)
	v_cvt_f32_f16_e32 v72, v144
	v_cvt_f32_f16_sdwa v73, v144 dst_sel:DWORD dst_unused:UNUSED_PAD src0_sel:WORD_1
	v_cvt_f32_f16_e32 v74, v145
	v_cvt_f32_f16_sdwa v75, v145 dst_sel:DWORD dst_unused:UNUSED_PAD src0_sel:WORD_1
	v_cvt_f32_f16_e32 v80, v146
	v_cvt_f32_f16_sdwa v81, v146 dst_sel:DWORD dst_unused:UNUSED_PAD src0_sel:WORD_1
	v_cvt_f32_f16_e32 v82, v147
	v_cvt_f32_f16_sdwa v83, v147 dst_sel:DWORD dst_unused:UNUSED_PAD src0_sel:WORD_1
	v_sub_f32_e32 v72, v72, v202
	v_sub_f32_e32 v73, v73, v202
	v_sub_f32_e32 v74, v74, v202
	v_sub_f32_e32 v75, v75, v202
	v_sub_f32_e32 v80, v80, v202
	v_sub_f32_e32 v81, v81, v202
	v_sub_f32_e32 v82, v82, v202
	v_sub_f32_e32 v83, v83, v202
	v_pk_mul_f32 v[72:73], v[202:203], v[72:73] op_sel:[1,0]
	v_pk_mul_f32 v[74:75], v[202:203], v[74:75] op_sel:[1,0]
	v_pk_mul_f32 v[80:81], v[202:203], v[80:81] op_sel:[1,0]
	v_pk_mul_f32 v[82:83], v[202:203], v[82:83] op_sel:[1,0]
	v_pk_fma_f32 v[20:21], v[72:73], v[168:169], v[20:21]
	v_pk_fma_f32 v[22:23], v[74:75], v[170:171], v[22:23]
	v_pk_fma_f32 v[16:17], v[80:81], v[172:173], v[16:17]
	v_pk_fma_f32 v[18:19], v[82:83], v[174:175], v[18:19]
	v_cvt_pk_f16_f32 v20, v20, v21
	v_cvt_pk_f16_f32 v21, v22, v23
	v_cvt_pk_f16_f32 v22, v16, v17
	v_cvt_pk_f16_f32 v23, v18, v19
	ds_write_b128 v235, v[20:23] offset:64
	v_fma_mix_f32 v210, v20, 1.0, v210 op_sel_hi:[1,0,0]
	v_fma_mix_f32 v211, v20, v20, v211 op_sel_hi:[1,1,0]
	v_fma_mix_f32 v210, v20, 1.0, v210 op_sel:[1,0,0] op_sel_hi:[1,0,0]
	v_fma_mix_f32 v211, v20, v20, v211 op_sel:[1,1,0] op_sel_hi:[1,1,0]
	v_fma_mix_f32 v210, v21, 1.0, v210 op_sel_hi:[1,0,0]
	v_fma_mix_f32 v211, v21, v21, v211 op_sel_hi:[1,1,0]
	v_fma_mix_f32 v210, v21, 1.0, v210 op_sel:[1,0,0] op_sel_hi:[1,0,0]
	v_fma_mix_f32 v211, v21, v21, v211 op_sel:[1,1,0] op_sel_hi:[1,1,0]
	v_fma_mix_f32 v210, v22, 1.0, v210 op_sel_hi:[1,0,0]
	v_fma_mix_f32 v211, v22, v22, v211 op_sel_hi:[1,1,0]
	v_fma_mix_f32 v210, v22, 1.0, v210 op_sel:[1,0,0] op_sel_hi:[1,0,0]
	v_fma_mix_f32 v211, v22, v22, v211 op_sel:[1,1,0] op_sel_hi:[1,1,0]
	v_fma_mix_f32 v210, v23, 1.0, v210 op_sel_hi:[1,0,0]
	v_fma_mix_f32 v211, v23, v23, v211 op_sel_hi:[1,1,0]
	v_fma_mix_f32 v210, v23, 1.0, v210 op_sel:[1,0,0] op_sel_hi:[1,0,0]
	v_fma_mix_f32 v211, v23, v23, v211 op_sel:[1,1,0] op_sel_hi:[1,1,0]
	ds_read_b128 v[240:243], v236
	ds_read_b128 v[96:99], v236 offset:1152
	s_waitcnt vmcnt(11)
	v_cvt_f32_f16_e32 v72, v132
	v_cvt_f32_f16_sdwa v73, v132 dst_sel:DWORD dst_unused:UNUSED_PAD src0_sel:WORD_1
	v_cvt_f32_f16_e32 v74, v133
	v_cvt_f32_f16_sdwa v75, v133 dst_sel:DWORD dst_unused:UNUSED_PAD src0_sel:WORD_1
	v_cvt_f32_f16_e32 v80, v134
	v_cvt_f32_f16_sdwa v81, v134 dst_sel:DWORD dst_unused:UNUSED_PAD src0_sel:WORD_1
	v_cvt_f32_f16_e32 v82, v135
	v_cvt_f32_f16_sdwa v83, v135 dst_sel:DWORD dst_unused:UNUSED_PAD src0_sel:WORD_1
	v_sub_f32_e32 v72, v72, v204
	v_sub_f32_e32 v73, v73, v204
	v_sub_f32_e32 v74, v74, v204
	v_sub_f32_e32 v75, v75, v204
	v_sub_f32_e32 v80, v80, v204
	v_sub_f32_e32 v81, v81, v204
	v_sub_f32_e32 v82, v82, v204
	v_sub_f32_e32 v83, v83, v204
	v_pk_mul_f32 v[72:73], v[204:205], v[72:73] op_sel:[1,0]
	v_pk_mul_f32 v[74:75], v[204:205], v[74:75] op_sel:[1,0]
	v_pk_mul_f32 v[80:81], v[204:205], v[80:81] op_sel:[1,0]
	v_pk_mul_f32 v[82:83], v[204:205], v[82:83] op_sel:[1,0]
	v_pk_fma_f32 v[12:13], v[72:73], v[160:161], v[12:13]
	v_pk_fma_f32 v[14:15], v[74:75], v[162:163], v[14:15]
	v_pk_fma_f32 v[8:9], v[80:81], v[164:165], v[8:9]
	v_pk_fma_f32 v[10:11], v[82:83], v[166:167], v[10:11]
	v_cvt_pk_f16_f32 v12, v12, v13
	v_cvt_pk_f16_f32 v13, v14, v15
	v_cvt_pk_f16_f32 v14, v8, v9
	v_cvt_pk_f16_f32 v15, v10, v11
	s_waitcnt lgkmcnt(0)
	v_add_u32_e32 v83, 0x3c000, v224
	buffer_store_dwordx4 v[240:243], v83, s[24:27], 0 offen nt
	v_add_u32_e32 v82, 0x3f000, v224
	buffer_store_dwordx4 v[96:99], v82, s[24:27], 0 offen nt
	ds_write_b128 v235, v[12:15]
	v_fma_mix_f32 v244, v12, 1.0, 0 op_sel_hi:[1,0,0]
	v_fma_mix_f32 v245, v12, v12, 0 op_sel_hi:[1,1,0]
	v_fma_mix_f32 v244, v12, 1.0, v244 op_sel:[1,0,0] op_sel_hi:[1,0,0]
	v_fma_mix_f32 v245, v12, v12, v245 op_sel:[1,1,0] op_sel_hi:[1,1,0]
	v_fma_mix_f32 v244, v13, 1.0, v244 op_sel_hi:[1,0,0]
	v_fma_mix_f32 v245, v13, v13, v245 op_sel_hi:[1,1,0]
	v_fma_mix_f32 v244, v13, 1.0, v244 op_sel:[1,0,0] op_sel_hi:[1,0,0]
	v_fma_mix_f32 v245, v13, v13, v245 op_sel:[1,1,0] op_sel_hi:[1,1,0]
	v_fma_mix_f32 v244, v14, 1.0, v244 op_sel_hi:[1,0,0]
	v_fma_mix_f32 v245, v14, v14, v245 op_sel_hi:[1,1,0]
	v_fma_mix_f32 v244, v14, 1.0, v244 op_sel:[1,0,0] op_sel_hi:[1,0,0]
	v_fma_mix_f32 v245, v14, v14, v245 op_sel:[1,1,0] op_sel_hi:[1,1,0]
	v_fma_mix_f32 v244, v15, 1.0, v244 op_sel_hi:[1,0,0]
	v_fma_mix_f32 v245, v15, v15, v245 op_sel_hi:[1,1,0]
	v_fma_mix_f32 v244, v15, 1.0, v244 op_sel:[1,0,0] op_sel_hi:[1,0,0]
	v_fma_mix_f32 v245, v15, v15, v245 op_sel:[1,1,0] op_sel_hi:[1,1,0]
	s_waitcnt vmcnt(12)
	v_cvt_f32_f16_e32 v72, v88
	v_cvt_f32_f16_sdwa v73, v88 dst_sel:DWORD dst_unused:UNUSED_PAD src0_sel:WORD_1
	v_cvt_f32_f16_e32 v74, v89
	v_cvt_f32_f16_sdwa v75, v89 dst_sel:DWORD dst_unused:UNUSED_PAD src0_sel:WORD_1
	v_cvt_f32_f16_e32 v80, v90
	v_cvt_f32_f16_sdwa v81, v90 dst_sel:DWORD dst_unused:UNUSED_PAD src0_sel:WORD_1
	v_cvt_f32_f16_e32 v82, v91
	v_cvt_f32_f16_sdwa v83, v91 dst_sel:DWORD dst_unused:UNUSED_PAD src0_sel:WORD_1
	v_sub_f32_e32 v72, v72, v204
	v_sub_f32_e32 v73, v73, v204
	v_sub_f32_e32 v74, v74, v204
	v_sub_f32_e32 v75, v75, v204
	v_sub_f32_e32 v80, v80, v204
	v_sub_f32_e32 v81, v81, v204
	v_sub_f32_e32 v82, v82, v204
	v_sub_f32_e32 v83, v83, v204
	v_pk_mul_f32 v[72:73], v[204:205], v[72:73] op_sel:[1,0]
	v_pk_mul_f32 v[74:75], v[204:205], v[74:75] op_sel:[1,0]
	v_pk_mul_f32 v[80:81], v[204:205], v[80:81] op_sel:[1,0]
	v_pk_mul_f32 v[82:83], v[204:205], v[82:83] op_sel:[1,0]
	v_pk_fma_f32 v[4:5], v[72:73], v[168:169], v[4:5]
	v_pk_fma_f32 v[6:7], v[74:75], v[170:171], v[6:7]
	v_pk_fma_f32 v[0:1], v[80:81], v[172:173], v[0:1]
	v_pk_fma_f32 v[2:3], v[82:83], v[174:175], v[2:3]
	v_cvt_pk_f16_f32 v4, v4, v5
	v_cvt_pk_f16_f32 v5, v6, v7
	v_cvt_pk_f16_f32 v6, v0, v1
	v_cvt_pk_f16_f32 v7, v2, v3
	ds_write_b128 v235, v[4:7] offset:64
	v_fma_mix_f32 v244, v4, 1.0, v244 op_sel_hi:[1,0,0]
	v_fma_mix_f32 v245, v4, v4, v245 op_sel_hi:[1,1,0]
	v_fma_mix_f32 v244, v4, 1.0, v244 op_sel:[1,0,0] op_sel_hi:[1,0,0]
	v_fma_mix_f32 v245, v4, v4, v245 op_sel:[1,1,0] op_sel_hi:[1,1,0]
	v_fma_mix_f32 v244, v5, 1.0, v244 op_sel_hi:[1,0,0]
	v_fma_mix_f32 v245, v5, v5, v245 op_sel_hi:[1,1,0]
	v_fma_mix_f32 v244, v5, 1.0, v244 op_sel:[1,0,0] op_sel_hi:[1,0,0]
	v_fma_mix_f32 v245, v5, v5, v245 op_sel:[1,1,0] op_sel_hi:[1,1,0]
	v_fma_mix_f32 v244, v6, 1.0, v244 op_sel_hi:[1,0,0]
	v_fma_mix_f32 v245, v6, v6, v245 op_sel_hi:[1,1,0]
	v_fma_mix_f32 v244, v6, 1.0, v244 op_sel:[1,0,0] op_sel_hi:[1,0,0]
	v_fma_mix_f32 v245, v6, v6, v245 op_sel:[1,1,0] op_sel_hi:[1,1,0]
	v_fma_mix_f32 v244, v7, 1.0, v244 op_sel_hi:[1,0,0]
	v_fma_mix_f32 v245, v7, v7, v245 op_sel_hi:[1,1,0]
	v_fma_mix_f32 v244, v7, 1.0, v244 op_sel:[1,0,0] op_sel_hi:[1,0,0]
	v_fma_mix_f32 v245, v7, v7, v245 op_sel:[1,1,0] op_sel_hi:[1,1,0]
	ds_read_b128 v[108:111], v236
	ds_read_b128 v[100:103], v236 offset:1152
	s_waitcnt lgkmcnt(0)
	v_add_u32_e32 v83, 0x42000, v224
	buffer_store_dwordx4 v[108:111], v83, s[24:27], 0 offen nt
	v_add_u32_e32 v82, 0x45000, v224
	buffer_store_dwordx4 v[100:103], v82, s[24:27], 0 offen nt
	v_xor_b32_e32 v225, 16, v234
	v_lshlrev_b32_e32 v225, 2, v225
	v_xor_b32_e32 v246, 32, v234
	v_lshlrev_b32_e32 v246, 2, v246
	ds_bpermute_b32 v92, v225, v206
	ds_bpermute_b32 v93, v225, v207
	ds_bpermute_b32 v94, v225, v140
	ds_bpermute_b32 v95, v225, v141
	ds_bpermute_b32 v120, v225, v142
	ds_bpermute_b32 v121, v225, v143
	ds_bpermute_b32 v122, v225, v216
	ds_bpermute_b32 v123, v225, v217
	s_waitcnt lgkmcnt(0)
	v_pk_add_f32 v[206:207], v[206:207], v[92:93]
	v_pk_add_f32 v[140:141], v[140:141], v[94:95]
	v_pk_add_f32 v[142:143], v[142:143], v[120:121]
	v_pk_add_f32 v[216:217], v[216:217], v[122:123]
	ds_bpermute_b32 v92, v225, v218
	ds_bpermute_b32 v93, v225, v219
	ds_bpermute_b32 v94, v225, v208
	ds_bpermute_b32 v95, v225, v209
	ds_bpermute_b32 v120, v225, v210
	ds_bpermute_b32 v121, v225, v211
	ds_bpermute_b32 v122, v225, v244
	ds_bpermute_b32 v123, v225, v245
	s_waitcnt lgkmcnt(0)
	v_pk_add_f32 v[218:219], v[218:219], v[92:93]
	v_pk_add_f32 v[208:209], v[208:209], v[94:95]
	v_pk_add_f32 v[210:211], v[210:211], v[120:121]
	v_pk_add_f32 v[244:245], v[244:245], v[122:123]
	ds_bpermute_b32 v92, v246, v206
	ds_bpermute_b32 v93, v246, v207
	ds_bpermute_b32 v94, v246, v140
	ds_bpermute_b32 v95, v246, v141
	ds_bpermute_b32 v120, v246, v142
	ds_bpermute_b32 v121, v246, v143
	ds_bpermute_b32 v122, v246, v216
	ds_bpermute_b32 v123, v246, v217
	s_waitcnt lgkmcnt(0)
	v_pk_add_f32 v[206:207], v[206:207], v[92:93]
	v_pk_add_f32 v[140:141], v[140:141], v[94:95]
	v_pk_add_f32 v[142:143], v[142:143], v[120:121]
	v_pk_add_f32 v[216:217], v[216:217], v[122:123]
	ds_bpermute_b32 v92, v246, v218
	ds_bpermute_b32 v93, v246, v219
	ds_bpermute_b32 v94, v246, v208
	ds_bpermute_b32 v95, v246, v209
	ds_bpermute_b32 v120, v246, v210
	ds_bpermute_b32 v121, v246, v211
	ds_bpermute_b32 v122, v246, v244
	ds_bpermute_b32 v123, v246, v245
	s_waitcnt lgkmcnt(0)
	v_pk_add_f32 v[218:219], v[218:219], v[92:93]
	v_pk_add_f32 v[208:209], v[208:209], v[94:95]
	v_pk_add_f32 v[210:211], v[210:211], v[120:121]
	v_pk_add_f32 v[244:245], v[244:245], v[122:123]
	s_mov_b64 exec, 0xffff
	global_store_dwordx2 v190, v[206:207], s[100:101] offset:0
	global_store_dwordx2 v190, v[140:141], s[100:101] offset:128
	global_store_dwordx2 v190, v[142:143], s[100:101] offset:256
	global_store_dwordx2 v190, v[216:217], s[100:101] offset:384
	global_store_dwordx2 v190, v[218:219], s[100:101] offset:1024
	global_store_dwordx2 v190, v[208:209], s[100:101] offset:1152
	global_store_dwordx2 v190, v[210:211], s[100:101] offset:1280
	global_store_dwordx2 v190, v[244:245], s[100:101] offset:1408
	s_mov_b64 exec, -1
	s_mov_b32 s83, s81
	s_mov_b32 s84, s82
	s_mov_b64 s[40:41], s[0:1]
	s_mov_b64 s[38:39], s[8:9]
	s_mov_b64 vcc, s[6:7]
	s_cbranch_vccz .LBB8_12
	s_waitcnt vmcnt(0)
	s_cmpk_gt_u32 s44, 0xff
	s_cbranch_scc1 .LBB8_31
	s_barrier

.LBB8_32:
	s_endpgm
	s_endpgm
	s_endpgm
	s_endpgm
	s_endpgm
	s_endpgm
	s_endpgm
	s_endpgm
	s_endpgm
	s_endpgm
	s_endpgm
	s_endpgm
	s_endpgm
	s_endpgm
	s_endpgm
	s_endpgm
	s_endpgm
	s_endpgm
	s_endpgm
	s_endpgm
	s_endpgm
	s_endpgm
	s_endpgm
	s_endpgm
	.section	.rodata,"a",@progbits
	.p2align	6, 0x0

.LBB9_26:
	v_add_u32_e32 v254, 0x18000, v168
	v_add_u32_e32 v255, 0x1c000, v168
	s_lshl_b32 s34, s70, 8
	s_add_i32 s34, s34, s48
	v_or_b32_e32 v250, s34, v167
	v_ashrrev_i32_e32 v251, 31, v250
	v_lshl_add_u64 v[250:251], v[250:251], 3, s[12:13]
	s_lshl_b32 s35, s68, 8
	s_or_b32 s35, s35, s51
	v_or_b32_e32 v252, s35, v166
	v_ashrrev_i32_e32 v253, 31, v252
	v_lshl_add_u64 v[252:253], v[252:253], 2, s[14:15]
	global_load_dword v226, v[250:251], off offset:4
	global_load_dword v227, v[250:251], off offset:132
	global_load_dword v228, v[250:251], off offset:260
	global_load_dword v229, v[250:251], off offset:388
	global_load_dword v230, v[250:251], off offset:1028
	global_load_dword v231, v[250:251], off offset:1156
	global_load_dword v232, v[250:251], off offset:1284
	global_load_dword v233, v[250:251], off offset:1412
	global_load_dwordx4 v[234:237], v[252:253], off
	global_load_dwordx4 v[238:241], v[252:253], off offset:16
	global_load_dwordx4 v[242:245], v[252:253], off offset:128
	global_load_dwordx4 v[246:249], v[252:253], off offset:144
	s_add_u32 s28, s28, 0x30080
	s_addc_u32 s29, s29, 0
	s_add_u32 s71, s30, 0x100
	v_mov_b32_e32 v0, 0
	s_addc_u32 s72, s31, 0
	s_mov_b32 s73, -2
	v_mov_b32_e32 v1, v0
	v_mov_b32_e32 v2, v0
	v_mov_b32_e32 v3, v0
	v_mov_b32_e32 v4, v0
	v_mov_b32_e32 v5, v0
	v_mov_b32_e32 v6, v0
	v_mov_b32_e32 v7, v0
	v_mov_b32_e32 v12, v0
	v_mov_b32_e32 v13, v0
	v_mov_b32_e32 v14, v0
	v_mov_b32_e32 v15, v0
	v_mov_b32_e32 v20, v0
	v_mov_b32_e32 v21, v0
	v_mov_b32_e32 v22, v0
	v_mov_b32_e32 v23, v0
	v_mov_b32_e32 v28, v0
	v_mov_b32_e32 v29, v0
	v_mov_b32_e32 v30, v0
	v_mov_b32_e32 v31, v0
	v_mov_b32_e32 v36, v0
	v_mov_b32_e32 v37, v0
	v_mov_b32_e32 v38, v0
	v_mov_b32_e32 v39, v0
	v_mov_b32_e32 v44, v0
	v_mov_b32_e32 v45, v0
	v_mov_b32_e32 v46, v0
	v_mov_b32_e32 v47, v0
	v_mov_b32_e32 v52, v0
	v_mov_b32_e32 v53, v0
	v_mov_b32_e32 v54, v0
	v_mov_b32_e32 v55, v0
	v_mov_b32_e32 v8, v0
	v_mov_b32_e32 v9, v0
	v_mov_b32_e32 v10, v0
	v_mov_b32_e32 v11, v0
	v_mov_b32_e32 v16, v0
	v_mov_b32_e32 v17, v0
	v_mov_b32_e32 v18, v0
	v_mov_b32_e32 v19, v0
	v_mov_b32_e32 v24, v0
	v_mov_b32_e32 v25, v0
	v_mov_b32_e32 v26, v0
	v_mov_b32_e32 v27, v0
	v_mov_b32_e32 v32, v0
	v_mov_b32_e32 v33, v0
	v_mov_b32_e32 v34, v0
	v_mov_b32_e32 v35, v0
	v_mov_b32_e32 v40, v0
	v_mov_b32_e32 v41, v0
	v_mov_b32_e32 v42, v0
	v_mov_b32_e32 v43, v0
	v_mov_b32_e32 v48, v0
	v_mov_b32_e32 v49, v0
	v_mov_b32_e32 v50, v0
	v_mov_b32_e32 v51, v0
	v_mov_b32_e32 v56, v0
	v_mov_b32_e32 v57, v0
	v_mov_b32_e32 v58, v0
	v_mov_b32_e32 v59, v0
	v_mov_b32_e32 v60, v0
	v_mov_b32_e32 v61, v0
	v_mov_b32_e32 v62, v0
	v_mov_b32_e32 v63, v0
	v_mov_b32_e32 v64, v0
	v_mov_b32_e32 v65, v0
	v_mov_b32_e32 v66, v0
	v_mov_b32_e32 v67, v0
	v_mov_b32_e32 v68, v0
	v_mov_b32_e32 v69, v0
	v_mov_b32_e32 v70, v0
	v_mov_b32_e32 v71, v0
	v_mov_b32_e32 v76, v0
	v_mov_b32_e32 v77, v0
	v_mov_b32_e32 v78, v0
	v_mov_b32_e32 v79, v0
	v_mov_b32_e32 v84, v0
	v_mov_b32_e32 v85, v0
	v_mov_b32_e32 v86, v0
	v_mov_b32_e32 v87, v0
	v_mov_b32_e32 v92, v0
	v_mov_b32_e32 v93, v0
	v_mov_b32_e32 v94, v0
	v_mov_b32_e32 v95, v0
	v_mov_b32_e32 v100, v0
	v_mov_b32_e32 v101, v0
	v_mov_b32_e32 v102, v0
	v_mov_b32_e32 v103, v0
	v_mov_b32_e32 v112, v0
	v_mov_b32_e32 v113, v0
	v_mov_b32_e32 v114, v0
	v_mov_b32_e32 v115, v0
	v_mov_b32_e32 v116, v0
	v_mov_b32_e32 v117, v0
	v_mov_b32_e32 v118, v0
	v_mov_b32_e32 v119, v0
	v_mov_b32_e32 v72, v0
	v_mov_b32_e32 v73, v0
	v_mov_b32_e32 v74, v0
	v_mov_b32_e32 v75, v0
	v_mov_b32_e32 v80, v0
	v_mov_b32_e32 v81, v0
	v_mov_b32_e32 v82, v0
	v_mov_b32_e32 v83, v0
	v_mov_b32_e32 v88, v0
	v_mov_b32_e32 v89, v0
	v_mov_b32_e32 v90, v0
	v_mov_b32_e32 v91, v0
	v_mov_b32_e32 v96, v0
	v_mov_b32_e32 v97, v0
	v_mov_b32_e32 v98, v0
	v_mov_b32_e32 v99, v0
	v_mov_b32_e32 v104, v0
	v_mov_b32_e32 v105, v0
	v_mov_b32_e32 v106, v0
	v_mov_b32_e32 v107, v0
	v_mov_b32_e32 v108, v0
	v_mov_b32_e32 v109, v0
	v_mov_b32_e32 v110, v0
	v_mov_b32_e32 v111, v0
	v_mov_b32_e32 v120, v0
	v_mov_b32_e32 v121, v0
	v_mov_b32_e32 v122, v0
	v_mov_b32_e32 v123, v0
	v_mov_b32_e32 v124, v0
	v_mov_b32_e32 v125, v0
	v_mov_b32_e32 v126, v0
	v_mov_b32_e32 v127, v0
	ds_read_b128 v[128:131], v172
	ds_read_b128 v[132:135], v172 offset:1024
	ds_read_b128 v[136:139], v172 offset:2048
	ds_read_b128 v[140:143], v172 offset:3072
.LBB9_27:
	s_add_u32 s30, s28, 0xfffd0080
	s_addc_u32 s31, s29, -1
	s_cmp_eq_u32 s73, 8
	s_cselect_b32 s35, s9, s31
	s_cselect_b32 s34, s8, s30
	s_cselect_b32 s31, s1, s72
	s_cselect_b32 s30, s0, s71
	s_add_i32 m0, s43, 0xc000
	ds_read_b128 v[158:161], v173
	ds_read_b128 v[162:165], v173 offset:1024
	ds_read_b128 v[178:181], v173 offset:2048
	ds_read_b128 v[182:185], v173 offset:3072
	ds_read_b128 v[186:189], v173 offset:4096
	ds_read_b128 v[190:193], v173 offset:5120
	ds_read_b128 v[194:197], v173 offset:6144
	ds_read_b128 v[198:201], v173 offset:7168
	global_load_lds_dwordx4 v152, s[28:29]
	s_add_i32 m0, s43, 0xe000
	s_nop 0
	global_load_lds_dwordx4 v154, s[28:29]
	s_waitcnt lgkmcnt(8)
	s_barrier
	s_waitcnt lgkmcnt(0)
	v_mfma_f32_16x16x32_f16 v[124:127], v[128:131], v[158:161], v[124:127]
	v_mfma_f32_16x16x32_f16 v[120:123], v[136:139], v[158:161], v[120:123]
	v_mfma_f32_16x16x32_f16 v[108:111], v[128:131], v[178:181], v[108:111]
	v_mfma_f32_16x16x32_f16 v[104:107], v[136:139], v[178:181], v[104:107]
	v_mfma_f32_16x16x32_f16 v[96:99], v[128:131], v[186:189], v[96:99]
	v_mfma_f32_16x16x32_f16 v[88:91], v[136:139], v[186:189], v[88:91]
	v_mfma_f32_16x16x32_f16 v[80:83], v[128:131], v[194:197], v[80:83]
	v_mfma_f32_16x16x32_f16 v[72:75], v[136:139], v[194:197], v[72:75]
	v_mfma_f32_16x16x32_f16 v[124:127], v[132:135], v[162:165], v[124:127]
	v_mfma_f32_16x16x32_f16 v[120:123], v[140:143], v[162:165], v[120:123]
	v_mfma_f32_16x16x32_f16 v[108:111], v[132:135], v[182:185], v[108:111]
	v_mfma_f32_16x16x32_f16 v[104:107], v[140:143], v[182:185], v[104:107]
	v_mfma_f32_16x16x32_f16 v[96:99], v[132:135], v[190:193], v[96:99]
	v_mfma_f32_16x16x32_f16 v[88:91], v[140:143], v[190:193], v[88:91]
	v_mfma_f32_16x16x32_f16 v[80:83], v[132:135], v[198:201], v[80:83]
	v_mfma_f32_16x16x32_f16 v[72:75], v[140:143], v[198:201], v[72:75]
	s_barrier
	s_add_i32 s74, s65, s42
	s_mov_b32 m0, s74
	ds_read_b128 v[202:205], v174
	ds_read_b128 v[206:209], v174 offset:1024
	ds_read_b128 v[210:213], v174 offset:2048
	ds_read_b128 v[214:217], v174 offset:3072
	global_load_lds_dwordx4 v146, s[30:31]
	s_add_i32 m0, s74, 0x2000
	s_add_u32 s78, s30, 0x80
	s_addc_u32 s79, s31, 0
	global_load_lds_dwordx4 v150, s[30:31]
	s_barrier
	s_waitcnt lgkmcnt(0)
	v_mfma_f32_16x16x32_f16 v[116:119], v[202:205], v[158:161], v[116:119]
	v_mfma_f32_16x16x32_f16 v[112:115], v[210:213], v[158:161], v[112:115]
	v_mfma_f32_16x16x32_f16 v[100:103], v[202:205], v[178:181], v[100:103]
	v_mfma_f32_16x16x32_f16 v[92:95], v[210:213], v[178:181], v[92:95]
	v_mfma_f32_16x16x32_f16 v[84:87], v[202:205], v[186:189], v[84:87]
	v_mfma_f32_16x16x32_f16 v[76:79], v[210:213], v[186:189], v[76:79]
	v_mfma_f32_16x16x32_f16 v[68:71], v[202:205], v[194:197], v[68:71]
	v_mfma_f32_16x16x32_f16 v[64:67], v[210:213], v[194:197], v[64:67]
	v_mfma_f32_16x16x32_f16 v[116:119], v[206:209], v[162:165], v[116:119]
	v_mfma_f32_16x16x32_f16 v[112:115], v[214:217], v[162:165], v[112:115]
	v_mfma_f32_16x16x32_f16 v[100:103], v[206:209], v[182:185], v[100:103]
	v_mfma_f32_16x16x32_f16 v[92:95], v[214:217], v[182:185], v[92:95]
	v_mfma_f32_16x16x32_f16 v[84:87], v[206:209], v[190:193], v[84:87]
	v_mfma_f32_16x16x32_f16 v[76:79], v[214:217], v[190:193], v[76:79]
	v_mfma_f32_16x16x32_f16 v[68:71], v[206:209], v[198:201], v[68:71]
	v_mfma_f32_16x16x32_f16 v[64:67], v[214:217], v[198:201], v[64:67]
	s_barrier
	s_mov_b32 m0, s43
	ds_read_b128 v[158:161], v173 offset:16384
	ds_read_b128 v[162:165], v173 offset:17408
	ds_read_b128 v[178:181], v173 offset:18432
	ds_read_b128 v[182:185], v173 offset:19456
	ds_read_b128 v[186:189], v173 offset:20480
	ds_read_b128 v[190:193], v173 offset:21504
	ds_read_b128 v[194:197], v173 offset:22528
	ds_read_b128 v[198:201], v173 offset:23552
	global_load_lds_dwordx4 v144, s[34:35]
	s_mov_b32 m0, s44
	s_add_u32 s80, s34, 0x80
	s_addc_u32 s81, s35, 0
	global_load_lds_dwordx4 v148, s[34:35]
	s_waitcnt vmcnt(10)
	s_barrier
	s_waitcnt lgkmcnt(0)
	v_mfma_f32_16x16x32_f16 v[60:63], v[128:131], v[158:161], v[60:63]
	v_mfma_f32_16x16x32_f16 v[56:59], v[136:139], v[158:161], v[56:59]
	v_mfma_f32_16x16x32_f16 v[48:51], v[128:131], v[178:181], v[48:51]
	v_mfma_f32_16x16x32_f16 v[40:43], v[136:139], v[178:181], v[40:43]
	v_mfma_f32_16x16x32_f16 v[32:35], v[128:131], v[186:189], v[32:35]
	v_mfma_f32_16x16x32_f16 v[24:27], v[136:139], v[186:189], v[24:27]
	v_mfma_f32_16x16x32_f16 v[16:19], v[128:131], v[194:197], v[16:19]
	v_mfma_f32_16x16x32_f16 v[8:11], v[136:139], v[194:197], v[8:11]
	v_mfma_f32_16x16x32_f16 v[60:63], v[132:135], v[162:165], v[60:63]
	v_mfma_f32_16x16x32_f16 v[56:59], v[140:143], v[162:165], v[56:59]
	v_mfma_f32_16x16x32_f16 v[48:51], v[132:135], v[182:185], v[48:51]
	v_mfma_f32_16x16x32_f16 v[40:43], v[140:143], v[182:185], v[40:43]
	v_mfma_f32_16x16x32_f16 v[32:35], v[132:135], v[190:193], v[32:35]
	v_mfma_f32_16x16x32_f16 v[24:27], v[140:143], v[190:193], v[24:27]
	v_mfma_f32_16x16x32_f16 v[16:19], v[132:135], v[198:201], v[16:19]
	v_mfma_f32_16x16x32_f16 v[8:11], v[140:143], v[198:201], v[8:11]
	s_barrier
	s_add_i32 s76, s66, s42
	s_mov_b32 m0, s76
	s_add_u32 s74, s30, 0xc000
	s_addc_u32 s75, s31, 0
	global_load_lds_dwordx4 v146, s[74:75]
	s_add_i32 m0, s76, 0x2000
	s_nop 0
	global_load_lds_dwordx4 v150, s[74:75]
	s_add_i32 s74, 0, 0x18000
	ds_read_b128 v[128:131], v254
	ds_read_b128 v[132:135], v254 offset:1024
	ds_read_b128 v[136:139], v254 offset:2048
	ds_read_b128 v[140:143], v254 offset:3072
	s_waitcnt vmcnt(6)
	s_barrier
	v_mfma_f32_16x16x32_f16 v[52:55], v[202:205], v[158:161], v[52:55]
	v_mfma_f32_16x16x32_f16 v[44:47], v[210:213], v[158:161], v[44:47]
	v_mfma_f32_16x16x32_f16 v[36:39], v[202:205], v[178:181], v[36:39]
	v_mfma_f32_16x16x32_f16 v[28:31], v[210:213], v[178:181], v[28:31]
	v_mfma_f32_16x16x32_f16 v[20:23], v[202:205], v[186:189], v[20:23]
	v_mfma_f32_16x16x32_f16 v[12:15], v[210:213], v[186:189], v[12:15]
	v_mfma_f32_16x16x32_f16 v[4:7], v[202:205], v[194:197], v[4:7]
	v_mfma_f32_16x16x32_f16 v[0:3], v[210:213], v[194:197], v[0:3]
	v_mfma_f32_16x16x32_f16 v[52:55], v[206:209], v[162:165], v[52:55]
	v_mfma_f32_16x16x32_f16 v[44:47], v[214:217], v[162:165], v[44:47]
	v_mfma_f32_16x16x32_f16 v[36:39], v[206:209], v[182:185], v[36:39]
	v_mfma_f32_16x16x32_f16 v[28:31], v[214:217], v[182:185], v[28:31]
	v_mfma_f32_16x16x32_f16 v[20:23], v[206:209], v[190:193], v[20:23]
	v_mfma_f32_16x16x32_f16 v[12:15], v[214:217], v[190:193], v[12:15]
	v_mfma_f32_16x16x32_f16 v[4:7], v[206:209], v[198:201], v[4:7]
	v_mfma_f32_16x16x32_f16 v[0:3], v[214:217], v[198:201], v[0:3]
	s_barrier
	s_add_u32 s34, s34, 0x30000
	s_addc_u32 s35, s35, 0
	s_mov_b32 m0, s45
	ds_read_b128 v[158:161], v173 offset:32768
	ds_read_b128 v[162:165], v173 offset:33792
	ds_read_b128 v[178:181], v173 offset:34816
	ds_read_b128 v[182:185], v173 offset:35840
	ds_read_b128 v[186:189], v173 offset:36864
	ds_read_b128 v[190:193], v173 offset:37888
	ds_read_b128 v[194:197], v173 offset:38912
	ds_read_b128 v[198:201], v173 offset:39936
	global_load_lds_dwordx4 v144, s[34:35]
	s_mov_b32 m0, s46
	s_nop 0
	global_load_lds_dwordx4 v148, s[34:35]
	s_waitcnt lgkmcnt(8)
	s_barrier
	s_waitcnt lgkmcnt(0)
	v_mfma_f32_16x16x32_f16 v[124:127], v[128:131], v[158:161], v[124:127]
	v_mfma_f32_16x16x32_f16 v[120:123], v[136:139], v[158:161], v[120:123]
	v_mfma_f32_16x16x32_f16 v[108:111], v[128:131], v[178:181], v[108:111]
	v_mfma_f32_16x16x32_f16 v[104:107], v[136:139], v[178:181], v[104:107]
	v_mfma_f32_16x16x32_f16 v[96:99], v[128:131], v[186:189], v[96:99]
	v_mfma_f32_16x16x32_f16 v[88:91], v[136:139], v[186:189], v[88:91]
	v_mfma_f32_16x16x32_f16 v[80:83], v[128:131], v[194:197], v[80:83]
	v_mfma_f32_16x16x32_f16 v[72:75], v[136:139], v[194:197], v[72:75]
	v_mfma_f32_16x16x32_f16 v[124:127], v[132:135], v[162:165], v[124:127]
	v_mfma_f32_16x16x32_f16 v[120:123], v[140:143], v[162:165], v[120:123]
	v_mfma_f32_16x16x32_f16 v[108:111], v[132:135], v[182:185], v[108:111]
	v_mfma_f32_16x16x32_f16 v[104:107], v[140:143], v[182:185], v[104:107]
	v_mfma_f32_16x16x32_f16 v[96:99], v[132:135], v[190:193], v[96:99]
	v_mfma_f32_16x16x32_f16 v[88:91], v[140:143], v[190:193], v[88:91]
	v_mfma_f32_16x16x32_f16 v[80:83], v[132:135], v[198:201], v[80:83]
	v_mfma_f32_16x16x32_f16 v[72:75], v[140:143], v[198:201], v[72:75]
	s_barrier
	s_add_i32 s34, 0, 0x1c000
	s_add_i32 s35, s74, s42
	s_mov_b32 m0, s35
	ds_read_b128 v[202:205], v255
	ds_read_b128 v[206:209], v255 offset:1024
	ds_read_b128 v[210:213], v255 offset:2048
	ds_read_b128 v[214:217], v255 offset:3072
	global_load_lds_dwordx4 v146, s[78:79]
	s_add_i32 m0, s35, 0x2000
	s_nop 0
	global_load_lds_dwordx4 v150, s[78:79]
	s_barrier
	s_waitcnt lgkmcnt(0)
	v_mfma_f32_16x16x32_f16 v[116:119], v[202:205], v[158:161], v[116:119]
	v_mfma_f32_16x16x32_f16 v[112:115], v[210:213], v[158:161], v[112:115]
	v_mfma_f32_16x16x32_f16 v[100:103], v[202:205], v[178:181], v[100:103]
	v_mfma_f32_16x16x32_f16 v[92:95], v[210:213], v[178:181], v[92:95]
	v_mfma_f32_16x16x32_f16 v[84:87], v[202:205], v[186:189], v[84:87]
	v_mfma_f32_16x16x32_f16 v[76:79], v[210:213], v[186:189], v[76:79]
	v_mfma_f32_16x16x32_f16 v[68:71], v[202:205], v[194:197], v[68:71]
	v_mfma_f32_16x16x32_f16 v[64:67], v[210:213], v[194:197], v[64:67]
	v_mfma_f32_16x16x32_f16 v[116:119], v[206:209], v[162:165], v[116:119]
	v_mfma_f32_16x16x32_f16 v[112:115], v[214:217], v[162:165], v[112:115]
	v_mfma_f32_16x16x32_f16 v[100:103], v[206:209], v[182:185], v[100:103]
	v_mfma_f32_16x16x32_f16 v[92:95], v[214:217], v[182:185], v[92:95]
	v_mfma_f32_16x16x32_f16 v[84:87], v[206:209], v[190:193], v[84:87]
	v_mfma_f32_16x16x32_f16 v[76:79], v[214:217], v[190:193], v[76:79]
	v_mfma_f32_16x16x32_f16 v[68:71], v[206:209], v[198:201], v[68:71]
	v_mfma_f32_16x16x32_f16 v[64:67], v[214:217], v[198:201], v[64:67]
	s_barrier
	s_mov_b32 m0, s49
	ds_read_b128 v[158:161], v173 offset:49152
	ds_read_b128 v[162:165], v173 offset:50176
	ds_read_b128 v[178:181], v173 offset:51200
	ds_read_b128 v[182:185], v173 offset:52224
	ds_read_b128 v[186:189], v173 offset:53248
	ds_read_b128 v[190:193], v173 offset:54272
	ds_read_b128 v[194:197], v173 offset:55296
	ds_read_b128 v[198:201], v173 offset:56320
	global_load_lds_dwordx4 v144, s[80:81]
	s_mov_b32 m0, s50
	s_nop 0
	global_load_lds_dwordx4 v148, s[80:81]
	s_waitcnt vmcnt(10)
	s_barrier
	s_waitcnt lgkmcnt(0)
	v_mfma_f32_16x16x32_f16 v[60:63], v[128:131], v[158:161], v[60:63]
	v_mfma_f32_16x16x32_f16 v[56:59], v[136:139], v[158:161], v[56:59]
	v_mfma_f32_16x16x32_f16 v[48:51], v[128:131], v[178:181], v[48:51]
	v_mfma_f32_16x16x32_f16 v[40:43], v[136:139], v[178:181], v[40:43]
	v_mfma_f32_16x16x32_f16 v[32:35], v[128:131], v[186:189], v[32:35]
	v_mfma_f32_16x16x32_f16 v[24:27], v[136:139], v[186:189], v[24:27]
	v_mfma_f32_16x16x32_f16 v[16:19], v[128:131], v[194:197], v[16:19]
	v_mfma_f32_16x16x32_f16 v[8:11], v[136:139], v[194:197], v[8:11]
	v_mfma_f32_16x16x32_f16 v[60:63], v[132:135], v[162:165], v[60:63]
	v_mfma_f32_16x16x32_f16 v[56:59], v[140:143], v[162:165], v[56:59]
	v_mfma_f32_16x16x32_f16 v[48:51], v[132:135], v[182:185], v[48:51]
	v_mfma_f32_16x16x32_f16 v[40:43], v[140:143], v[182:185], v[40:43]
	v_mfma_f32_16x16x32_f16 v[32:35], v[132:135], v[190:193], v[32:35]
	v_mfma_f32_16x16x32_f16 v[24:27], v[140:143], v[190:193], v[24:27]
	v_mfma_f32_16x16x32_f16 v[16:19], v[132:135], v[198:201], v[16:19]
	v_mfma_f32_16x16x32_f16 v[8:11], v[140:143], v[198:201], v[8:11]
	s_barrier
	s_add_i32 s34, s34, s42
	s_mov_b32 m0, s34
	s_add_u32 s30, s30, 0xc080
	s_addc_u32 s31, s31, 0
	global_load_lds_dwordx4 v146, s[30:31]
	s_add_i32 m0, s34, 0x2000
	s_nop 0
	global_load_lds_dwordx4 v150, s[30:31]
	ds_read_b128 v[128:131], v172
	ds_read_b128 v[132:135], v172 offset:1024
	ds_read_b128 v[136:139], v172 offset:2048
	ds_read_b128 v[140:143], v172 offset:3072
	s_waitcnt vmcnt(6)
	s_barrier
	v_mfma_f32_16x16x32_f16 v[52:55], v[202:205], v[158:161], v[52:55]
	v_mfma_f32_16x16x32_f16 v[44:47], v[210:213], v[158:161], v[44:47]
	v_mfma_f32_16x16x32_f16 v[36:39], v[202:205], v[178:181], v[36:39]
	v_mfma_f32_16x16x32_f16 v[28:31], v[210:213], v[178:181], v[28:31]
	v_mfma_f32_16x16x32_f16 v[20:23], v[202:205], v[186:189], v[20:23]
	v_mfma_f32_16x16x32_f16 v[12:15], v[210:213], v[186:189], v[12:15]
	v_mfma_f32_16x16x32_f16 v[4:7], v[202:205], v[194:197], v[4:7]
	v_mfma_f32_16x16x32_f16 v[0:3], v[210:213], v[194:197], v[0:3]
	v_mfma_f32_16x16x32_f16 v[52:55], v[206:209], v[162:165], v[52:55]
	v_mfma_f32_16x16x32_f16 v[44:47], v[214:217], v[162:165], v[44:47]
	v_mfma_f32_16x16x32_f16 v[36:39], v[206:209], v[182:185], v[36:39]
	v_mfma_f32_16x16x32_f16 v[28:31], v[214:217], v[182:185], v[28:31]
	v_mfma_f32_16x16x32_f16 v[20:23], v[206:209], v[190:193], v[20:23]
	v_mfma_f32_16x16x32_f16 v[12:15], v[214:217], v[190:193], v[12:15]
	v_mfma_f32_16x16x32_f16 v[4:7], v[206:209], v[198:201], v[4:7]
	v_mfma_f32_16x16x32_f16 v[0:3], v[214:217], v[198:201], v[0:3]
	s_barrier
	s_add_i32 s73, s73, 2
	s_add_u32 s28, s28, 0x100
	s_addc_u32 s29, s29, 0
	s_add_u32 s71, s71, 0x100
	s_addc_u32 s72, s72, 0
	s_cmp_gt_u32 s73, 9
	s_cbranch_scc0 .LBB9_27
	s_lshl_b32 s28, s70, 8
	s_add_i32 s28, s28, s48
	s_lshl_b32 s29, s68, 8
	s_or_b32 s29, s29, s51
	s_waitcnt vmcnt(6)
	v_pk_fma_f32 v[126:127], v[126:127], v[226:227], v[236:237] op_sel_hi:[1,0,1]
	v_pk_fma_f32 v[124:125], v[124:125], v[226:227], v[234:235] op_sel_hi:[1,0,1]
	v_pk_fma_f32 v[122:123], v[122:123], v[226:227], v[240:241] op_sel_hi:[1,0,1]
	v_pk_fma_f32 v[120:121], v[120:121], v[226:227], v[238:239] op_sel_hi:[1,0,1]
	v_cvt_pk_f16_f32 v124, v124, v125
	v_cvt_pk_f16_f32 v125, v126, v127
	v_cvt_pk_f16_f32 v126, v120, v121
	v_cvt_pk_f16_f32 v123, v122, v123
	v_pk_fma_f32 v[118:119], v[118:119], v[226:227], v[244:245] op_sel_hi:[1,0,1]
	v_pk_fma_f32 v[116:117], v[116:117], v[226:227], v[242:243] op_sel_hi:[1,0,1]
	v_pk_fma_f32 v[114:115], v[114:115], v[226:227], v[248:249] op_sel_hi:[1,0,1]
	v_pk_fma_f32 v[112:113], v[112:113], v[226:227], v[246:247] op_sel_hi:[1,0,1]
	v_pk_max_f16 v120, v124, 0
	v_pk_max_f16 v121, v125, 0
	v_pk_max_f16 v122, v126, 0
	v_pk_max_f16 v123, v123, 0
	v_cvt_pk_f16_f32 v116, v116, v117
	v_cvt_pk_f16_f32 v117, v118, v119
	v_cvt_pk_f16_f32 v118, v112, v113
	v_cvt_pk_f16_f32 v115, v114, v115
	v_pk_fma_f32 v[110:111], v[110:111], v[226:227], v[236:237] op_sel:[0,1,0]
	v_pk_fma_f32 v[108:109], v[108:109], v[226:227], v[234:235] op_sel:[0,1,0]
	v_pk_fma_f32 v[106:107], v[106:107], v[226:227], v[240:241] op_sel:[0,1,0]
	v_pk_fma_f32 v[104:105], v[104:105], v[226:227], v[238:239] op_sel:[0,1,0]
	v_pk_fma_f32 v[102:103], v[102:103], v[226:227], v[244:245] op_sel:[0,1,0]
	v_pk_fma_f32 v[100:101], v[100:101], v[226:227], v[242:243] op_sel:[0,1,0]
	v_pk_fma_f32 v[94:95], v[94:95], v[226:227], v[248:249] op_sel:[0,1,0]
	v_pk_fma_f32 v[92:93], v[92:93], v[226:227], v[246:247] op_sel:[0,1,0]
	ds_write_b128 v175, v[120:123]
	v_or_b32_e32 v120, s28, v169
	v_pk_max_f16 v112, v116, 0
	v_pk_max_f16 v113, v117, 0
	v_pk_max_f16 v114, v118, 0
	v_pk_max_f16 v115, v115, 0
	v_cvt_pk_f16_f32 v108, v108, v109
	v_cvt_pk_f16_f32 v109, v110, v111
	v_cvt_pk_f16_f32 v110, v104, v105
	v_cvt_pk_f16_f32 v107, v106, v107
	v_cvt_pk_f16_f32 v100, v100, v101
	v_cvt_pk_f16_f32 v101, v102, v103
	v_cvt_pk_f16_f32 v102, v92, v93
	v_cvt_pk_f16_f32 v95, v94, v95
	ds_write_b128 v175, v[112:115] offset:64
	v_mul_lo_u32 v116, v120, s10
	v_pk_max_f16 v104, v108, 0
	v_pk_max_f16 v105, v109, 0
	v_pk_max_f16 v106, v110, 0
	v_pk_max_f16 v107, v107, 0
	v_pk_max_f16 v92, v100, 0
	v_pk_max_f16 v93, v101, 0
	v_pk_max_f16 v94, v102, 0
	v_pk_max_f16 v95, v95, 0
	ds_read_b128 v[112:115], v176
	v_add_u32_e32 v120, s29, v116
	ds_read_b128 v[116:119], v176 offset:1152
	ds_write_b128 v175, v[104:107]
	ds_write_b128 v175, v[92:95] offset:64
	ds_read_b128 v[92:95], v176
	ds_read_b128 v[100:103], v176 offset:1152
	v_lshlrev_b32_e32 v121, 1, v120
	v_add_u32_e32 v122, v121, v170
	v_add_u32_e32 v104, s55, v121
	s_waitcnt lgkmcnt(0)
	buffer_store_dwordx4 v[112:115], v122, s[20:23], 0 offen nt
	v_add_u32_e32 v105, v104, v170
	v_pk_fma_f32 v[90:91], v[90:91], v[228:229], v[240:241] op_sel_hi:[1,0,1]
	v_add_u32_e32 v112, v121, v171
	buffer_store_dwordx4 v[116:119], v112, s[20:23], 0 offen nt
	buffer_store_dwordx4 v[92:95], v105, s[20:23], 0 offen nt
	v_pk_fma_f32 v[88:89], v[88:89], v[228:229], v[238:239] op_sel_hi:[1,0,1]
	v_pk_fma_f32 v[86:87], v[86:87], v[228:229], v[244:245] op_sel_hi:[1,0,1]
	v_pk_fma_f32 v[92:93], v[98:99], v[228:229], v[236:237] op_sel_hi:[1,0,1]
	v_pk_fma_f32 v[94:95], v[96:97], v[228:229], v[234:235] op_sel_hi:[1,0,1]
	v_pk_fma_f32 v[84:85], v[84:85], v[228:229], v[242:243] op_sel_hi:[1,0,1]
	v_pk_fma_f32 v[78:79], v[78:79], v[228:229], v[248:249] op_sel_hi:[1,0,1]
	v_pk_fma_f32 v[76:77], v[76:77], v[228:229], v[246:247] op_sel_hi:[1,0,1]
	v_cvt_pk_f16_f32 v94, v94, v95
	v_cvt_pk_f16_f32 v92, v92, v93
	v_cvt_pk_f16_f32 v93, v88, v89
	v_cvt_pk_f16_f32 v91, v90, v91
	v_cvt_pk_f16_f32 v84, v84, v85
	v_cvt_pk_f16_f32 v85, v86, v87
	v_cvt_pk_f16_f32 v86, v76, v77
	v_cvt_pk_f16_f32 v79, v78, v79
	v_pk_max_f16 v88, v94, 0
	v_pk_max_f16 v89, v92, 0
	v_pk_max_f16 v90, v93, 0
	v_pk_max_f16 v91, v91, 0
	v_pk_max_f16 v76, v84, 0
	v_pk_max_f16 v77, v85, 0
	v_pk_max_f16 v78, v86, 0
	v_pk_max_f16 v79, v79, 0
	ds_write_b128 v175, v[88:91]
	ds_write_b128 v175, v[76:79] offset:64
	ds_read_b128 v[76:79], v176
	ds_read_b128 v[84:87], v176 offset:1152
	v_add_u32_e32 v88, s55, v104
	v_add_u32_e32 v105, v104, v171
	v_add_u32_e32 v89, v88, v170
	buffer_store_dwordx4 v[100:103], v105, s[20:23], 0 offen nt
	s_waitcnt lgkmcnt(1)
	buffer_store_dwordx4 v[76:79], v89, s[20:23], 0 offen nt
	v_pk_fma_f32 v[74:75], v[74:75], v[228:229], v[240:241] op_sel:[0,1,0]
	v_pk_fma_f32 v[72:73], v[72:73], v[228:229], v[238:239] op_sel:[0,1,0]
	v_add_u32_e32 v76, v88, v171
	s_waitcnt lgkmcnt(0)
	buffer_store_dwordx4 v[84:87], v76, s[20:23], 0 offen nt
	v_pk_fma_f32 v[76:77], v[82:83], v[228:229], v[236:237] op_sel:[0,1,0]
	v_pk_fma_f32 v[78:79], v[80:81], v[228:229], v[234:235] op_sel:[0,1,0]
	v_pk_fma_f32 v[70:71], v[70:71], v[228:229], v[244:245] op_sel:[0,1,0]
	v_pk_fma_f32 v[68:69], v[68:69], v[228:229], v[242:243] op_sel:[0,1,0]
	v_pk_fma_f32 v[66:67], v[66:67], v[228:229], v[248:249] op_sel:[0,1,0]
	v_pk_fma_f32 v[64:65], v[64:65], v[228:229], v[246:247] op_sel:[0,1,0]
	v_cvt_pk_f16_f32 v78, v78, v79
	v_cvt_pk_f16_f32 v76, v76, v77
	v_cvt_pk_f16_f32 v77, v72, v73
	v_cvt_pk_f16_f32 v75, v74, v75
	v_cvt_pk_f16_f32 v68, v68, v69
	v_cvt_pk_f16_f32 v69, v70, v71
	v_cvt_pk_f16_f32 v70, v64, v65
	v_cvt_pk_f16_f32 v67, v66, v67
	v_pk_fma_f32 v[62:63], v[62:63], v[230:231], v[236:237] op_sel_hi:[1,0,1]
	v_pk_fma_f32 v[60:61], v[60:61], v[230:231], v[234:235] op_sel_hi:[1,0,1]
	v_pk_fma_f32 v[58:59], v[58:59], v[230:231], v[240:241] op_sel_hi:[1,0,1]
	v_pk_fma_f32 v[56:57], v[56:57], v[230:231], v[238:239] op_sel_hi:[1,0,1]
	v_pk_fma_f32 v[54:55], v[54:55], v[230:231], v[244:245] op_sel_hi:[1,0,1]
	v_pk_fma_f32 v[52:53], v[52:53], v[230:231], v[242:243] op_sel_hi:[1,0,1]
	v_pk_fma_f32 v[46:47], v[46:47], v[230:231], v[248:249] op_sel_hi:[1,0,1]
	v_pk_fma_f32 v[44:45], v[44:45], v[230:231], v[246:247] op_sel_hi:[1,0,1]
	v_pk_max_f16 v72, v78, 0
	v_pk_max_f16 v73, v76, 0
	v_pk_max_f16 v74, v77, 0
	v_pk_max_f16 v75, v75, 0
	v_pk_max_f16 v64, v68, 0
	v_pk_max_f16 v65, v69, 0
	v_pk_max_f16 v66, v70, 0
	v_pk_max_f16 v67, v67, 0
	v_cvt_pk_f16_f32 v60, v60, v61
	v_cvt_pk_f16_f32 v61, v62, v63
	v_cvt_pk_f16_f32 v62, v56, v57
	v_cvt_pk_f16_f32 v59, v58, v59
	v_cvt_pk_f16_f32 v52, v52, v53
	v_cvt_pk_f16_f32 v53, v54, v55
	v_cvt_pk_f16_f32 v54, v44, v45
	v_cvt_pk_f16_f32 v47, v46, v47
	ds_write_b128 v175, v[72:75]
	ds_write_b128 v175, v[64:67] offset:64
	v_pk_max_f16 v56, v60, 0
	v_pk_max_f16 v57, v61, 0
	v_pk_max_f16 v58, v62, 0
	v_pk_max_f16 v59, v59, 0
	v_pk_max_f16 v44, v52, 0
	v_pk_max_f16 v45, v53, 0
	v_pk_max_f16 v46, v54, 0
	v_pk_max_f16 v47, v47, 0
	ds_read_b128 v[64:67], v176
	ds_read_b128 v[68:71], v176 offset:1152
	ds_write_b128 v175, v[56:59]
	ds_write_b128 v175, v[44:47] offset:64
	ds_read_b128 v[44:47], v176
	ds_read_b128 v[52:55], v176 offset:1152
	v_add_u32_e32 v72, s56, v120
	v_lshlrev_b32_e32 v73, 1, v72
	v_add_u32_e32 v74, v73, v170
	v_add_u32_e32 v56, s62, v88
	s_waitcnt lgkmcnt(5)
	buffer_store_dwordx4 v[64:67], v74, s[20:23], 0 offen nt
	v_add_u32_e32 v57, v56, v170
	v_pk_fma_f32 v[42:43], v[42:43], v[230:231], v[240:241] op_sel:[0,1,0]
	v_add_u32_e32 v64, v73, v171
	s_waitcnt lgkmcnt(4)
	buffer_store_dwordx4 v[68:71], v64, s[20:23], 0 offen nt
	s_waitcnt lgkmcnt(1)
	buffer_store_dwordx4 v[44:47], v57, s[20:23], 0 offen nt
	v_pk_fma_f32 v[40:41], v[40:41], v[230:231], v[238:239] op_sel:[0,1,0]
	v_pk_fma_f32 v[38:39], v[38:39], v[230:231], v[244:245] op_sel:[0,1,0]
	v_add_u32_e32 v44, v56, v171
	s_waitcnt lgkmcnt(0)
	buffer_store_dwordx4 v[52:55], v44, s[20:23], 0 offen nt
	v_pk_fma_f32 v[44:45], v[50:51], v[230:231], v[236:237] op_sel:[0,1,0]
	v_pk_fma_f32 v[46:47], v[48:49], v[230:231], v[234:235] op_sel:[0,1,0]
	v_pk_fma_f32 v[36:37], v[36:37], v[230:231], v[242:243] op_sel:[0,1,0]
	v_pk_fma_f32 v[30:31], v[30:31], v[230:231], v[248:249] op_sel:[0,1,0]
	v_pk_fma_f32 v[28:29], v[28:29], v[230:231], v[246:247] op_sel:[0,1,0]
	v_cvt_pk_f16_f32 v46, v46, v47
	v_cvt_pk_f16_f32 v44, v44, v45
	v_cvt_pk_f16_f32 v45, v40, v41
	v_cvt_pk_f16_f32 v43, v42, v43
	v_cvt_pk_f16_f32 v36, v36, v37
	v_cvt_pk_f16_f32 v37, v38, v39
	v_cvt_pk_f16_f32 v38, v28, v29
	v_cvt_pk_f16_f32 v31, v30, v31
	v_pk_max_f16 v40, v46, 0
	v_pk_max_f16 v41, v44, 0
	v_pk_max_f16 v42, v45, 0
	v_pk_max_f16 v43, v43, 0
	v_pk_max_f16 v28, v36, 0
	v_pk_max_f16 v29, v37, 0
	v_pk_max_f16 v30, v38, 0
	v_pk_max_f16 v31, v31, 0
	ds_write_b128 v175, v[40:43]
	ds_write_b128 v175, v[28:31] offset:64
	ds_read_b128 v[28:31], v176
	ds_read_b128 v[36:39], v176 offset:1152
	v_add_u32_e32 v40, s63, v72
	v_lshlrev_b32_e32 v41, 1, v40
	v_add_u32_e32 v42, v41, v170
	s_waitcnt lgkmcnt(1)
	buffer_store_dwordx4 v[28:31], v42, s[20:23], 0 offen nt
	v_pk_fma_f32 v[26:27], v[26:27], v[232:233], v[240:241] op_sel_hi:[1,0,1]
	v_pk_fma_f32 v[24:25], v[24:25], v[232:233], v[238:239] op_sel_hi:[1,0,1]
	v_add_u32_e32 v28, v41, v171
	s_waitcnt lgkmcnt(0)
	buffer_store_dwordx4 v[36:39], v28, s[20:23], 0 offen nt
	v_pk_fma_f32 v[28:29], v[34:35], v[232:233], v[236:237] op_sel_hi:[1,0,1]
	v_pk_fma_f32 v[30:31], v[32:33], v[232:233], v[234:235] op_sel_hi:[1,0,1]
	v_pk_fma_f32 v[22:23], v[22:23], v[232:233], v[244:245] op_sel_hi:[1,0,1]
	v_pk_fma_f32 v[20:21], v[20:21], v[232:233], v[242:243] op_sel_hi:[1,0,1]
	v_pk_fma_f32 v[14:15], v[14:15], v[232:233], v[248:249] op_sel_hi:[1,0,1]
	v_pk_fma_f32 v[12:13], v[12:13], v[232:233], v[246:247] op_sel_hi:[1,0,1]
	v_cvt_pk_f16_f32 v30, v30, v31
	v_cvt_pk_f16_f32 v28, v28, v29
	v_cvt_pk_f16_f32 v29, v24, v25
	v_cvt_pk_f16_f32 v27, v26, v27
	v_cvt_pk_f16_f32 v20, v20, v21
	v_cvt_pk_f16_f32 v21, v22, v23
	v_cvt_pk_f16_f32 v22, v12, v13
	v_cvt_pk_f16_f32 v15, v14, v15
	v_pk_max_f16 v24, v30, 0
	v_pk_max_f16 v25, v28, 0
	v_pk_max_f16 v26, v29, 0
	v_pk_max_f16 v27, v27, 0
	v_pk_max_f16 v12, v20, 0
	v_pk_max_f16 v13, v21, 0
	v_pk_max_f16 v14, v22, 0
	v_pk_max_f16 v15, v15, 0
	ds_write_b128 v175, v[24:27]
	ds_write_b128 v175, v[12:15] offset:64
	ds_read_b128 v[12:15], v176
	ds_read_b128 v[20:23], v176 offset:1152
	v_add_u32_e32 v24, s64, v40
	v_lshlrev_b32_e32 v25, 1, v24
	v_add_u32_e32 v26, v25, v170
	s_waitcnt lgkmcnt(1)
	buffer_store_dwordx4 v[12:15], v26, s[20:23], 0 offen nt
	v_pk_fma_f32 v[10:11], v[10:11], v[232:233], v[240:241] op_sel:[0,1,0]
	v_pk_fma_f32 v[8:9], v[8:9], v[232:233], v[238:239] op_sel:[0,1,0]
	v_pk_fma_f32 v[12:13], v[18:19], v[232:233], v[236:237] op_sel:[0,1,0]
	v_pk_fma_f32 v[14:15], v[16:17], v[232:233], v[234:235] op_sel:[0,1,0]
	v_pk_fma_f32 v[6:7], v[6:7], v[232:233], v[244:245] op_sel:[0,1,0]
	v_pk_fma_f32 v[4:5], v[4:5], v[232:233], v[242:243] op_sel:[0,1,0]
	v_pk_fma_f32 v[2:3], v[2:3], v[232:233], v[248:249] op_sel:[0,1,0]
	v_pk_fma_f32 v[0:1], v[0:1], v[232:233], v[246:247] op_sel:[0,1,0]
	v_cvt_pk_f16_f32 v14, v14, v15
	v_cvt_pk_f16_f32 v12, v12, v13
	v_cvt_pk_f16_f32 v13, v8, v9
	v_cvt_pk_f16_f32 v11, v10, v11
	v_cvt_pk_f16_f32 v4, v4, v5
	v_cvt_pk_f16_f32 v5, v6, v7
	v_cvt_pk_f16_f32 v6, v0, v1
	v_cvt_pk_f16_f32 v3, v2, v3
	v_pk_max_f16 v8, v14, 0
	v_pk_max_f16 v9, v12, 0
	v_pk_max_f16 v10, v13, 0
	v_pk_max_f16 v11, v11, 0
	v_pk_max_f16 v0, v4, 0
	v_pk_max_f16 v1, v5, 0
	v_pk_max_f16 v2, v6, 0
	v_pk_max_f16 v3, v3, 0
	ds_write_b128 v175, v[8:11]
	ds_write_b128 v175, v[0:3] offset:64
	ds_read_b128 v[0:3], v176
	ds_read_b128 v[4:7], v176 offset:1152
	v_add_lshl_u32 v8, v24, s64, 1
	v_add_u32_e32 v25, v25, v171
	v_add_u32_e32 v9, v8, v170
	s_waitcnt lgkmcnt(4)
	buffer_store_dwordx4 v[20:23], v25, s[20:23], 0 offen nt
	s_waitcnt lgkmcnt(1)
	buffer_store_dwordx4 v[0:3], v9, s[20:23], 0 offen nt
	s_mov_b32 s68, s67
	s_mov_b32 s70, s69
	v_add_u32_e32 v0, v8, v171
	s_mov_b64 s[30:31], s[0:1]
	s_mov_b64 s[28:29], s[8:9]
	s_mov_b64 vcc, s[6:7]
	s_waitcnt lgkmcnt(0)
	buffer_store_dwordx4 v[4:7], v0, s[20:23], 0 offen nt
	s_cbranch_vccz .LBB9_12
	s_waitcnt vmcnt(0)
	s_cmpk_gt_u32 s36, 0xff
	s_cbranch_scc1 .LBB9_31
	s_barrier

	.amdhsa_kernel _Z6k_gemmIN2pg6EpiLinILi1EEELi768EEvNS0_4GemmET_
		.amdhsa_group_segment_fixed_size 0
		.amdhsa_private_segment_fixed_size 0
		.amdhsa_kernarg_size 320
		.amdhsa_user_sgpr_count 2
		.amdhsa_user_sgpr_dispatch_ptr 0
		.amdhsa_user_sgpr_queue_ptr 0
		.amdhsa_user_sgpr_kernarg_segment_ptr 1
		.amdhsa_user_sgpr_dispatch_id 0
		.amdhsa_user_sgpr_kernarg_preload_length 0
		.amdhsa_user_sgpr_kernarg_preload_offset 0
		.amdhsa_user_sgpr_private_segment_size 0
		.amdhsa_uses_dynamic_stack 0
		.amdhsa_enable_private_segment 0
		.amdhsa_system_sgpr_workgroup_id_x 1
		.amdhsa_system_sgpr_workgroup_id_y 0
		.amdhsa_system_sgpr_workgroup_id_z 0
		.amdhsa_system_sgpr_workgroup_info 0
		.amdhsa_system_vgpr_workitem_id 0
		.amdhsa_next_free_vgpr 256
		.amdhsa_next_free_sgpr 82
		.amdhsa_accum_offset 256
		.amdhsa_reserve_vcc 1
		.amdhsa_float_round_mode_32 0
		.amdhsa_float_round_mode_16_64 0
		.amdhsa_float_denorm_mode_32 3
		.amdhsa_float_denorm_mode_16_64 3
		.amdhsa_dx10_clamp 1
		.amdhsa_ieee_mode 1
		.amdhsa_fp16_overflow 0
		.amdhsa_tg_split 0
		.amdhsa_exception_fp_ieee_invalid_op 0
		.amdhsa_exception_fp_denorm_src 0
		.amdhsa_exception_fp_ieee_div_zero 0
		.amdhsa_exception_fp_ieee_overflow 0
		.amdhsa_exception_fp_ieee_underflow 0
		.amdhsa_exception_fp_ieee_inexact 0
		.amdhsa_exception_int_div_zero 0
	.end_amdhsa_kernel

.LBB10_26:
	v_add_u32_e32 v254, 0x18000, v228
	v_add_u32_e32 v255, 0x1c000, v228
	s_add_u32 s38, s38, 0xc0080
	s_addc_u32 s39, s39, 0
	s_add_u32 s85, s40, 0x100
	v_mov_b32_e32 v0, 0
	s_addc_u32 s86, s41, 0
	s_mov_b32 s87, -2
	v_mov_b32_e32 v1, v0
	v_mov_b32_e32 v2, v0
	v_mov_b32_e32 v3, v0
	v_mov_b32_e32 v4, v0
	v_mov_b32_e32 v5, v0
	v_mov_b32_e32 v6, v0
	v_mov_b32_e32 v7, v0
	v_mov_b32_e32 v16, v0
	v_mov_b32_e32 v17, v0
	v_mov_b32_e32 v18, v0
	v_mov_b32_e32 v19, v0
	v_mov_b32_e32 v20, v0
	v_mov_b32_e32 v21, v0
	v_mov_b32_e32 v22, v0
	v_mov_b32_e32 v23, v0
	v_mov_b32_e32 v32, v0
	v_mov_b32_e32 v33, v0
	v_mov_b32_e32 v34, v0
	v_mov_b32_e32 v35, v0
	v_mov_b32_e32 v36, v0
	v_mov_b32_e32 v37, v0
	v_mov_b32_e32 v38, v0
	v_mov_b32_e32 v39, v0
	v_mov_b32_e32 v48, v0
	v_mov_b32_e32 v49, v0
	v_mov_b32_e32 v50, v0
	v_mov_b32_e32 v51, v0
	v_mov_b32_e32 v52, v0
	v_mov_b32_e32 v53, v0
	v_mov_b32_e32 v54, v0
	v_mov_b32_e32 v55, v0
	v_mov_b32_e32 v8, v0
	v_mov_b32_e32 v9, v0
	v_mov_b32_e32 v10, v0
	v_mov_b32_e32 v11, v0
	v_mov_b32_e32 v12, v0
	v_mov_b32_e32 v13, v0
	v_mov_b32_e32 v14, v0
	v_mov_b32_e32 v15, v0
	v_mov_b32_e32 v24, v0
	v_mov_b32_e32 v25, v0
	v_mov_b32_e32 v26, v0
	v_mov_b32_e32 v27, v0
	v_mov_b32_e32 v28, v0
	v_mov_b32_e32 v29, v0
	v_mov_b32_e32 v30, v0
	v_mov_b32_e32 v31, v0
	v_mov_b32_e32 v40, v0
	v_mov_b32_e32 v41, v0
	v_mov_b32_e32 v42, v0
	v_mov_b32_e32 v43, v0
	v_mov_b32_e32 v44, v0
	v_mov_b32_e32 v45, v0
	v_mov_b32_e32 v46, v0
	v_mov_b32_e32 v47, v0
	v_mov_b32_e32 v56, v0
	v_mov_b32_e32 v57, v0
	v_mov_b32_e32 v58, v0
	v_mov_b32_e32 v59, v0
	v_mov_b32_e32 v60, v0
	v_mov_b32_e32 v61, v0
	v_mov_b32_e32 v62, v0
	v_mov_b32_e32 v63, v0
	v_mov_b32_e32 v64, v0
	v_mov_b32_e32 v65, v0
	v_mov_b32_e32 v66, v0
	v_mov_b32_e32 v67, v0
	v_mov_b32_e32 v68, v0
	v_mov_b32_e32 v69, v0
	v_mov_b32_e32 v70, v0
	v_mov_b32_e32 v71, v0
	v_mov_b32_e32 v96, v0
	v_mov_b32_e32 v97, v0
	v_mov_b32_e32 v98, v0
	v_mov_b32_e32 v99, v0
	v_mov_b32_e32 v100, v0
	v_mov_b32_e32 v101, v0
	v_mov_b32_e32 v102, v0
	v_mov_b32_e32 v103, v0
	v_mov_b32_e32 v112, v0
	v_mov_b32_e32 v113, v0
	v_mov_b32_e32 v114, v0
	v_mov_b32_e32 v115, v0
	v_mov_b32_e32 v116, v0
	v_mov_b32_e32 v117, v0
	v_mov_b32_e32 v118, v0
	v_mov_b32_e32 v119, v0
	v_mov_b32_e32 v128, v0
	v_mov_b32_e32 v129, v0
	v_mov_b32_e32 v130, v0
	v_mov_b32_e32 v131, v0
	v_mov_b32_e32 v132, v0
	v_mov_b32_e32 v133, v0
	v_mov_b32_e32 v134, v0
	v_mov_b32_e32 v135, v0
	v_mov_b32_e32 v76, v0
	v_mov_b32_e32 v77, v0
	v_mov_b32_e32 v78, v0
	v_mov_b32_e32 v79, v0
	v_mov_b32_e32 v84, v0
	v_mov_b32_e32 v85, v0
	v_mov_b32_e32 v86, v0
	v_mov_b32_e32 v87, v0
	v_mov_b32_e32 v104, v0
	v_mov_b32_e32 v105, v0
	v_mov_b32_e32 v106, v0
	v_mov_b32_e32 v107, v0
	v_mov_b32_e32 v108, v0
	v_mov_b32_e32 v109, v0
	v_mov_b32_e32 v110, v0
	v_mov_b32_e32 v111, v0
	v_mov_b32_e32 v120, v0
	v_mov_b32_e32 v121, v0
	v_mov_b32_e32 v122, v0
	v_mov_b32_e32 v123, v0
	v_mov_b32_e32 v124, v0
	v_mov_b32_e32 v125, v0
	v_mov_b32_e32 v126, v0
	v_mov_b32_e32 v127, v0
	v_mov_b32_e32 v140, v0
	v_mov_b32_e32 v141, v0
	v_mov_b32_e32 v142, v0
	v_mov_b32_e32 v143, v0
	v_mov_b32_e32 v144, v0
	v_mov_b32_e32 v145, v0
	v_mov_b32_e32 v146, v0
	v_mov_b32_e32 v147, v0
	ds_read_b128 v[72:75], v231
	ds_read_b128 v[80:83], v231 offset:1024
	ds_read_b128 v[88:91], v231 offset:2048
	ds_read_b128 v[92:95], v231 offset:3072
.LBB10_27:
	s_add_u32 s40, s38, 0xfff40080
	s_addc_u32 s41, s39, -1
	s_cmp_eq_u32 s87, 44
	s_cselect_b32 s43, s9, s41
	s_cselect_b32 s42, s8, s40
	s_cselect_b32 s41, s1, s86
	s_cselect_b32 s40, s0, s85
	s_add_i32 m0, s51, 0xc000
	ds_read_b128 v[136:139], v232
	ds_read_b128 v[148:151], v232 offset:1024
	ds_read_b128 v[152:155], v232 offset:2048
	ds_read_b128 v[156:159], v232 offset:3072
	ds_read_b128 v[160:163], v232 offset:4096
	ds_read_b128 v[164:167], v232 offset:5120
	ds_read_b128 v[168:171], v232 offset:6144
	ds_read_b128 v[172:175], v232 offset:7168
	global_load_lds_dwordx4 v184, s[38:39]
	s_add_i32 m0, s51, 0xe000
	s_nop 0
	global_load_lds_dwordx4 v186, s[38:39]
	s_waitcnt lgkmcnt(8)
	s_barrier
	s_waitcnt lgkmcnt(0)
	v_mfma_f32_16x16x32_f16 v[144:147], v[72:75], v[136:139], v[144:147]
	v_mfma_f32_16x16x32_f16 v[140:143], v[88:91], v[136:139], v[140:143]
	v_mfma_f32_16x16x32_f16 v[124:127], v[72:75], v[152:155], v[124:127]
	v_mfma_f32_16x16x32_f16 v[120:123], v[88:91], v[152:155], v[120:123]
	v_mfma_f32_16x16x32_f16 v[108:111], v[72:75], v[160:163], v[108:111]
	v_mfma_f32_16x16x32_f16 v[104:107], v[88:91], v[160:163], v[104:107]
	v_mfma_f32_16x16x32_f16 v[84:87], v[72:75], v[168:171], v[84:87]
	v_mfma_f32_16x16x32_f16 v[76:79], v[88:91], v[168:171], v[76:79]
	v_mfma_f32_16x16x32_f16 v[144:147], v[80:83], v[148:151], v[144:147]
	v_mfma_f32_16x16x32_f16 v[140:143], v[92:95], v[148:151], v[140:143]
	v_mfma_f32_16x16x32_f16 v[124:127], v[80:83], v[156:159], v[124:127]
	v_mfma_f32_16x16x32_f16 v[120:123], v[92:95], v[156:159], v[120:123]
	v_mfma_f32_16x16x32_f16 v[108:111], v[80:83], v[164:167], v[108:111]
	v_mfma_f32_16x16x32_f16 v[104:107], v[92:95], v[164:167], v[104:107]
	v_mfma_f32_16x16x32_f16 v[84:87], v[80:83], v[172:175], v[84:87]
	v_mfma_f32_16x16x32_f16 v[76:79], v[92:95], v[172:175], v[76:79]
	s_barrier
	s_add_i32 s88, s69, s50
	s_mov_b32 m0, s88
	ds_read_b128 v[190:193], v233
	ds_read_b128 v[194:197], v233 offset:1024
	ds_read_b128 v[198:201], v233 offset:2048
	ds_read_b128 v[202:205], v233 offset:3072
	global_load_lds_dwordx4 v178, s[40:41]
	s_add_i32 m0, s88, 0x2000
	s_add_u32 s92, s40, 0x80
	s_addc_u32 s93, s41, 0
	global_load_lds_dwordx4 v182, s[40:41]
	s_barrier
	s_waitcnt lgkmcnt(0)
	v_mfma_f32_16x16x32_f16 v[132:135], v[190:193], v[136:139], v[132:135]
	v_mfma_f32_16x16x32_f16 v[128:131], v[198:201], v[136:139], v[128:131]
	v_mfma_f32_16x16x32_f16 v[116:119], v[190:193], v[152:155], v[116:119]
	v_mfma_f32_16x16x32_f16 v[112:115], v[198:201], v[152:155], v[112:115]
	v_mfma_f32_16x16x32_f16 v[100:103], v[190:193], v[160:163], v[100:103]
	v_mfma_f32_16x16x32_f16 v[96:99], v[198:201], v[160:163], v[96:99]
	v_mfma_f32_16x16x32_f16 v[68:71], v[190:193], v[168:171], v[68:71]
	v_mfma_f32_16x16x32_f16 v[64:67], v[198:201], v[168:171], v[64:67]
	v_mfma_f32_16x16x32_f16 v[132:135], v[194:197], v[148:151], v[132:135]
	v_mfma_f32_16x16x32_f16 v[128:131], v[202:205], v[148:151], v[128:131]
	v_mfma_f32_16x16x32_f16 v[116:119], v[194:197], v[156:159], v[116:119]
	v_mfma_f32_16x16x32_f16 v[112:115], v[202:205], v[156:159], v[112:115]
	v_mfma_f32_16x16x32_f16 v[100:103], v[194:197], v[164:167], v[100:103]
	v_mfma_f32_16x16x32_f16 v[96:99], v[202:205], v[164:167], v[96:99]
	v_mfma_f32_16x16x32_f16 v[68:71], v[194:197], v[172:175], v[68:71]
	v_mfma_f32_16x16x32_f16 v[64:67], v[202:205], v[172:175], v[64:67]
	s_barrier
	s_mov_b32 m0, s51
	ds_read_b128 v[136:139], v232 offset:16384
	ds_read_b128 v[148:151], v232 offset:17408
	ds_read_b128 v[152:155], v232 offset:18432
	ds_read_b128 v[156:159], v232 offset:19456
	ds_read_b128 v[160:163], v232 offset:20480
	ds_read_b128 v[164:167], v232 offset:21504
	ds_read_b128 v[168:171], v232 offset:22528
	ds_read_b128 v[172:175], v232 offset:23552
	global_load_lds_dwordx4 v176, s[42:43]
	s_mov_b32 m0, s52
	s_add_u32 s94, s42, 0x80
	s_addc_u32 s95, s43, 0
	global_load_lds_dwordx4 v180, s[42:43]
	s_waitcnt vmcnt(10)
	s_barrier
	s_waitcnt lgkmcnt(0)
	v_mfma_f32_16x16x32_f16 v[60:63], v[72:75], v[136:139], v[60:63]
	v_mfma_f32_16x16x32_f16 v[56:59], v[88:91], v[136:139], v[56:59]
	v_mfma_f32_16x16x32_f16 v[44:47], v[72:75], v[152:155], v[44:47]
	v_mfma_f32_16x16x32_f16 v[40:43], v[88:91], v[152:155], v[40:43]
	v_mfma_f32_16x16x32_f16 v[28:31], v[72:75], v[160:163], v[28:31]
	v_mfma_f32_16x16x32_f16 v[24:27], v[88:91], v[160:163], v[24:27]
	v_mfma_f32_16x16x32_f16 v[12:15], v[72:75], v[168:171], v[12:15]
	v_mfma_f32_16x16x32_f16 v[8:11], v[88:91], v[168:171], v[8:11]
	v_mfma_f32_16x16x32_f16 v[60:63], v[80:83], v[148:151], v[60:63]
	v_mfma_f32_16x16x32_f16 v[56:59], v[92:95], v[148:151], v[56:59]
	v_mfma_f32_16x16x32_f16 v[44:47], v[80:83], v[156:159], v[44:47]
	v_mfma_f32_16x16x32_f16 v[40:43], v[92:95], v[156:159], v[40:43]
	v_mfma_f32_16x16x32_f16 v[28:31], v[80:83], v[164:167], v[28:31]
	v_mfma_f32_16x16x32_f16 v[24:27], v[92:95], v[164:167], v[24:27]
	v_mfma_f32_16x16x32_f16 v[12:15], v[80:83], v[172:175], v[12:15]
	v_mfma_f32_16x16x32_f16 v[8:11], v[92:95], v[172:175], v[8:11]
	s_barrier
	s_add_i32 s90, s70, s50
	s_mov_b32 m0, s90
	s_add_u32 s88, s40, 0x30000
	s_addc_u32 s89, s41, 0
	global_load_lds_dwordx4 v178, s[88:89]
	s_add_i32 m0, s90, 0x2000
	s_nop 0
	global_load_lds_dwordx4 v182, s[88:89]
	s_add_i32 s88, 0, 0x18000
	ds_read_b128 v[72:75], v254
	ds_read_b128 v[80:83], v254 offset:1024
	ds_read_b128 v[88:91], v254 offset:2048
	ds_read_b128 v[92:95], v254 offset:3072
	s_waitcnt vmcnt(6)
	s_barrier
	v_mfma_f32_16x16x32_f16 v[52:55], v[190:193], v[136:139], v[52:55]
	v_mfma_f32_16x16x32_f16 v[48:51], v[198:201], v[136:139], v[48:51]
	v_mfma_f32_16x16x32_f16 v[36:39], v[190:193], v[152:155], v[36:39]
	v_mfma_f32_16x16x32_f16 v[32:35], v[198:201], v[152:155], v[32:35]
	v_mfma_f32_16x16x32_f16 v[20:23], v[190:193], v[160:163], v[20:23]
	v_mfma_f32_16x16x32_f16 v[16:19], v[198:201], v[160:163], v[16:19]
	v_mfma_f32_16x16x32_f16 v[4:7], v[190:193], v[168:171], v[4:7]
	v_mfma_f32_16x16x32_f16 v[0:3], v[198:201], v[168:171], v[0:3]
	v_mfma_f32_16x16x32_f16 v[52:55], v[194:197], v[148:151], v[52:55]
	v_mfma_f32_16x16x32_f16 v[48:51], v[202:205], v[148:151], v[48:51]
	v_mfma_f32_16x16x32_f16 v[36:39], v[194:197], v[156:159], v[36:39]
	v_mfma_f32_16x16x32_f16 v[32:35], v[202:205], v[156:159], v[32:35]
	v_mfma_f32_16x16x32_f16 v[20:23], v[194:197], v[164:167], v[20:23]
	v_mfma_f32_16x16x32_f16 v[16:19], v[202:205], v[164:167], v[16:19]
	v_mfma_f32_16x16x32_f16 v[4:7], v[194:197], v[172:175], v[4:7]
	v_mfma_f32_16x16x32_f16 v[0:3], v[202:205], v[172:175], v[0:3]
	s_barrier
	s_add_u32 s42, s42, 0xc0000
	s_addc_u32 s43, s43, 0
	s_mov_b32 m0, s53
	ds_read_b128 v[136:139], v232 offset:32768
	ds_read_b128 v[148:151], v232 offset:33792
	ds_read_b128 v[152:155], v232 offset:34816
	ds_read_b128 v[156:159], v232 offset:35840
	ds_read_b128 v[160:163], v232 offset:36864
	ds_read_b128 v[164:167], v232 offset:37888
	ds_read_b128 v[168:171], v232 offset:38912
	ds_read_b128 v[172:175], v232 offset:39936
	global_load_lds_dwordx4 v176, s[42:43]
	s_mov_b32 m0, s54
	s_nop 0
	global_load_lds_dwordx4 v180, s[42:43]
	s_waitcnt lgkmcnt(8)
	s_barrier
	s_waitcnt lgkmcnt(0)
	v_mfma_f32_16x16x32_f16 v[144:147], v[72:75], v[136:139], v[144:147]
	v_mfma_f32_16x16x32_f16 v[140:143], v[88:91], v[136:139], v[140:143]
	v_mfma_f32_16x16x32_f16 v[124:127], v[72:75], v[152:155], v[124:127]
	v_mfma_f32_16x16x32_f16 v[120:123], v[88:91], v[152:155], v[120:123]
	v_mfma_f32_16x16x32_f16 v[108:111], v[72:75], v[160:163], v[108:111]
	v_mfma_f32_16x16x32_f16 v[104:107], v[88:91], v[160:163], v[104:107]
	v_mfma_f32_16x16x32_f16 v[84:87], v[72:75], v[168:171], v[84:87]
	v_mfma_f32_16x16x32_f16 v[76:79], v[88:91], v[168:171], v[76:79]
	v_mfma_f32_16x16x32_f16 v[144:147], v[80:83], v[148:151], v[144:147]
	v_mfma_f32_16x16x32_f16 v[140:143], v[92:95], v[148:151], v[140:143]
	v_mfma_f32_16x16x32_f16 v[124:127], v[80:83], v[156:159], v[124:127]
	v_mfma_f32_16x16x32_f16 v[120:123], v[92:95], v[156:159], v[120:123]
	v_mfma_f32_16x16x32_f16 v[108:111], v[80:83], v[164:167], v[108:111]
	v_mfma_f32_16x16x32_f16 v[104:107], v[92:95], v[164:167], v[104:107]
	v_mfma_f32_16x16x32_f16 v[84:87], v[80:83], v[172:175], v[84:87]
	v_mfma_f32_16x16x32_f16 v[76:79], v[92:95], v[172:175], v[76:79]
	s_barrier
	s_add_i32 s42, 0, 0x1c000
	s_add_i32 s43, s88, s50
	s_mov_b32 m0, s43
	ds_read_b128 v[190:193], v255
	ds_read_b128 v[194:197], v255 offset:1024
	ds_read_b128 v[198:201], v255 offset:2048
	ds_read_b128 v[202:205], v255 offset:3072
	global_load_lds_dwordx4 v178, s[92:93]
	s_add_i32 m0, s43, 0x2000
	s_nop 0
	global_load_lds_dwordx4 v182, s[92:93]
	s_barrier
	s_waitcnt lgkmcnt(0)
	v_mfma_f32_16x16x32_f16 v[132:135], v[190:193], v[136:139], v[132:135]
	v_mfma_f32_16x16x32_f16 v[128:131], v[198:201], v[136:139], v[128:131]
	v_mfma_f32_16x16x32_f16 v[116:119], v[190:193], v[152:155], v[116:119]
	v_mfma_f32_16x16x32_f16 v[112:115], v[198:201], v[152:155], v[112:115]
	v_mfma_f32_16x16x32_f16 v[100:103], v[190:193], v[160:163], v[100:103]
	v_mfma_f32_16x16x32_f16 v[96:99], v[198:201], v[160:163], v[96:99]
	v_mfma_f32_16x16x32_f16 v[68:71], v[190:193], v[168:171], v[68:71]
	v_mfma_f32_16x16x32_f16 v[64:67], v[198:201], v[168:171], v[64:67]
	v_mfma_f32_16x16x32_f16 v[132:135], v[194:197], v[148:151], v[132:135]
	v_mfma_f32_16x16x32_f16 v[128:131], v[202:205], v[148:151], v[128:131]
	v_mfma_f32_16x16x32_f16 v[116:119], v[194:197], v[156:159], v[116:119]
	v_mfma_f32_16x16x32_f16 v[112:115], v[202:205], v[156:159], v[112:115]
	v_mfma_f32_16x16x32_f16 v[100:103], v[194:197], v[164:167], v[100:103]
	v_mfma_f32_16x16x32_f16 v[96:99], v[202:205], v[164:167], v[96:99]
	v_mfma_f32_16x16x32_f16 v[68:71], v[194:197], v[172:175], v[68:71]
	v_mfma_f32_16x16x32_f16 v[64:67], v[202:205], v[172:175], v[64:67]
	s_barrier
	s_mov_b32 m0, s58
	ds_read_b128 v[136:139], v232 offset:49152
	ds_read_b128 v[148:151], v232 offset:50176
	ds_read_b128 v[152:155], v232 offset:51200
	ds_read_b128 v[156:159], v232 offset:52224
	ds_read_b128 v[160:163], v232 offset:53248
	ds_read_b128 v[164:167], v232 offset:54272
	ds_read_b128 v[168:171], v232 offset:55296
	ds_read_b128 v[172:175], v232 offset:56320
	global_load_lds_dwordx4 v176, s[94:95]
	s_mov_b32 m0, s59
	s_nop 0
	global_load_lds_dwordx4 v180, s[94:95]
	s_waitcnt vmcnt(10)
	s_barrier
	s_waitcnt lgkmcnt(0)
	v_mfma_f32_16x16x32_f16 v[60:63], v[72:75], v[136:139], v[60:63]
	v_mfma_f32_16x16x32_f16 v[56:59], v[88:91], v[136:139], v[56:59]
	v_mfma_f32_16x16x32_f16 v[44:47], v[72:75], v[152:155], v[44:47]
	v_mfma_f32_16x16x32_f16 v[40:43], v[88:91], v[152:155], v[40:43]
	v_mfma_f32_16x16x32_f16 v[28:31], v[72:75], v[160:163], v[28:31]
	v_mfma_f32_16x16x32_f16 v[24:27], v[88:91], v[160:163], v[24:27]
	v_mfma_f32_16x16x32_f16 v[12:15], v[72:75], v[168:171], v[12:15]
	v_mfma_f32_16x16x32_f16 v[8:11], v[88:91], v[168:171], v[8:11]
	v_mfma_f32_16x16x32_f16 v[60:63], v[80:83], v[148:151], v[60:63]
	v_mfma_f32_16x16x32_f16 v[56:59], v[92:95], v[148:151], v[56:59]
	v_mfma_f32_16x16x32_f16 v[44:47], v[80:83], v[156:159], v[44:47]
	v_mfma_f32_16x16x32_f16 v[40:43], v[92:95], v[156:159], v[40:43]
	v_mfma_f32_16x16x32_f16 v[28:31], v[80:83], v[164:167], v[28:31]
	v_mfma_f32_16x16x32_f16 v[24:27], v[92:95], v[164:167], v[24:27]
	v_mfma_f32_16x16x32_f16 v[12:15], v[80:83], v[172:175], v[12:15]
	v_mfma_f32_16x16x32_f16 v[8:11], v[92:95], v[172:175], v[8:11]
	s_barrier
	s_add_i32 s42, s42, s50
	s_mov_b32 m0, s42
	s_add_u32 s40, s40, 0x30080
	s_addc_u32 s41, s41, 0
	global_load_lds_dwordx4 v178, s[40:41]
	s_add_i32 m0, s42, 0x2000
	s_nop 0
	global_load_lds_dwordx4 v182, s[40:41]
	ds_read_b128 v[72:75], v231
	ds_read_b128 v[80:83], v231 offset:1024
	ds_read_b128 v[88:91], v231 offset:2048
	ds_read_b128 v[92:95], v231 offset:3072
	s_waitcnt vmcnt(6)
	s_barrier
	v_mfma_f32_16x16x32_f16 v[52:55], v[190:193], v[136:139], v[52:55]
	v_mfma_f32_16x16x32_f16 v[48:51], v[198:201], v[136:139], v[48:51]
	v_mfma_f32_16x16x32_f16 v[36:39], v[190:193], v[152:155], v[36:39]
	v_mfma_f32_16x16x32_f16 v[32:35], v[198:201], v[152:155], v[32:35]
	v_mfma_f32_16x16x32_f16 v[20:23], v[190:193], v[160:163], v[20:23]
	v_mfma_f32_16x16x32_f16 v[16:19], v[198:201], v[160:163], v[16:19]
	v_mfma_f32_16x16x32_f16 v[4:7], v[190:193], v[168:171], v[4:7]
	v_mfma_f32_16x16x32_f16 v[0:3], v[198:201], v[168:171], v[0:3]
	v_mfma_f32_16x16x32_f16 v[52:55], v[194:197], v[148:151], v[52:55]
	v_mfma_f32_16x16x32_f16 v[48:51], v[202:205], v[148:151], v[48:51]
	v_mfma_f32_16x16x32_f16 v[36:39], v[194:197], v[156:159], v[36:39]
	v_mfma_f32_16x16x32_f16 v[32:35], v[202:205], v[156:159], v[32:35]
	v_mfma_f32_16x16x32_f16 v[20:23], v[194:197], v[164:167], v[20:23]
	v_mfma_f32_16x16x32_f16 v[16:19], v[202:205], v[164:167], v[16:19]
	v_mfma_f32_16x16x32_f16 v[4:7], v[194:197], v[172:175], v[4:7]
	v_mfma_f32_16x16x32_f16 v[0:3], v[202:205], v[172:175], v[0:3]
	s_barrier
	s_add_i32 s87, s87, 2
	s_add_u32 s38, s38, 0x100
	s_addc_u32 s39, s39, 0
	s_add_u32 s85, s85, 0x100
	s_addc_u32 s86, s86, 0
	s_cmp_gt_u32 s87, 45
	s_cbranch_scc0 .LBB10_27
	s_lshl_b32 s92, s84, 8
	s_add_i32 s92, s92, s57
	s_lshl_b32 s93, s83, 8
	s_or_b32 s93, s93, s60
	v_lshlrev_b32_e32 v237, 2, v226
	s_lshl_b32 s96, s93, 2
	s_add_u32 s94, s16, s96
	s_addc_u32 s95, s17, 0
	global_load_dwordx4 v[72:75], v237, s[94:95] offset:0
	global_load_dwordx4 v[80:83], v237, s[94:95] offset:16
	global_load_dwordx4 v[88:91], v237, s[94:95] offset:128
	global_load_dwordx4 v[92:95], v237, s[94:95] offset:144
	s_add_u32 s94, s18, s96
	s_addc_u32 s95, s19, 0
	global_load_dwordx4 v[136:139], v237, s[94:95] offset:0
	global_load_dwordx4 v[148:151], v237, s[94:95] offset:16
	global_load_dwordx4 v[152:155], v237, s[94:95] offset:128
	global_load_dwordx4 v[156:159], v237, s[94:95] offset:144
	s_add_u32 s94, s14, s96
	s_addc_u32 s95, s15, 0
	global_load_dwordx4 v[160:163], v237, s[94:95] offset:0
	global_load_dwordx4 v[164:167], v237, s[94:95] offset:16
	global_load_dwordx4 v[168:171], v237, s[94:95] offset:128
	global_load_dwordx4 v[172:175], v237, s[94:95] offset:144
	v_lshlrev_b32_e32 v190, 3, v227
	s_lshl_b32 s96, s92, 3
	s_add_u32 s94, s12, s96
	s_addc_u32 s95, s13, 0
	global_load_dwordx2 v[238:239], v190, s[94:95] offset:0
	global_load_dwordx2 v[192:193], v190, s[94:95] offset:128
	global_load_dwordx2 v[194:195], v190, s[94:95] offset:256
	global_load_dwordx2 v[196:197], v190, s[94:95] offset:384
	global_load_dwordx2 v[198:199], v190, s[94:95] offset:1024
	global_load_dwordx2 v[200:201], v190, s[94:95] offset:1152
	global_load_dwordx2 v[202:203], v190, s[94:95] offset:1280
	global_load_dwordx2 v[204:205], v190, s[94:95] offset:1408
	v_mul_u32_u24_e32 v191, 0x600, v227
	v_lshl_add_u32 v191, v226, 1, v191
	s_mul_i32 s96, s92, 0x600
	s_lshl_b32 s97, s93, 1
	s_add_u32 s96, s96, s97
	s_add_u32 s98, s10, s96
	s_addc_u32 s99, s11, 0
	s_add_u32 s94, s98, 0x0
	s_addc_u32 s95, s99, 0
	global_load_dwordx4 v[208:211], v191, s[94:95] offset:0 nt
	global_load_dwordx4 v[212:215], v191, s[94:95] offset:64 nt
	s_add_u32 s94, s98, 0x6000
	s_addc_u32 s95, s99, 0
	global_load_dwordx4 v[216:219], v191, s[94:95] offset:0 nt
	global_load_dwordx4 v[220:223], v191, s[94:95] offset:64 nt
	v_add_u32_e32 v224, s92, v229
	v_mul_u32_u24_e32 v224, 0x600, v224
	s_lshl_b32 s97, s93, 1
	v_add3_u32 v224, v224, v230, s97
	s_lshl_b32 s96, s83, 2
	s_lshr_b32 s97, s60, 6
	s_add_u32 s96, s96, s97
	s_lshl_b32 s96, s96, 19
	s_lshl_b32 s97, s92, 3
	s_add_u32 s96, s96, s97
	s_add_u32 s100, s28, s96
	s_addc_u32 s101, s29, 0
	s_waitcnt vmcnt(19)
	v_pk_add_f32 v[72:73], v[72:73], v[136:137]
	v_pk_add_f32 v[74:75], v[74:75], v[138:139]
	s_waitcnt vmcnt(18)
	v_pk_add_f32 v[80:81], v[80:81], v[148:149]
	v_pk_add_f32 v[82:83], v[82:83], v[150:151]
	s_waitcnt vmcnt(17)
	v_pk_add_f32 v[88:89], v[88:89], v[152:153]
	v_pk_add_f32 v[90:91], v[90:91], v[154:155]
	s_waitcnt vmcnt(16)
	v_pk_add_f32 v[92:93], v[92:93], v[156:157]
	v_pk_add_f32 v[94:95], v[94:95], v[158:159]
	v_pk_add_f32 v[144:145], v[144:145], v[72:73]
	v_pk_add_f32 v[146:147], v[146:147], v[74:75]
	v_pk_add_f32 v[124:125], v[124:125], v[72:73]
	v_pk_add_f32 v[126:127], v[126:127], v[74:75]
	v_pk_add_f32 v[108:109], v[108:109], v[72:73]
	v_pk_add_f32 v[110:111], v[110:111], v[74:75]
	v_pk_add_f32 v[84:85], v[84:85], v[72:73]
	v_pk_add_f32 v[86:87], v[86:87], v[74:75]
	v_pk_add_f32 v[60:61], v[60:61], v[72:73]
	v_pk_add_f32 v[62:63], v[62:63], v[74:75]
	v_pk_add_f32 v[44:45], v[44:45], v[72:73]
	v_pk_add_f32 v[46:47], v[46:47], v[74:75]
	v_pk_add_f32 v[28:29], v[28:29], v[72:73]
	v_pk_add_f32 v[30:31], v[30:31], v[74:75]
	v_pk_add_f32 v[12:13], v[12:13], v[72:73]
	v_pk_add_f32 v[14:15], v[14:15], v[74:75]
	v_pk_add_f32 v[140:141], v[140:141], v[80:81]
	v_pk_add_f32 v[142:143], v[142:143], v[82:83]
	v_pk_add_f32 v[120:121], v[120:121], v[80:81]
	v_pk_add_f32 v[122:123], v[122:123], v[82:83]
	v_pk_add_f32 v[104:105], v[104:105], v[80:81]
	v_pk_add_f32 v[106:107], v[106:107], v[82:83]
	v_pk_add_f32 v[76:77], v[76:77], v[80:81]
	v_pk_add_f32 v[78:79], v[78:79], v[82:83]
	v_pk_add_f32 v[56:57], v[56:57], v[80:81]
	v_pk_add_f32 v[58:59], v[58:59], v[82:83]
	v_pk_add_f32 v[40:41], v[40:41], v[80:81]
	v_pk_add_f32 v[42:43], v[42:43], v[82:83]
	v_pk_add_f32 v[24:25], v[24:25], v[80:81]
	v_pk_add_f32 v[26:27], v[26:27], v[82:83]
	v_pk_add_f32 v[8:9], v[8:9], v[80:81]
	v_pk_add_f32 v[10:11], v[10:11], v[82:83]
	v_pk_add_f32 v[132:133], v[132:133], v[88:89]
	v_pk_add_f32 v[134:135], v[134:135], v[90:91]
	v_pk_add_f32 v[116:117], v[116:117], v[88:89]
	v_pk_add_f32 v[118:119], v[118:119], v[90:91]
	v_pk_add_f32 v[100:101], v[100:101], v[88:89]
	v_pk_add_f32 v[102:103], v[102:103], v[90:91]
	v_pk_add_f32 v[68:69], v[68:69], v[88:89]
	v_pk_add_f32 v[70:71], v[70:71], v[90:91]
	v_pk_add_f32 v[52:53], v[52:53], v[88:89]
	v_pk_add_f32 v[54:55], v[54:55], v[90:91]
	v_pk_add_f32 v[36:37], v[36:37], v[88:89]
	v_pk_add_f32 v[38:39], v[38:39], v[90:91]
	v_pk_add_f32 v[20:21], v[20:21], v[88:89]
	v_pk_add_f32 v[22:23], v[22:23], v[90:91]
	v_pk_add_f32 v[4:5], v[4:5], v[88:89]
	v_pk_add_f32 v[6:7], v[6:7], v[90:91]
	v_pk_add_f32 v[128:129], v[128:129], v[92:93]
	v_pk_add_f32 v[130:131], v[130:131], v[94:95]
	v_pk_add_f32 v[112:113], v[112:113], v[92:93]
	v_pk_add_f32 v[114:115], v[114:115], v[94:95]
	v_pk_add_f32 v[96:97], v[96:97], v[92:93]
	v_pk_add_f32 v[98:99], v[98:99], v[94:95]
	v_pk_add_f32 v[64:65], v[64:65], v[92:93]
	v_pk_add_f32 v[66:67], v[66:67], v[94:95]
	v_pk_add_f32 v[48:49], v[48:49], v[92:93]
	v_pk_add_f32 v[50:51], v[50:51], v[94:95]
	v_pk_add_f32 v[32:33], v[32:33], v[92:93]
	v_pk_add_f32 v[34:35], v[34:35], v[94:95]
	v_pk_add_f32 v[16:17], v[16:17], v[92:93]
	v_pk_add_f32 v[18:19], v[18:19], v[94:95]
	v_pk_add_f32 v[0:1], v[0:1], v[92:93]
	v_pk_add_f32 v[2:3], v[2:3], v[94:95]
	s_add_u32 s94, s98, 0xc000
	s_addc_u32 s95, s99, 0
	global_load_dwordx4 v[240:243], v191, s[94:95] offset:0 nt
	global_load_dwordx4 v[244:247], v191, s[94:95] offset:64 nt
	s_add_u32 s94, s98, 0x12000
	s_addc_u32 s95, s99, 0
	global_load_dwordx4 v[248:251], v191, s[94:95] offset:0 nt
	global_load_dwordx4 v[252:255], v191, s[94:95] offset:64 nt
	s_add_u32 s94, s98, 0x30000
	s_addc_u32 s95, s99, 0
	global_load_dwordx4 v[136:139], v191, s[94:95] offset:0 nt
	global_load_dwordx4 v[148:151], v191, s[94:95] offset:64 nt
	s_add_u32 s94, s98, 0x36000
	s_addc_u32 s95, s99, 0
	global_load_dwordx4 v[152:155], v191, s[94:95] offset:0 nt
	global_load_dwordx4 v[156:159], v191, s[94:95] offset:64 nt
	s_waitcnt vmcnt(19)
	s_waitcnt vmcnt(11)
	v_cvt_f32_f16_e32 v72, v208
	v_cvt_f32_f16_sdwa v73, v208 dst_sel:DWORD dst_unused:UNUSED_PAD src0_sel:WORD_1
	v_cvt_f32_f16_e32 v74, v209
	v_cvt_f32_f16_sdwa v75, v209 dst_sel:DWORD dst_unused:UNUSED_PAD src0_sel:WORD_1
	v_cvt_f32_f16_e32 v80, v210
	v_cvt_f32_f16_sdwa v81, v210 dst_sel:DWORD dst_unused:UNUSED_PAD src0_sel:WORD_1
	v_cvt_f32_f16_e32 v82, v211
	v_cvt_f32_f16_sdwa v83, v211 dst_sel:DWORD dst_unused:UNUSED_PAD src0_sel:WORD_1
	v_sub_f32_e32 v72, v72, v238
	v_sub_f32_e32 v73, v73, v238
	v_sub_f32_e32 v74, v74, v238
	v_sub_f32_e32 v75, v75, v238
	v_sub_f32_e32 v80, v80, v238
	v_sub_f32_e32 v81, v81, v238
	v_sub_f32_e32 v82, v82, v238
	v_sub_f32_e32 v83, v83, v238
	v_pk_mul_f32 v[72:73], v[238:239], v[72:73] op_sel:[1,0]
	v_pk_mul_f32 v[74:75], v[238:239], v[74:75] op_sel:[1,0]
	v_pk_mul_f32 v[80:81], v[238:239], v[80:81] op_sel:[1,0]
	v_pk_mul_f32 v[82:83], v[238:239], v[82:83] op_sel:[1,0]
	v_pk_fma_f32 v[144:145], v[72:73], v[160:161], v[144:145]
	v_pk_fma_f32 v[146:147], v[74:75], v[162:163], v[146:147]
	v_pk_fma_f32 v[140:141], v[80:81], v[164:165], v[140:141]
	v_pk_fma_f32 v[142:143], v[82:83], v[166:167], v[142:143]
	v_cvt_pk_f16_f32 v144, v144, v145
	v_cvt_pk_f16_f32 v145, v146, v147
	v_cvt_pk_f16_f32 v146, v140, v141
	v_cvt_pk_f16_f32 v147, v142, v143
	ds_write_b128 v235, v[144:147]
	v_fma_mix_f32 v206, v144, 1.0, 0 op_sel_hi:[1,0,0]
	v_fma_mix_f32 v207, v144, v144, 0 op_sel_hi:[1,1,0]
	v_fma_mix_f32 v206, v144, 1.0, v206 op_sel:[1,0,0] op_sel_hi:[1,0,0]
	v_fma_mix_f32 v207, v144, v144, v207 op_sel:[1,1,0] op_sel_hi:[1,1,0]
	v_fma_mix_f32 v206, v145, 1.0, v206 op_sel_hi:[1,0,0]
	v_fma_mix_f32 v207, v145, v145, v207 op_sel_hi:[1,1,0]
	v_fma_mix_f32 v206, v145, 1.0, v206 op_sel:[1,0,0] op_sel_hi:[1,0,0]
	v_fma_mix_f32 v207, v145, v145, v207 op_sel:[1,1,0] op_sel_hi:[1,1,0]
	v_fma_mix_f32 v206, v146, 1.0, v206 op_sel_hi:[1,0,0]
	v_fma_mix_f32 v207, v146, v146, v207 op_sel_hi:[1,1,0]
	v_fma_mix_f32 v206, v146, 1.0, v206 op_sel:[1,0,0] op_sel_hi:[1,0,0]
	v_fma_mix_f32 v207, v146, v146, v207 op_sel:[1,1,0] op_sel_hi:[1,1,0]
	v_fma_mix_f32 v206, v147, 1.0, v206 op_sel_hi:[1,0,0]
	v_fma_mix_f32 v207, v147, v147, v207 op_sel_hi:[1,1,0]
	v_fma_mix_f32 v206, v147, 1.0, v206 op_sel:[1,0,0] op_sel_hi:[1,0,0]
	v_fma_mix_f32 v207, v147, v147, v207 op_sel:[1,1,0] op_sel_hi:[1,1,0]
	s_waitcnt vmcnt(10)
	v_cvt_f32_f16_e32 v72, v212
	v_cvt_f32_f16_sdwa v73, v212 dst_sel:DWORD dst_unused:UNUSED_PAD src0_sel:WORD_1
	v_cvt_f32_f16_e32 v74, v213
	v_cvt_f32_f16_sdwa v75, v213 dst_sel:DWORD dst_unused:UNUSED_PAD src0_sel:WORD_1
	v_cvt_f32_f16_e32 v80, v214
	v_cvt_f32_f16_sdwa v81, v214 dst_sel:DWORD dst_unused:UNUSED_PAD src0_sel:WORD_1
	v_cvt_f32_f16_e32 v82, v215
	v_cvt_f32_f16_sdwa v83, v215 dst_sel:DWORD dst_unused:UNUSED_PAD src0_sel:WORD_1
	v_sub_f32_e32 v72, v72, v238
	v_sub_f32_e32 v73, v73, v238
	v_sub_f32_e32 v74, v74, v238
	v_sub_f32_e32 v75, v75, v238
	v_sub_f32_e32 v80, v80, v238
	v_sub_f32_e32 v81, v81, v238
	v_sub_f32_e32 v82, v82, v238
	v_sub_f32_e32 v83, v83, v238
	v_pk_mul_f32 v[72:73], v[238:239], v[72:73] op_sel:[1,0]
	v_pk_mul_f32 v[74:75], v[238:239], v[74:75] op_sel:[1,0]
	v_pk_mul_f32 v[80:81], v[238:239], v[80:81] op_sel:[1,0]
	v_pk_mul_f32 v[82:83], v[238:239], v[82:83] op_sel:[1,0]
	v_pk_fma_f32 v[132:133], v[72:73], v[168:169], v[132:133]
	v_pk_fma_f32 v[134:135], v[74:75], v[170:171], v[134:135]
	v_pk_fma_f32 v[128:129], v[80:81], v[172:173], v[128:129]
	v_pk_fma_f32 v[130:131], v[82:83], v[174:175], v[130:131]
	v_cvt_pk_f16_f32 v132, v132, v133
	v_cvt_pk_f16_f32 v133, v134, v135
	v_cvt_pk_f16_f32 v134, v128, v129
	v_cvt_pk_f16_f32 v135, v130, v131
	ds_write_b128 v235, v[132:135] offset:64
	v_fma_mix_f32 v206, v132, 1.0, v206 op_sel_hi:[1,0,0]
	v_fma_mix_f32 v207, v132, v132, v207 op_sel_hi:[1,1,0]
	v_fma_mix_f32 v206, v132, 1.0, v206 op_sel:[1,0,0] op_sel_hi:[1,0,0]
	v_fma_mix_f32 v207, v132, v132, v207 op_sel:[1,1,0] op_sel_hi:[1,1,0]
	v_fma_mix_f32 v206, v133, 1.0, v206 op_sel_hi:[1,0,0]
	v_fma_mix_f32 v207, v133, v133, v207 op_sel_hi:[1,1,0]
	v_fma_mix_f32 v206, v133, 1.0, v206 op_sel:[1,0,0] op_sel_hi:[1,0,0]
	v_fma_mix_f32 v207, v133, v133, v207 op_sel:[1,1,0] op_sel_hi:[1,1,0]
	v_fma_mix_f32 v206, v134, 1.0, v206 op_sel_hi:[1,0,0]
	v_fma_mix_f32 v207, v134, v134, v207 op_sel_hi:[1,1,0]
	v_fma_mix_f32 v206, v134, 1.0, v206 op_sel:[1,0,0] op_sel_hi:[1,0,0]
	v_fma_mix_f32 v207, v134, v134, v207 op_sel:[1,1,0] op_sel_hi:[1,1,0]
	v_fma_mix_f32 v206, v135, 1.0, v206 op_sel_hi:[1,0,0]
	v_fma_mix_f32 v207, v135, v135, v207 op_sel_hi:[1,1,0]
	v_fma_mix_f32 v206, v135, 1.0, v206 op_sel:[1,0,0] op_sel_hi:[1,0,0]
	v_fma_mix_f32 v207, v135, v135, v207 op_sel:[1,1,0] op_sel_hi:[1,1,0]
	ds_read_b128 v[88:91], v236
	ds_read_b128 v[92:95], v236 offset:1152
	s_waitcnt vmcnt(9)
	v_cvt_f32_f16_e32 v72, v216
	v_cvt_f32_f16_sdwa v73, v216 dst_sel:DWORD dst_unused:UNUSED_PAD src0_sel:WORD_1
	v_cvt_f32_f16_e32 v74, v217
	v_cvt_f32_f16_sdwa v75, v217 dst_sel:DWORD dst_unused:UNUSED_PAD src0_sel:WORD_1
	v_cvt_f32_f16_e32 v80, v218
	v_cvt_f32_f16_sdwa v81, v218 dst_sel:DWORD dst_unused:UNUSED_PAD src0_sel:WORD_1
	v_cvt_f32_f16_e32 v82, v219
	v_cvt_f32_f16_sdwa v83, v219 dst_sel:DWORD dst_unused:UNUSED_PAD src0_sel:WORD_1
	v_sub_f32_e32 v72, v72, v192
	v_sub_f32_e32 v73, v73, v192
	v_sub_f32_e32 v74, v74, v192
	v_sub_f32_e32 v75, v75, v192
	v_sub_f32_e32 v80, v80, v192
	v_sub_f32_e32 v81, v81, v192
	v_sub_f32_e32 v82, v82, v192
	v_sub_f32_e32 v83, v83, v192
	v_pk_mul_f32 v[72:73], v[192:193], v[72:73] op_sel:[1,0]
	v_pk_mul_f32 v[74:75], v[192:193], v[74:75] op_sel:[1,0]
	v_pk_mul_f32 v[80:81], v[192:193], v[80:81] op_sel:[1,0]
	v_pk_mul_f32 v[82:83], v[192:193], v[82:83] op_sel:[1,0]
	v_pk_fma_f32 v[124:125], v[72:73], v[160:161], v[124:125]
	v_pk_fma_f32 v[126:127], v[74:75], v[162:163], v[126:127]
	v_pk_fma_f32 v[120:121], v[80:81], v[164:165], v[120:121]
	v_pk_fma_f32 v[122:123], v[82:83], v[166:167], v[122:123]
	v_cvt_pk_f16_f32 v124, v124, v125
	v_cvt_pk_f16_f32 v125, v126, v127
	v_cvt_pk_f16_f32 v126, v120, v121
	v_cvt_pk_f16_f32 v127, v122, v123
	s_waitcnt lgkmcnt(0)
	buffer_store_dwordx4 v[88:91], v224, s[24:27], 0 offen nt
	v_add_u32_e32 v82, 0x3000, v224
	buffer_store_dwordx4 v[92:95], v82, s[24:27], 0 offen nt
	ds_write_b128 v235, v[124:127]
	v_fma_mix_f32 v140, v124, 1.0, 0 op_sel_hi:[1,0,0]
	v_fma_mix_f32 v141, v124, v124, 0 op_sel_hi:[1,1,0]
	v_fma_mix_f32 v140, v124, 1.0, v140 op_sel:[1,0,0] op_sel_hi:[1,0,0]
	v_fma_mix_f32 v141, v124, v124, v141 op_sel:[1,1,0] op_sel_hi:[1,1,0]
	v_fma_mix_f32 v140, v125, 1.0, v140 op_sel_hi:[1,0,0]
	v_fma_mix_f32 v141, v125, v125, v141 op_sel_hi:[1,1,0]
	v_fma_mix_f32 v140, v125, 1.0, v140 op_sel:[1,0,0] op_sel_hi:[1,0,0]
	v_fma_mix_f32 v141, v125, v125, v141 op_sel:[1,1,0] op_sel_hi:[1,1,0]
	v_fma_mix_f32 v140, v126, 1.0, v140 op_sel_hi:[1,0,0]
	v_fma_mix_f32 v141, v126, v126, v141 op_sel_hi:[1,1,0]
	v_fma_mix_f32 v140, v126, 1.0, v140 op_sel:[1,0,0] op_sel_hi:[1,0,0]
	v_fma_mix_f32 v141, v126, v126, v141 op_sel:[1,1,0] op_sel_hi:[1,1,0]
	v_fma_mix_f32 v140, v127, 1.0, v140 op_sel_hi:[1,0,0]
	v_fma_mix_f32 v141, v127, v127, v141 op_sel_hi:[1,1,0]
	v_fma_mix_f32 v140, v127, 1.0, v140 op_sel:[1,0,0] op_sel_hi:[1,0,0]
	v_fma_mix_f32 v141, v127, v127, v141 op_sel:[1,1,0] op_sel_hi:[1,1,0]
	s_waitcnt vmcnt(10)
	v_cvt_f32_f16_e32 v72, v220
	v_cvt_f32_f16_sdwa v73, v220 dst_sel:DWORD dst_unused:UNUSED_PAD src0_sel:WORD_1
	v_cvt_f32_f16_e32 v74, v221
	v_cvt_f32_f16_sdwa v75, v221 dst_sel:DWORD dst_unused:UNUSED_PAD src0_sel:WORD_1
	v_cvt_f32_f16_e32 v80, v222
	v_cvt_f32_f16_sdwa v81, v222 dst_sel:DWORD dst_unused:UNUSED_PAD src0_sel:WORD_1
	v_cvt_f32_f16_e32 v82, v223
	v_cvt_f32_f16_sdwa v83, v223 dst_sel:DWORD dst_unused:UNUSED_PAD src0_sel:WORD_1
	v_sub_f32_e32 v72, v72, v192
	v_sub_f32_e32 v73, v73, v192
	v_sub_f32_e32 v74, v74, v192
	v_sub_f32_e32 v75, v75, v192
	v_sub_f32_e32 v80, v80, v192
	v_sub_f32_e32 v81, v81, v192
	v_sub_f32_e32 v82, v82, v192
	v_sub_f32_e32 v83, v83, v192
	v_pk_mul_f32 v[72:73], v[192:193], v[72:73] op_sel:[1,0]
	v_pk_mul_f32 v[74:75], v[192:193], v[74:75] op_sel:[1,0]
	v_pk_mul_f32 v[80:81], v[192:193], v[80:81] op_sel:[1,0]
	v_pk_mul_f32 v[82:83], v[192:193], v[82:83] op_sel:[1,0]
	v_pk_fma_f32 v[116:117], v[72:73], v[168:169], v[116:117]
	v_pk_fma_f32 v[118:119], v[74:75], v[170:171], v[118:119]
	v_pk_fma_f32 v[112:113], v[80:81], v[172:173], v[112:113]
	v_pk_fma_f32 v[114:115], v[82:83], v[174:175], v[114:115]
	v_cvt_pk_f16_f32 v116, v116, v117
	v_cvt_pk_f16_f32 v117, v118, v119
	v_cvt_pk_f16_f32 v118, v112, v113
	v_cvt_pk_f16_f32 v119, v114, v115
	ds_write_b128 v235, v[116:119] offset:64
	v_fma_mix_f32 v140, v116, 1.0, v140 op_sel_hi:[1,0,0]
	v_fma_mix_f32 v141, v116, v116, v141 op_sel_hi:[1,1,0]
	v_fma_mix_f32 v140, v116, 1.0, v140 op_sel:[1,0,0] op_sel_hi:[1,0,0]
	v_fma_mix_f32 v141, v116, v116, v141 op_sel:[1,1,0] op_sel_hi:[1,1,0]
	v_fma_mix_f32 v140, v117, 1.0, v140 op_sel_hi:[1,0,0]
	v_fma_mix_f32 v141, v117, v117, v141 op_sel_hi:[1,1,0]
	v_fma_mix_f32 v140, v117, 1.0, v140 op_sel:[1,0,0] op_sel_hi:[1,0,0]
	v_fma_mix_f32 v141, v117, v117, v141 op_sel:[1,1,0] op_sel_hi:[1,1,0]
	v_fma_mix_f32 v140, v118, 1.0, v140 op_sel_hi:[1,0,0]
	v_fma_mix_f32 v141, v118, v118, v141 op_sel_hi:[1,1,0]
	v_fma_mix_f32 v140, v118, 1.0, v140 op_sel:[1,0,0] op_sel_hi:[1,0,0]
	v_fma_mix_f32 v141, v118, v118, v141 op_sel:[1,1,0] op_sel_hi:[1,1,0]
	v_fma_mix_f32 v140, v119, 1.0, v140 op_sel_hi:[1,0,0]
	v_fma_mix_f32 v141, v119, v119, v141 op_sel_hi:[1,1,0]
	v_fma_mix_f32 v140, v119, 1.0, v140 op_sel:[1,0,0] op_sel_hi:[1,0,0]
	v_fma_mix_f32 v141, v119, v119, v141 op_sel:[1,1,0] op_sel_hi:[1,1,0]
	ds_read_b128 v[208:211], v236
	ds_read_b128 v[128:131], v236 offset:1152
	s_add_u32 s94, s98, 0x3c000
	s_addc_u32 s95, s99, 0
	global_load_dwordx4 v[212:215], v191, s[94:95] offset:0 nt
	global_load_dwordx4 v[144:147], v191, s[94:95] offset:64 nt
	s_add_u32 s94, s98, 0x42000
	s_addc_u32 s95, s99, 0
	global_load_dwordx4 v[132:135], v191, s[94:95] offset:0 nt
	global_load_dwordx4 v[88:91], v191, s[94:95] offset:64 nt
	s_waitcnt vmcnt(13)
	v_cvt_f32_f16_e32 v72, v240
	v_cvt_f32_f16_sdwa v73, v240 dst_sel:DWORD dst_unused:UNUSED_PAD src0_sel:WORD_1
	v_cvt_f32_f16_e32 v74, v241
	v_cvt_f32_f16_sdwa v75, v241 dst_sel:DWORD dst_unused:UNUSED_PAD src0_sel:WORD_1
	v_cvt_f32_f16_e32 v80, v242
	v_cvt_f32_f16_sdwa v81, v242 dst_sel:DWORD dst_unused:UNUSED_PAD src0_sel:WORD_1
	v_cvt_f32_f16_e32 v82, v243
	v_cvt_f32_f16_sdwa v83, v243 dst_sel:DWORD dst_unused:UNUSED_PAD src0_sel:WORD_1
	v_sub_f32_e32 v72, v72, v194
	v_sub_f32_e32 v73, v73, v194
	v_sub_f32_e32 v74, v74, v194
	v_sub_f32_e32 v75, v75, v194
	v_sub_f32_e32 v80, v80, v194
	v_sub_f32_e32 v81, v81, v194
	v_sub_f32_e32 v82, v82, v194
	v_sub_f32_e32 v83, v83, v194
	v_pk_mul_f32 v[72:73], v[194:195], v[72:73] op_sel:[1,0]
	v_pk_mul_f32 v[74:75], v[194:195], v[74:75] op_sel:[1,0]
	v_pk_mul_f32 v[80:81], v[194:195], v[80:81] op_sel:[1,0]
	v_pk_mul_f32 v[82:83], v[194:195], v[82:83] op_sel:[1,0]
	v_pk_fma_f32 v[108:109], v[72:73], v[160:161], v[108:109]
	v_pk_fma_f32 v[110:111], v[74:75], v[162:163], v[110:111]
	v_pk_fma_f32 v[104:105], v[80:81], v[164:165], v[104:105]
	v_pk_fma_f32 v[106:107], v[82:83], v[166:167], v[106:107]
	v_cvt_pk_f16_f32 v108, v108, v109
	v_cvt_pk_f16_f32 v109, v110, v111
	v_cvt_pk_f16_f32 v110, v104, v105
	v_cvt_pk_f16_f32 v111, v106, v107
	s_waitcnt lgkmcnt(0)
	v_add_u32_e32 v83, 0x6000, v224
	buffer_store_dwordx4 v[208:211], v83, s[24:27], 0 offen nt
	v_add_u32_e32 v82, 0x9000, v224
	buffer_store_dwordx4 v[128:131], v82, s[24:27], 0 offen nt
	ds_write_b128 v235, v[108:111]
	v_fma_mix_f32 v142, v108, 1.0, 0 op_sel_hi:[1,0,0]
	v_fma_mix_f32 v143, v108, v108, 0 op_sel_hi:[1,1,0]
	v_fma_mix_f32 v142, v108, 1.0, v142 op_sel:[1,0,0] op_sel_hi:[1,0,0]
	v_fma_mix_f32 v143, v108, v108, v143 op_sel:[1,1,0] op_sel_hi:[1,1,0]
	v_fma_mix_f32 v142, v109, 1.0, v142 op_sel_hi:[1,0,0]
	v_fma_mix_f32 v143, v109, v109, v143 op_sel_hi:[1,1,0]
	v_fma_mix_f32 v142, v109, 1.0, v142 op_sel:[1,0,0] op_sel_hi:[1,0,0]
	v_fma_mix_f32 v143, v109, v109, v143 op_sel:[1,1,0] op_sel_hi:[1,1,0]
	v_fma_mix_f32 v142, v110, 1.0, v142 op_sel_hi:[1,0,0]
	v_fma_mix_f32 v143, v110, v110, v143 op_sel_hi:[1,1,0]
	v_fma_mix_f32 v142, v110, 1.0, v142 op_sel:[1,0,0] op_sel_hi:[1,0,0]
	v_fma_mix_f32 v143, v110, v110, v143 op_sel:[1,1,0] op_sel_hi:[1,1,0]
	v_fma_mix_f32 v142, v111, 1.0, v142 op_sel_hi:[1,0,0]
	v_fma_mix_f32 v143, v111, v111, v143 op_sel_hi:[1,1,0]
	v_fma_mix_f32 v142, v111, 1.0, v142 op_sel:[1,0,0] op_sel_hi:[1,0,0]
	v_fma_mix_f32 v143, v111, v111, v143 op_sel:[1,1,0] op_sel_hi:[1,1,0]
	s_waitcnt vmcnt(14)
	v_cvt_f32_f16_e32 v72, v244
	v_cvt_f32_f16_sdwa v73, v244 dst_sel:DWORD dst_unused:UNUSED_PAD src0_sel:WORD_1
	v_cvt_f32_f16_e32 v74, v245
	v_cvt_f32_f16_sdwa v75, v245 dst_sel:DWORD dst_unused:UNUSED_PAD src0_sel:WORD_1
	v_cvt_f32_f16_e32 v80, v246
	v_cvt_f32_f16_sdwa v81, v246 dst_sel:DWORD dst_unused:UNUSED_PAD src0_sel:WORD_1
	v_cvt_f32_f16_e32 v82, v247
	v_cvt_f32_f16_sdwa v83, v247 dst_sel:DWORD dst_unused:UNUSED_PAD src0_sel:WORD_1
	v_sub_f32_e32 v72, v72, v194
	v_sub_f32_e32 v73, v73, v194
	v_sub_f32_e32 v74, v74, v194
	v_sub_f32_e32 v75, v75, v194
	v_sub_f32_e32 v80, v80, v194
	v_sub_f32_e32 v81, v81, v194
	v_sub_f32_e32 v82, v82, v194
	v_sub_f32_e32 v83, v83, v194
	v_pk_mul_f32 v[72:73], v[194:195], v[72:73] op_sel:[1,0]
	v_pk_mul_f32 v[74:75], v[194:195], v[74:75] op_sel:[1,0]
	v_pk_mul_f32 v[80:81], v[194:195], v[80:81] op_sel:[1,0]
	v_pk_mul_f32 v[82:83], v[194:195], v[82:83] op_sel:[1,0]
	v_pk_fma_f32 v[100:101], v[72:73], v[168:169], v[100:101]
	v_pk_fma_f32 v[102:103], v[74:75], v[170:171], v[102:103]
	v_pk_fma_f32 v[96:97], v[80:81], v[172:173], v[96:97]
	v_pk_fma_f32 v[98:99], v[82:83], v[174:175], v[98:99]
	v_cvt_pk_f16_f32 v100, v100, v101
	v_cvt_pk_f16_f32 v101, v102, v103
	v_cvt_pk_f16_f32 v102, v96, v97
	v_cvt_pk_f16_f32 v103, v98, v99
	ds_write_b128 v235, v[100:103] offset:64
	v_fma_mix_f32 v142, v100, 1.0, v142 op_sel_hi:[1,0,0]
	v_fma_mix_f32 v143, v100, v100, v143 op_sel_hi:[1,1,0]
	v_fma_mix_f32 v142, v100, 1.0, v142 op_sel:[1,0,0] op_sel_hi:[1,0,0]
	v_fma_mix_f32 v143, v100, v100, v143 op_sel:[1,1,0] op_sel_hi:[1,1,0]
	v_fma_mix_f32 v142, v101, 1.0, v142 op_sel_hi:[1,0,0]
	v_fma_mix_f32 v143, v101, v101, v143 op_sel_hi:[1,1,0]
	v_fma_mix_f32 v142, v101, 1.0, v142 op_sel:[1,0,0] op_sel_hi:[1,0,0]
	v_fma_mix_f32 v143, v101, v101, v143 op_sel:[1,1,0] op_sel_hi:[1,1,0]
	v_fma_mix_f32 v142, v102, 1.0, v142 op_sel_hi:[1,0,0]
	v_fma_mix_f32 v143, v102, v102, v143 op_sel_hi:[1,1,0]
	v_fma_mix_f32 v142, v102, 1.0, v142 op_sel:[1,0,0] op_sel_hi:[1,0,0]
	v_fma_mix_f32 v143, v102, v102, v143 op_sel:[1,1,0] op_sel_hi:[1,1,0]
	v_fma_mix_f32 v142, v103, 1.0, v142 op_sel_hi:[1,0,0]
	v_fma_mix_f32 v143, v103, v103, v143 op_sel_hi:[1,1,0]
	v_fma_mix_f32 v142, v103, 1.0, v142 op_sel:[1,0,0] op_sel_hi:[1,0,0]
	v_fma_mix_f32 v143, v103, v103, v143 op_sel:[1,1,0] op_sel_hi:[1,1,0]
	ds_read_b128 v[92:95], v236
	ds_read_b128 v[120:123], v236 offset:1152
	s_waitcnt vmcnt(13)
	v_cvt_f32_f16_e32 v72, v248
	v_cvt_f32_f16_sdwa v73, v248 dst_sel:DWORD dst_unused:UNUSED_PAD src0_sel:WORD_1
	v_cvt_f32_f16_e32 v74, v249
	v_cvt_f32_f16_sdwa v75, v249 dst_sel:DWORD dst_unused:UNUSED_PAD src0_sel:WORD_1
	v_cvt_f32_f16_e32 v80, v250
	v_cvt_f32_f16_sdwa v81, v250 dst_sel:DWORD dst_unused:UNUSED_PAD src0_sel:WORD_1
	v_cvt_f32_f16_e32 v82, v251
	v_cvt_f32_f16_sdwa v83, v251 dst_sel:DWORD dst_unused:UNUSED_PAD src0_sel:WORD_1
	v_sub_f32_e32 v72, v72, v196
	v_sub_f32_e32 v73, v73, v196
	v_sub_f32_e32 v74, v74, v196
	v_sub_f32_e32 v75, v75, v196
	v_sub_f32_e32 v80, v80, v196
	v_sub_f32_e32 v81, v81, v196
	v_sub_f32_e32 v82, v82, v196
	v_sub_f32_e32 v83, v83, v196
	v_pk_mul_f32 v[72:73], v[196:197], v[72:73] op_sel:[1,0]
	v_pk_mul_f32 v[74:75], v[196:197], v[74:75] op_sel:[1,0]
	v_pk_mul_f32 v[80:81], v[196:197], v[80:81] op_sel:[1,0]
	v_pk_mul_f32 v[82:83], v[196:197], v[82:83] op_sel:[1,0]
	v_pk_fma_f32 v[84:85], v[72:73], v[160:161], v[84:85]
	v_pk_fma_f32 v[86:87], v[74:75], v[162:163], v[86:87]
	v_pk_fma_f32 v[76:77], v[80:81], v[164:165], v[76:77]
	v_pk_fma_f32 v[78:79], v[82:83], v[166:167], v[78:79]
	v_cvt_pk_f16_f32 v84, v84, v85
	v_cvt_pk_f16_f32 v85, v86, v87
	v_cvt_pk_f16_f32 v86, v76, v77
	v_cvt_pk_f16_f32 v87, v78, v79
	s_waitcnt lgkmcnt(0)
	v_add_u32_e32 v83, 0xc000, v224
	buffer_store_dwordx4 v[92:95], v83, s[24:27], 0 offen nt
	v_add_u32_e32 v82, 0xf000, v224
	buffer_store_dwordx4 v[120:123], v82, s[24:27], 0 offen nt
	ds_write_b128 v235, v[84:87]
	v_fma_mix_f32 v216, v84, 1.0, 0 op_sel_hi:[1,0,0]
	v_fma_mix_f32 v217, v84, v84, 0 op_sel_hi:[1,1,0]
	v_fma_mix_f32 v216, v84, 1.0, v216 op_sel:[1,0,0] op_sel_hi:[1,0,0]
	v_fma_mix_f32 v217, v84, v84, v217 op_sel:[1,1,0] op_sel_hi:[1,1,0]
	v_fma_mix_f32 v216, v85, 1.0, v216 op_sel_hi:[1,0,0]
	v_fma_mix_f32 v217, v85, v85, v217 op_sel_hi:[1,1,0]
	v_fma_mix_f32 v216, v85, 1.0, v216 op_sel:[1,0,0] op_sel_hi:[1,0,0]
	v_fma_mix_f32 v217, v85, v85, v217 op_sel:[1,1,0] op_sel_hi:[1,1,0]
	v_fma_mix_f32 v216, v86, 1.0, v216 op_sel_hi:[1,0,0]
	v_fma_mix_f32 v217, v86, v86, v217 op_sel_hi:[1,1,0]
	v_fma_mix_f32 v216, v86, 1.0, v216 op_sel:[1,0,0] op_sel_hi:[1,0,0]
	v_fma_mix_f32 v217, v86, v86, v217 op_sel:[1,1,0] op_sel_hi:[1,1,0]
	v_fma_mix_f32 v216, v87, 1.0, v216 op_sel_hi:[1,0,0]
	v_fma_mix_f32 v217, v87, v87, v217 op_sel_hi:[1,1,0]
	v_fma_mix_f32 v216, v87, 1.0, v216 op_sel:[1,0,0] op_sel_hi:[1,0,0]
	v_fma_mix_f32 v217, v87, v87, v217 op_sel:[1,1,0] op_sel_hi:[1,1,0]
	s_waitcnt vmcnt(14)
	v_cvt_f32_f16_e32 v72, v252
	v_cvt_f32_f16_sdwa v73, v252 dst_sel:DWORD dst_unused:UNUSED_PAD src0_sel:WORD_1
	v_cvt_f32_f16_e32 v74, v253
	v_cvt_f32_f16_sdwa v75, v253 dst_sel:DWORD dst_unused:UNUSED_PAD src0_sel:WORD_1
	v_cvt_f32_f16_e32 v80, v254
	v_cvt_f32_f16_sdwa v81, v254 dst_sel:DWORD dst_unused:UNUSED_PAD src0_sel:WORD_1
	v_cvt_f32_f16_e32 v82, v255
	v_cvt_f32_f16_sdwa v83, v255 dst_sel:DWORD dst_unused:UNUSED_PAD src0_sel:WORD_1
	v_sub_f32_e32 v72, v72, v196
	v_sub_f32_e32 v73, v73, v196
	v_sub_f32_e32 v74, v74, v196
	v_sub_f32_e32 v75, v75, v196
	v_sub_f32_e32 v80, v80, v196
	v_sub_f32_e32 v81, v81, v196
	v_sub_f32_e32 v82, v82, v196
	v_sub_f32_e32 v83, v83, v196
	v_pk_mul_f32 v[72:73], v[196:197], v[72:73] op_sel:[1,0]
	v_pk_mul_f32 v[74:75], v[196:197], v[74:75] op_sel:[1,0]
	v_pk_mul_f32 v[80:81], v[196:197], v[80:81] op_sel:[1,0]
	v_pk_mul_f32 v[82:83], v[196:197], v[82:83] op_sel:[1,0]
	v_pk_fma_f32 v[68:69], v[72:73], v[168:169], v[68:69]
	v_pk_fma_f32 v[70:71], v[74:75], v[170:171], v[70:71]
	v_pk_fma_f32 v[64:65], v[80:81], v[172:173], v[64:65]
	v_pk_fma_f32 v[66:67], v[82:83], v[174:175], v[66:67]
	v_cvt_pk_f16_f32 v68, v68, v69
	v_cvt_pk_f16_f32 v69, v70, v71
	v_cvt_pk_f16_f32 v70, v64, v65
	v_cvt_pk_f16_f32 v71, v66, v67
	ds_write_b128 v235, v[68:71] offset:64
	v_fma_mix_f32 v216, v68, 1.0, v216 op_sel_hi:[1,0,0]
	v_fma_mix_f32 v217, v68, v68, v217 op_sel_hi:[1,1,0]
	v_fma_mix_f32 v216, v68, 1.0, v216 op_sel:[1,0,0] op_sel_hi:[1,0,0]
	v_fma_mix_f32 v217, v68, v68, v217 op_sel:[1,1,0] op_sel_hi:[1,1,0]
	v_fma_mix_f32 v216, v69, 1.0, v216 op_sel_hi:[1,0,0]
	v_fma_mix_f32 v217, v69, v69, v217 op_sel_hi:[1,1,0]
	v_fma_mix_f32 v216, v69, 1.0, v216 op_sel:[1,0,0] op_sel_hi:[1,0,0]
	v_fma_mix_f32 v217, v69, v69, v217 op_sel:[1,1,0] op_sel_hi:[1,1,0]
	v_fma_mix_f32 v216, v70, 1.0, v216 op_sel_hi:[1,0,0]
	v_fma_mix_f32 v217, v70, v70, v217 op_sel_hi:[1,1,0]
	v_fma_mix_f32 v216, v70, 1.0, v216 op_sel:[1,0,0] op_sel_hi:[1,0,0]
	v_fma_mix_f32 v217, v70, v70, v217 op_sel:[1,1,0] op_sel_hi:[1,1,0]
	v_fma_mix_f32 v216, v71, 1.0, v216 op_sel_hi:[1,0,0]
	v_fma_mix_f32 v217, v71, v71, v217 op_sel_hi:[1,1,0]
	v_fma_mix_f32 v216, v71, 1.0, v216 op_sel:[1,0,0] op_sel_hi:[1,0,0]
	v_fma_mix_f32 v217, v71, v71, v217 op_sel:[1,1,0] op_sel_hi:[1,1,0]
	ds_read_b128 v[112:115], v236
	ds_read_b128 v[220:223], v236 offset:1152
	s_waitcnt vmcnt(13)
	v_cvt_f32_f16_e32 v72, v136
	v_cvt_f32_f16_sdwa v73, v136 dst_sel:DWORD dst_unused:UNUSED_PAD src0_sel:WORD_1
	v_cvt_f32_f16_e32 v74, v137
	v_cvt_f32_f16_sdwa v75, v137 dst_sel:DWORD dst_unused:UNUSED_PAD src0_sel:WORD_1
	v_cvt_f32_f16_e32 v80, v138
	v_cvt_f32_f16_sdwa v81, v138 dst_sel:DWORD dst_unused:UNUSED_PAD src0_sel:WORD_1
	v_cvt_f32_f16_e32 v82, v139
	v_cvt_f32_f16_sdwa v83, v139 dst_sel:DWORD dst_unused:UNUSED_PAD src0_sel:WORD_1
	v_sub_f32_e32 v72, v72, v198
	v_sub_f32_e32 v73, v73, v198
	v_sub_f32_e32 v74, v74, v198
	v_sub_f32_e32 v75, v75, v198
	v_sub_f32_e32 v80, v80, v198
	v_sub_f32_e32 v81, v81, v198
	v_sub_f32_e32 v82, v82, v198
	v_sub_f32_e32 v83, v83, v198
	v_pk_mul_f32 v[72:73], v[198:199], v[72:73] op_sel:[1,0]
	v_pk_mul_f32 v[74:75], v[198:199], v[74:75] op_sel:[1,0]
	v_pk_mul_f32 v[80:81], v[198:199], v[80:81] op_sel:[1,0]
	v_pk_mul_f32 v[82:83], v[198:199], v[82:83] op_sel:[1,0]
	v_pk_fma_f32 v[60:61], v[72:73], v[160:161], v[60:61]
	v_pk_fma_f32 v[62:63], v[74:75], v[162:163], v[62:63]
	v_pk_fma_f32 v[56:57], v[80:81], v[164:165], v[56:57]
	v_pk_fma_f32 v[58:59], v[82:83], v[166:167], v[58:59]
	v_cvt_pk_f16_f32 v60, v60, v61
	v_cvt_pk_f16_f32 v61, v62, v63
	v_cvt_pk_f16_f32 v62, v56, v57
	v_cvt_pk_f16_f32 v63, v58, v59
	s_waitcnt lgkmcnt(0)
	v_add_u32_e32 v83, 0x12000, v224
	buffer_store_dwordx4 v[112:115], v83, s[24:27], 0 offen nt
	v_add_u32_e32 v82, 0x15000, v224
	buffer_store_dwordx4 v[220:223], v82, s[24:27], 0 offen nt
	ds_write_b128 v235, v[60:63]
	v_fma_mix_f32 v218, v60, 1.0, 0 op_sel_hi:[1,0,0]
	v_fma_mix_f32 v219, v60, v60, 0 op_sel_hi:[1,1,0]
	v_fma_mix_f32 v218, v60, 1.0, v218 op_sel:[1,0,0] op_sel_hi:[1,0,0]
	v_fma_mix_f32 v219, v60, v60, v219 op_sel:[1,1,0] op_sel_hi:[1,1,0]
	v_fma_mix_f32 v218, v61, 1.0, v218 op_sel_hi:[1,0,0]
	v_fma_mix_f32 v219, v61, v61, v219 op_sel_hi:[1,1,0]
	v_fma_mix_f32 v218, v61, 1.0, v218 op_sel:[1,0,0] op_sel_hi:[1,0,0]
	v_fma_mix_f32 v219, v61, v61, v219 op_sel:[1,1,0] op_sel_hi:[1,1,0]
	v_fma_mix_f32 v218, v62, 1.0, v218 op_sel_hi:[1,0,0]
	v_fma_mix_f32 v219, v62, v62, v219 op_sel_hi:[1,1,0]
	v_fma_mix_f32 v218, v62, 1.0, v218 op_sel:[1,0,0] op_sel_hi:[1,0,0]
	v_fma_mix_f32 v219, v62, v62, v219 op_sel:[1,1,0] op_sel_hi:[1,1,0]
	v_fma_mix_f32 v218, v63, 1.0, v218 op_sel_hi:[1,0,0]
	v_fma_mix_f32 v219, v63, v63, v219 op_sel_hi:[1,1,0]
	v_fma_mix_f32 v218, v63, 1.0, v218 op_sel:[1,0,0] op_sel_hi:[1,0,0]
	v_fma_mix_f32 v219, v63, v63, v219 op_sel:[1,1,0] op_sel_hi:[1,1,0]
	s_waitcnt vmcnt(14)
	v_cvt_f32_f16_e32 v72, v148
	v_cvt_f32_f16_sdwa v73, v148 dst_sel:DWORD dst_unused:UNUSED_PAD src0_sel:WORD_1
	v_cvt_f32_f16_e32 v74, v149
	v_cvt_f32_f16_sdwa v75, v149 dst_sel:DWORD dst_unused:UNUSED_PAD src0_sel:WORD_1
	v_cvt_f32_f16_e32 v80, v150
	v_cvt_f32_f16_sdwa v81, v150 dst_sel:DWORD dst_unused:UNUSED_PAD src0_sel:WORD_1
	v_cvt_f32_f16_e32 v82, v151
	v_cvt_f32_f16_sdwa v83, v151 dst_sel:DWORD dst_unused:UNUSED_PAD src0_sel:WORD_1
	v_sub_f32_e32 v72, v72, v198
	v_sub_f32_e32 v73, v73, v198
	v_sub_f32_e32 v74, v74, v198
	v_sub_f32_e32 v75, v75, v198
	v_sub_f32_e32 v80, v80, v198
	v_sub_f32_e32 v81, v81, v198
	v_sub_f32_e32 v82, v82, v198
	v_sub_f32_e32 v83, v83, v198
	v_pk_mul_f32 v[72:73], v[198:199], v[72:73] op_sel:[1,0]
	v_pk_mul_f32 v[74:75], v[198:199], v[74:75] op_sel:[1,0]
	v_pk_mul_f32 v[80:81], v[198:199], v[80:81] op_sel:[1,0]
	v_pk_mul_f32 v[82:83], v[198:199], v[82:83] op_sel:[1,0]
	v_pk_fma_f32 v[52:53], v[72:73], v[168:169], v[52:53]
	v_pk_fma_f32 v[54:55], v[74:75], v[170:171], v[54:55]
	v_pk_fma_f32 v[48:49], v[80:81], v[172:173], v[48:49]
	v_pk_fma_f32 v[50:51], v[82:83], v[174:175], v[50:51]
	v_cvt_pk_f16_f32 v52, v52, v53
	v_cvt_pk_f16_f32 v53, v54, v55
	v_cvt_pk_f16_f32 v54, v48, v49
	v_cvt_pk_f16_f32 v55, v50, v51
	ds_write_b128 v235, v[52:55] offset:64
	v_fma_mix_f32 v218, v52, 1.0, v218 op_sel_hi:[1,0,0]
	v_fma_mix_f32 v219, v52, v52, v219 op_sel_hi:[1,1,0]
	v_fma_mix_f32 v218, v52, 1.0, v218 op_sel:[1,0,0] op_sel_hi:[1,0,0]
	v_fma_mix_f32 v219, v52, v52, v219 op_sel:[1,1,0] op_sel_hi:[1,1,0]
	v_fma_mix_f32 v218, v53, 1.0, v218 op_sel_hi:[1,0,0]
	v_fma_mix_f32 v219, v53, v53, v219 op_sel_hi:[1,1,0]
	v_fma_mix_f32 v218, v53, 1.0, v218 op_sel:[1,0,0] op_sel_hi:[1,0,0]
	v_fma_mix_f32 v219, v53, v53, v219 op_sel:[1,1,0] op_sel_hi:[1,1,0]
	v_fma_mix_f32 v218, v54, 1.0, v218 op_sel_hi:[1,0,0]
	v_fma_mix_f32 v219, v54, v54, v219 op_sel_hi:[1,1,0]
	v_fma_mix_f32 v218, v54, 1.0, v218 op_sel:[1,0,0] op_sel_hi:[1,0,0]
	v_fma_mix_f32 v219, v54, v54, v219 op_sel:[1,1,0] op_sel_hi:[1,1,0]
	v_fma_mix_f32 v218, v55, 1.0, v218 op_sel_hi:[1,0,0]
	v_fma_mix_f32 v219, v55, v55, v219 op_sel_hi:[1,1,0]
	v_fma_mix_f32 v218, v55, 1.0, v218 op_sel:[1,0,0] op_sel_hi:[1,0,0]
	v_fma_mix_f32 v219, v55, v55, v219 op_sel:[1,1,0] op_sel_hi:[1,1,0]
	ds_read_b128 v[124:127], v236
	ds_read_b128 v[116:119], v236 offset:1152
	s_waitcnt vmcnt(13)
	v_cvt_f32_f16_e32 v72, v152
	v_cvt_f32_f16_sdwa v73, v152 dst_sel:DWORD dst_unused:UNUSED_PAD src0_sel:WORD_1
	v_cvt_f32_f16_e32 v74, v153
	v_cvt_f32_f16_sdwa v75, v153 dst_sel:DWORD dst_unused:UNUSED_PAD src0_sel:WORD_1
	v_cvt_f32_f16_e32 v80, v154
	v_cvt_f32_f16_sdwa v81, v154 dst_sel:DWORD dst_unused:UNUSED_PAD src0_sel:WORD_1
	v_cvt_f32_f16_e32 v82, v155
	v_cvt_f32_f16_sdwa v83, v155 dst_sel:DWORD dst_unused:UNUSED_PAD src0_sel:WORD_1
	v_sub_f32_e32 v72, v72, v200
	v_sub_f32_e32 v73, v73, v200
	v_sub_f32_e32 v74, v74, v200
	v_sub_f32_e32 v75, v75, v200
	v_sub_f32_e32 v80, v80, v200
	v_sub_f32_e32 v81, v81, v200
	v_sub_f32_e32 v82, v82, v200
	v_sub_f32_e32 v83, v83, v200
	v_pk_mul_f32 v[72:73], v[200:201], v[72:73] op_sel:[1,0]
	v_pk_mul_f32 v[74:75], v[200:201], v[74:75] op_sel:[1,0]
	v_pk_mul_f32 v[80:81], v[200:201], v[80:81] op_sel:[1,0]
	v_pk_mul_f32 v[82:83], v[200:201], v[82:83] op_sel:[1,0]
	v_pk_fma_f32 v[44:45], v[72:73], v[160:161], v[44:45]
	v_pk_fma_f32 v[46:47], v[74:75], v[162:163], v[46:47]
	v_pk_fma_f32 v[40:41], v[80:81], v[164:165], v[40:41]
	v_pk_fma_f32 v[42:43], v[82:83], v[166:167], v[42:43]
	v_cvt_pk_f16_f32 v44, v44, v45
	v_cvt_pk_f16_f32 v45, v46, v47
	v_cvt_pk_f16_f32 v46, v40, v41
	v_cvt_pk_f16_f32 v47, v42, v43
	s_waitcnt lgkmcnt(0)
	v_add_u32_e32 v83, 0x30000, v224
	buffer_store_dwordx4 v[124:127], v83, s[24:27], 0 offen nt
	v_add_u32_e32 v82, 0x33000, v224
	buffer_store_dwordx4 v[116:119], v82, s[24:27], 0 offen nt
	ds_write_b128 v235, v[44:47]
	v_fma_mix_f32 v208, v44, 1.0, 0 op_sel_hi:[1,0,0]
	v_fma_mix_f32 v209, v44, v44, 0 op_sel_hi:[1,1,0]
	v_fma_mix_f32 v208, v44, 1.0, v208 op_sel:[1,0,0] op_sel_hi:[1,0,0]
	v_fma_mix_f32 v209, v44, v44, v209 op_sel:[1,1,0] op_sel_hi:[1,1,0]
	v_fma_mix_f32 v208, v45, 1.0, v208 op_sel_hi:[1,0,0]
	v_fma_mix_f32 v209, v45, v45, v209 op_sel_hi:[1,1,0]
	v_fma_mix_f32 v208, v45, 1.0, v208 op_sel:[1,0,0] op_sel_hi:[1,0,0]
	v_fma_mix_f32 v209, v45, v45, v209 op_sel:[1,1,0] op_sel_hi:[1,1,0]
	v_fma_mix_f32 v208, v46, 1.0, v208 op_sel_hi:[1,0,0]
	v_fma_mix_f32 v209, v46, v46, v209 op_sel_hi:[1,1,0]
	v_fma_mix_f32 v208, v46, 1.0, v208 op_sel:[1,0,0] op_sel_hi:[1,0,0]
	v_fma_mix_f32 v209, v46, v46, v209 op_sel:[1,1,0] op_sel_hi:[1,1,0]
	v_fma_mix_f32 v208, v47, 1.0, v208 op_sel_hi:[1,0,0]
	v_fma_mix_f32 v209, v47, v47, v209 op_sel_hi:[1,1,0]
	v_fma_mix_f32 v208, v47, 1.0, v208 op_sel:[1,0,0] op_sel_hi:[1,0,0]
	v_fma_mix_f32 v209, v47, v47, v209 op_sel:[1,1,0] op_sel_hi:[1,1,0]
	s_waitcnt vmcnt(14)
	v_cvt_f32_f16_e32 v72, v156
	v_cvt_f32_f16_sdwa v73, v156 dst_sel:DWORD dst_unused:UNUSED_PAD src0_sel:WORD_1
	v_cvt_f32_f16_e32 v74, v157
	v_cvt_f32_f16_sdwa v75, v157 dst_sel:DWORD dst_unused:UNUSED_PAD src0_sel:WORD_1
	v_cvt_f32_f16_e32 v80, v158
	v_cvt_f32_f16_sdwa v81, v158 dst_sel:DWORD dst_unused:UNUSED_PAD src0_sel:WORD_1
	v_cvt_f32_f16_e32 v82, v159
	v_cvt_f32_f16_sdwa v83, v159 dst_sel:DWORD dst_unused:UNUSED_PAD src0_sel:WORD_1
	v_sub_f32_e32 v72, v72, v200
	v_sub_f32_e32 v73, v73, v200
	v_sub_f32_e32 v74, v74, v200
	v_sub_f32_e32 v75, v75, v200
	v_sub_f32_e32 v80, v80, v200
	v_sub_f32_e32 v81, v81, v200
	v_sub_f32_e32 v82, v82, v200
	v_sub_f32_e32 v83, v83, v200
	v_pk_mul_f32 v[72:73], v[200:201], v[72:73] op_sel:[1,0]
	v_pk_mul_f32 v[74:75], v[200:201], v[74:75] op_sel:[1,0]
	v_pk_mul_f32 v[80:81], v[200:201], v[80:81] op_sel:[1,0]
	v_pk_mul_f32 v[82:83], v[200:201], v[82:83] op_sel:[1,0]
	v_pk_fma_f32 v[36:37], v[72:73], v[168:169], v[36:37]
	v_pk_fma_f32 v[38:39], v[74:75], v[170:171], v[38:39]
	v_pk_fma_f32 v[32:33], v[80:81], v[172:173], v[32:33]
	v_pk_fma_f32 v[34:35], v[82:83], v[174:175], v[34:35]
	v_cvt_pk_f16_f32 v36, v36, v37
	v_cvt_pk_f16_f32 v37, v38, v39
	v_cvt_pk_f16_f32 v38, v32, v33
	v_cvt_pk_f16_f32 v39, v34, v35
	ds_write_b128 v235, v[36:39] offset:64
	v_fma_mix_f32 v208, v36, 1.0, v208 op_sel_hi:[1,0,0]
	v_fma_mix_f32 v209, v36, v36, v209 op_sel_hi:[1,1,0]
	v_fma_mix_f32 v208, v36, 1.0, v208 op_sel:[1,0,0] op_sel_hi:[1,0,0]
	v_fma_mix_f32 v209, v36, v36, v209 op_sel:[1,1,0] op_sel_hi:[1,1,0]
	v_fma_mix_f32 v208, v37, 1.0, v208 op_sel_hi:[1,0,0]
	v_fma_mix_f32 v209, v37, v37, v209 op_sel_hi:[1,1,0]
	v_fma_mix_f32 v208, v37, 1.0, v208 op_sel:[1,0,0] op_sel_hi:[1,0,0]
	v_fma_mix_f32 v209, v37, v37, v209 op_sel:[1,1,0] op_sel_hi:[1,1,0]
	v_fma_mix_f32 v208, v38, 1.0, v208 op_sel_hi:[1,0,0]
	v_fma_mix_f32 v209, v38, v38, v209 op_sel_hi:[1,1,0]
	v_fma_mix_f32 v208, v38, 1.0, v208 op_sel:[1,0,0] op_sel_hi:[1,0,0]
	v_fma_mix_f32 v209, v38, v38, v209 op_sel:[1,1,0] op_sel_hi:[1,1,0]
	v_fma_mix_f32 v208, v39, 1.0, v208 op_sel_hi:[1,0,0]
	v_fma_mix_f32 v209, v39, v39, v209 op_sel_hi:[1,1,0]
	v_fma_mix_f32 v208, v39, 1.0, v208 op_sel:[1,0,0] op_sel_hi:[1,0,0]
	v_fma_mix_f32 v209, v39, v39, v209 op_sel:[1,1,0] op_sel_hi:[1,1,0]
	ds_read_b128 v[128:131], v236
	ds_read_b128 v[104:107], v236 offset:1152
	s_waitcnt vmcnt(11)
	v_cvt_f32_f16_e32 v72, v212
	v_cvt_f32_f16_sdwa v73, v212 dst_sel:DWORD dst_unused:UNUSED_PAD src0_sel:WORD_1
	v_cvt_f32_f16_e32 v74, v213
	v_cvt_f32_f16_sdwa v75, v213 dst_sel:DWORD dst_unused:UNUSED_PAD src0_sel:WORD_1
	v_cvt_f32_f16_e32 v80, v214
	v_cvt_f32_f16_sdwa v81, v214 dst_sel:DWORD dst_unused:UNUSED_PAD src0_sel:WORD_1
	v_cvt_f32_f16_e32 v82, v215
	v_cvt_f32_f16_sdwa v83, v215 dst_sel:DWORD dst_unused:UNUSED_PAD src0_sel:WORD_1
	v_sub_f32_e32 v72, v72, v202
	v_sub_f32_e32 v73, v73, v202
	v_sub_f32_e32 v74, v74, v202
	v_sub_f32_e32 v75, v75, v202
	v_sub_f32_e32 v80, v80, v202
	v_sub_f32_e32 v81, v81, v202
	v_sub_f32_e32 v82, v82, v202
	v_sub_f32_e32 v83, v83, v202
	v_pk_mul_f32 v[72:73], v[202:203], v[72:73] op_sel:[1,0]
	v_pk_mul_f32 v[74:75], v[202:203], v[74:75] op_sel:[1,0]
	v_pk_mul_f32 v[80:81], v[202:203], v[80:81] op_sel:[1,0]
	v_pk_mul_f32 v[82:83], v[202:203], v[82:83] op_sel:[1,0]
	v_pk_fma_f32 v[28:29], v[72:73], v[160:161], v[28:29]
	v_pk_fma_f32 v[30:31], v[74:75], v[162:163], v[30:31]
	v_pk_fma_f32 v[24:25], v[80:81], v[164:165], v[24:25]
	v_pk_fma_f32 v[26:27], v[82:83], v[166:167], v[26:27]
	v_cvt_pk_f16_f32 v28, v28, v29
	v_cvt_pk_f16_f32 v29, v30, v31
	v_cvt_pk_f16_f32 v30, v24, v25
	v_cvt_pk_f16_f32 v31, v26, v27
	s_waitcnt lgkmcnt(0)
	v_add_u32_e32 v83, 0x36000, v224
	buffer_store_dwordx4 v[128:131], v83, s[24:27], 0 offen nt
	v_add_u32_e32 v82, 0x39000, v224
	buffer_store_dwordx4 v[104:107], v82, s[24:27], 0 offen nt
	ds_write_b128 v235, v[28:31]
	v_fma_mix_f32 v210, v28, 1.0, 0 op_sel_hi:[1,0,0]
	v_fma_mix_f32 v211, v28, v28, 0 op_sel_hi:[1,1,0]
	v_fma_mix_f32 v210, v28, 1.0, v210 op_sel:[1,0,0] op_sel_hi:[1,0,0]
	v_fma_mix_f32 v211, v28, v28, v211 op_sel:[1,1,0] op_sel_hi:[1,1,0]
	v_fma_mix_f32 v210, v29, 1.0, v210 op_sel_hi:[1,0,0]
	v_fma_mix_f32 v211, v29, v29, v211 op_sel_hi:[1,1,0]
	v_fma_mix_f32 v210, v29, 1.0, v210 op_sel:[1,0,0] op_sel_hi:[1,0,0]
	v_fma_mix_f32 v211, v29, v29, v211 op_sel:[1,1,0] op_sel_hi:[1,1,0]
	v_fma_mix_f32 v210, v30, 1.0, v210 op_sel_hi:[1,0,0]
	v_fma_mix_f32 v211, v30, v30, v211 op_sel_hi:[1,1,0]
	v_fma_mix_f32 v210, v30, 1.0, v210 op_sel:[1,0,0] op_sel_hi:[1,0,0]
	v_fma_mix_f32 v211, v30, v30, v211 op_sel:[1,1,0] op_sel_hi:[1,1,0]
	v_fma_mix_f32 v210, v31, 1.0, v210 op_sel_hi:[1,0,0]
	v_fma_mix_f32 v211, v31, v31, v211 op_sel_hi:[1,1,0]
	v_fma_mix_f32 v210, v31, 1.0, v210 op_sel:[1,0,0] op_sel_hi:[1,0,0]
	v_fma_mix_f32 v211, v31, v31, v211 op_sel:[1,1,0] op_sel_hi:[1,1,0]
	s_waitcnt vmcnt(12)
	v_cvt_f32_f16_e32 v72, v144
	v_cvt_f32_f16_sdwa v73, v144 dst_sel:DWORD dst_unused:UNUSED_PAD src0_sel:WORD_1
	v_cvt_f32_f16_e32 v74, v145
	v_cvt_f32_f16_sdwa v75, v145 dst_sel:DWORD dst_unused:UNUSED_PAD src0_sel:WORD_1
	v_cvt_f32_f16_e32 v80, v146
	v_cvt_f32_f16_sdwa v81, v146 dst_sel:DWORD dst_unused:UNUSED_PAD src0_sel:WORD_1
	v_cvt_f32_f16_e32 v82, v147
	v_cvt_f32_f16_sdwa v83, v147 dst_sel:DWORD dst_unused:UNUSED_PAD src0_sel:WORD_1
	v_sub_f32_e32 v72, v72, v202
	v_sub_f32_e32 v73, v73, v202
	v_sub_f32_e32 v74, v74, v202
	v_sub_f32_e32 v75, v75, v202
	v_sub_f32_e32 v80, v80, v202
	v_sub_f32_e32 v81, v81, v202
	v_sub_f32_e32 v82, v82, v202
	v_sub_f32_e32 v83, v83, v202
	v_pk_mul_f32 v[72:73], v[202:203], v[72:73] op_sel:[1,0]
	v_pk_mul_f32 v[74:75], v[202:203], v[74:75] op_sel:[1,0]
	v_pk_mul_f32 v[80:81], v[202:203], v[80:81] op_sel:[1,0]
	v_pk_mul_f32 v[82:83], v[202:203], v[82:83] op_sel:[1,0]
	v_pk_fma_f32 v[20:21], v[72:73], v[168:169], v[20:21]
	v_pk_fma_f32 v[22:23], v[74:75], v[170:171], v[22:23]
	v_pk_fma_f32 v[16:17], v[80:81], v[172:173], v[16:17]
	v_pk_fma_f32 v[18:19], v[82:83], v[174:175], v[18:19]
	v_cvt_pk_f16_f32 v20, v20, v21
	v_cvt_pk_f16_f32 v21, v22, v23
	v_cvt_pk_f16_f32 v22, v16, v17
	v_cvt_pk_f16_f32 v23, v18, v19
	ds_write_b128 v235, v[20:23] offset:64
	v_fma_mix_f32 v210, v20, 1.0, v210 op_sel_hi:[1,0,0]
	v_fma_mix_f32 v211, v20, v20, v211 op_sel_hi:[1,1,0]
	v_fma_mix_f32 v210, v20, 1.0, v210 op_sel:[1,0,0] op_sel_hi:[1,0,0]
	v_fma_mix_f32 v211, v20, v20, v211 op_sel:[1,1,0] op_sel_hi:[1,1,0]
	v_fma_mix_f32 v210, v21, 1.0, v210 op_sel_hi:[1,0,0]
	v_fma_mix_f32 v211, v21, v21, v211 op_sel_hi:[1,1,0]
	v_fma_mix_f32 v210, v21, 1.0, v210 op_sel:[1,0,0] op_sel_hi:[1,0,0]
	v_fma_mix_f32 v211, v21, v21, v211 op_sel:[1,1,0] op_sel_hi:[1,1,0]
	v_fma_mix_f32 v210, v22, 1.0, v210 op_sel_hi:[1,0,0]
	v_fma_mix_f32 v211, v22, v22, v211 op_sel_hi:[1,1,0]
	v_fma_mix_f32 v210, v22, 1.0, v210 op_sel:[1,0,0] op_sel_hi:[1,0,0]
	v_fma_mix_f32 v211, v22, v22, v211 op_sel:[1,1,0] op_sel_hi:[1,1,0]
	v_fma_mix_f32 v210, v23, 1.0, v210 op_sel_hi:[1,0,0]
	v_fma_mix_f32 v211, v23, v23, v211 op_sel_hi:[1,1,0]
	v_fma_mix_f32 v210, v23, 1.0, v210 op_sel:[1,0,0] op_sel_hi:[1,0,0]
	v_fma_mix_f32 v211, v23, v23, v211 op_sel:[1,1,0] op_sel_hi:[1,1,0]
	ds_read_b128 v[240:243], v236
	ds_read_b128 v[96:99], v236 offset:1152
	s_waitcnt vmcnt(11)
	v_cvt_f32_f16_e32 v72, v132
	v_cvt_f32_f16_sdwa v73, v132 dst_sel:DWORD dst_unused:UNUSED_PAD src0_sel:WORD_1
	v_cvt_f32_f16_e32 v74, v133
	v_cvt_f32_f16_sdwa v75, v133 dst_sel:DWORD dst_unused:UNUSED_PAD src0_sel:WORD_1
	v_cvt_f32_f16_e32 v80, v134
	v_cvt_f32_f16_sdwa v81, v134 dst_sel:DWORD dst_unused:UNUSED_PAD src0_sel:WORD_1
	v_cvt_f32_f16_e32 v82, v135
	v_cvt_f32_f16_sdwa v83, v135 dst_sel:DWORD dst_unused:UNUSED_PAD src0_sel:WORD_1
	v_sub_f32_e32 v72, v72, v204
	v_sub_f32_e32 v73, v73, v204
	v_sub_f32_e32 v74, v74, v204
	v_sub_f32_e32 v75, v75, v204
	v_sub_f32_e32 v80, v80, v204
	v_sub_f32_e32 v81, v81, v204
	v_sub_f32_e32 v82, v82, v204
	v_sub_f32_e32 v83, v83, v204
	v_pk_mul_f32 v[72:73], v[204:205], v[72:73] op_sel:[1,0]
	v_pk_mul_f32 v[74:75], v[204:205], v[74:75] op_sel:[1,0]
	v_pk_mul_f32 v[80:81], v[204:205], v[80:81] op_sel:[1,0]
	v_pk_mul_f32 v[82:83], v[204:205], v[82:83] op_sel:[1,0]
	v_pk_fma_f32 v[12:13], v[72:73], v[160:161], v[12:13]
	v_pk_fma_f32 v[14:15], v[74:75], v[162:163], v[14:15]
	v_pk_fma_f32 v[8:9], v[80:81], v[164:165], v[8:9]
	v_pk_fma_f32 v[10:11], v[82:83], v[166:167], v[10:11]
	v_cvt_pk_f16_f32 v12, v12, v13
	v_cvt_pk_f16_f32 v13, v14, v15
	v_cvt_pk_f16_f32 v14, v8, v9
	v_cvt_pk_f16_f32 v15, v10, v11
	s_waitcnt lgkmcnt(0)
	v_add_u32_e32 v83, 0x3c000, v224
	buffer_store_dwordx4 v[240:243], v83, s[24:27], 0 offen nt
	v_add_u32_e32 v82, 0x3f000, v224
	buffer_store_dwordx4 v[96:99], v82, s[24:27], 0 offen nt
	ds_write_b128 v235, v[12:15]
	v_fma_mix_f32 v244, v12, 1.0, 0 op_sel_hi:[1,0,0]
	v_fma_mix_f32 v245, v12, v12, 0 op_sel_hi:[1,1,0]
	v_fma_mix_f32 v244, v12, 1.0, v244 op_sel:[1,0,0] op_sel_hi:[1,0,0]
	v_fma_mix_f32 v245, v12, v12, v245 op_sel:[1,1,0] op_sel_hi:[1,1,0]
	v_fma_mix_f32 v244, v13, 1.0, v244 op_sel_hi:[1,0,0]
	v_fma_mix_f32 v245, v13, v13, v245 op_sel_hi:[1,1,0]
	v_fma_mix_f32 v244, v13, 1.0, v244 op_sel:[1,0,0] op_sel_hi:[1,0,0]
	v_fma_mix_f32 v245, v13, v13, v245 op_sel:[1,1,0] op_sel_hi:[1,1,0]
	v_fma_mix_f32 v244, v14, 1.0, v244 op_sel_hi:[1,0,0]
	v_fma_mix_f32 v245, v14, v14, v245 op_sel_hi:[1,1,0]
	v_fma_mix_f32 v244, v14, 1.0, v244 op_sel:[1,0,0] op_sel_hi:[1,0,0]
	v_fma_mix_f32 v245, v14, v14, v245 op_sel:[1,1,0] op_sel_hi:[1,1,0]
	v_fma_mix_f32 v244, v15, 1.0, v244 op_sel_hi:[1,0,0]
	v_fma_mix_f32 v245, v15, v15, v245 op_sel_hi:[1,1,0]
	v_fma_mix_f32 v244, v15, 1.0, v244 op_sel:[1,0,0] op_sel_hi:[1,0,0]
	v_fma_mix_f32 v245, v15, v15, v245 op_sel:[1,1,0] op_sel_hi:[1,1,0]
	s_waitcnt vmcnt(12)
	v_cvt_f32_f16_e32 v72, v88
	v_cvt_f32_f16_sdwa v73, v88 dst_sel:DWORD dst_unused:UNUSED_PAD src0_sel:WORD_1
	v_cvt_f32_f16_e32 v74, v89
	v_cvt_f32_f16_sdwa v75, v89 dst_sel:DWORD dst_unused:UNUSED_PAD src0_sel:WORD_1
	v_cvt_f32_f16_e32 v80, v90
	v_cvt_f32_f16_sdwa v81, v90 dst_sel:DWORD dst_unused:UNUSED_PAD src0_sel:WORD_1
	v_cvt_f32_f16_e32 v82, v91
	v_cvt_f32_f16_sdwa v83, v91 dst_sel:DWORD dst_unused:UNUSED_PAD src0_sel:WORD_1
	v_sub_f32_e32 v72, v72, v204
	v_sub_f32_e32 v73, v73, v204
	v_sub_f32_e32 v74, v74, v204
	v_sub_f32_e32 v75, v75, v204
	v_sub_f32_e32 v80, v80, v204
	v_sub_f32_e32 v81, v81, v204
	v_sub_f32_e32 v82, v82, v204
	v_sub_f32_e32 v83, v83, v204
	v_pk_mul_f32 v[72:73], v[204:205], v[72:73] op_sel:[1,0]
	v_pk_mul_f32 v[74:75], v[204:205], v[74:75] op_sel:[1,0]
	v_pk_mul_f32 v[80:81], v[204:205], v[80:81] op_sel:[1,0]
	v_pk_mul_f32 v[82:83], v[204:205], v[82:83] op_sel:[1,0]
	v_pk_fma_f32 v[4:5], v[72:73], v[168:169], v[4:5]
	v_pk_fma_f32 v[6:7], v[74:75], v[170:171], v[6:7]
	v_pk_fma_f32 v[0:1], v[80:81], v[172:173], v[0:1]
	v_pk_fma_f32 v[2:3], v[82:83], v[174:175], v[2:3]
	v_cvt_pk_f16_f32 v4, v4, v5
	v_cvt_pk_f16_f32 v5, v6, v7
	v_cvt_pk_f16_f32 v6, v0, v1
	v_cvt_pk_f16_f32 v7, v2, v3
	ds_write_b128 v235, v[4:7] offset:64
	v_fma_mix_f32 v244, v4, 1.0, v244 op_sel_hi:[1,0,0]
	v_fma_mix_f32 v245, v4, v4, v245 op_sel_hi:[1,1,0]
	v_fma_mix_f32 v244, v4, 1.0, v244 op_sel:[1,0,0] op_sel_hi:[1,0,0]
	v_fma_mix_f32 v245, v4, v4, v245 op_sel:[1,1,0] op_sel_hi:[1,1,0]
	v_fma_mix_f32 v244, v5, 1.0, v244 op_sel_hi:[1,0,0]
	v_fma_mix_f32 v245, v5, v5, v245 op_sel_hi:[1,1,0]
	v_fma_mix_f32 v244, v5, 1.0, v244 op_sel:[1,0,0] op_sel_hi:[1,0,0]
	v_fma_mix_f32 v245, v5, v5, v245 op_sel:[1,1,0] op_sel_hi:[1,1,0]
	v_fma_mix_f32 v244, v6, 1.0, v244 op_sel_hi:[1,0,0]
	v_fma_mix_f32 v245, v6, v6, v245 op_sel_hi:[1,1,0]
	v_fma_mix_f32 v244, v6, 1.0, v244 op_sel:[1,0,0] op_sel_hi:[1,0,0]
	v_fma_mix_f32 v245, v6, v6, v245 op_sel:[1,1,0] op_sel_hi:[1,1,0]
	v_fma_mix_f32 v244, v7, 1.0, v244 op_sel_hi:[1,0,0]
	v_fma_mix_f32 v245, v7, v7, v245 op_sel_hi:[1,1,0]
	v_fma_mix_f32 v244, v7, 1.0, v244 op_sel:[1,0,0] op_sel_hi:[1,0,0]
	v_fma_mix_f32 v245, v7, v7, v245 op_sel:[1,1,0] op_sel_hi:[1,1,0]
	ds_read_b128 v[108:111], v236
	ds_read_b128 v[100:103], v236 offset:1152
	s_waitcnt lgkmcnt(0)
	v_add_u32_e32 v83, 0x42000, v224
	buffer_store_dwordx4 v[108:111], v83, s[24:27], 0 offen nt
	v_add_u32_e32 v82, 0x45000, v224
	buffer_store_dwordx4 v[100:103], v82, s[24:27], 0 offen nt
	v_xor_b32_e32 v225, 16, v234
	v_lshlrev_b32_e32 v225, 2, v225
	v_xor_b32_e32 v246, 32, v234
	v_lshlrev_b32_e32 v246, 2, v246
	ds_bpermute_b32 v92, v225, v206
	ds_bpermute_b32 v93, v225, v207
	ds_bpermute_b32 v94, v225, v140
	ds_bpermute_b32 v95, v225, v141
	ds_bpermute_b32 v120, v225, v142
	ds_bpermute_b32 v121, v225, v143
	ds_bpermute_b32 v122, v225, v216
	ds_bpermute_b32 v123, v225, v217
	s_waitcnt lgkmcnt(0)
	v_pk_add_f32 v[206:207], v[206:207], v[92:93]
	v_pk_add_f32 v[140:141], v[140:141], v[94:95]
	v_pk_add_f32 v[142:143], v[142:143], v[120:121]
	v_pk_add_f32 v[216:217], v[216:217], v[122:123]
	ds_bpermute_b32 v92, v225, v218
	ds_bpermute_b32 v93, v225, v219
	ds_bpermute_b32 v94, v225, v208
	ds_bpermute_b32 v95, v225, v209
	ds_bpermute_b32 v120, v225, v210
	ds_bpermute_b32 v121, v225, v211
	ds_bpermute_b32 v122, v225, v244
	ds_bpermute_b32 v123, v225, v245
	s_waitcnt lgkmcnt(0)
	v_pk_add_f32 v[218:219], v[218:219], v[92:93]
	v_pk_add_f32 v[208:209], v[208:209], v[94:95]
	v_pk_add_f32 v[210:211], v[210:211], v[120:121]
	v_pk_add_f32 v[244:245], v[244:245], v[122:123]
	ds_bpermute_b32 v92, v246, v206
	ds_bpermute_b32 v93, v246, v207
	ds_bpermute_b32 v94, v246, v140
	ds_bpermute_b32 v95, v246, v141
	ds_bpermute_b32 v120, v246, v142
	ds_bpermute_b32 v121, v246, v143
	ds_bpermute_b32 v122, v246, v216
	ds_bpermute_b32 v123, v246, v217
	s_waitcnt lgkmcnt(0)
	v_pk_add_f32 v[206:207], v[206:207], v[92:93]
	v_pk_add_f32 v[140:141], v[140:141], v[94:95]
	v_pk_add_f32 v[142:143], v[142:143], v[120:121]
	v_pk_add_f32 v[216:217], v[216:217], v[122:123]
	ds_bpermute_b32 v92, v246, v218
	ds_bpermute_b32 v93, v246, v219
	ds_bpermute_b32 v94, v246, v208
	ds_bpermute_b32 v95, v246, v209
	ds_bpermute_b32 v120, v246, v210
	ds_bpermute_b32 v121, v246, v211
	ds_bpermute_b32 v122, v246, v244
	ds_bpermute_b32 v123, v246, v245
	s_waitcnt lgkmcnt(0)
	v_pk_add_f32 v[218:219], v[218:219], v[92:93]
	v_pk_add_f32 v[208:209], v[208:209], v[94:95]
	v_pk_add_f32 v[210:211], v[210:211], v[120:121]
	v_pk_add_f32 v[244:245], v[244:245], v[122:123]
	s_mov_b64 exec, 0xffff
	global_store_dwordx2 v190, v[206:207], s[100:101] offset:0
	global_store_dwordx2 v190, v[140:141], s[100:101] offset:128
	global_store_dwordx2 v190, v[142:143], s[100:101] offset:256
	global_store_dwordx2 v190, v[216:217], s[100:101] offset:384
	global_store_dwordx2 v190, v[218:219], s[100:101] offset:1024
	global_store_dwordx2 v190, v[208:209], s[100:101] offset:1152
	global_store_dwordx2 v190, v[210:211], s[100:101] offset:1280
	global_store_dwordx2 v190, v[244:245], s[100:101] offset:1408
	s_mov_b64 exec, -1
	s_mov_b32 s83, s81
	s_mov_b32 s84, s82
	s_mov_b64 s[40:41], s[0:1]
	s_mov_b64 s[38:39], s[8:9]
	s_mov_b64 vcc, s[6:7]
	s_cbranch_vccz .LBB10_12
	s_waitcnt vmcnt(0)
	s_cmpk_gt_u32 s44, 0xff
	s_cbranch_scc1 .LBB10_31
	s_barrier

.LBB10_32:
	s_endpgm
	s_endpgm
	s_endpgm
	s_endpgm
	s_endpgm
	s_endpgm
	s_endpgm
	s_endpgm
	s_endpgm
	s_endpgm
	s_endpgm
	s_endpgm
	s_endpgm
	s_endpgm
	s_endpgm
	s_endpgm
	s_endpgm
	s_endpgm
	s_endpgm
	s_endpgm
	s_endpgm
	s_endpgm
	s_endpgm
	s_endpgm
	.section	.rodata,"a",@progbits
	.p2align	6, 0x0

amdhsa.kernels:
  - .agpr_count:     16
    .args:
      - .actual_access:  read_only
        .address_space:  global
        .offset:         0
        .size:           8
        .value_kind:     global_buffer
      - .actual_access:  read_only
        .address_space:  global
        .offset:         8
        .size:           8
        .value_kind:     global_buffer
      - .actual_access:  write_only
        .address_space:  global
        .offset:         16
        .size:           8
        .value_kind:     global_buffer
    .group_segment_fixed_size: 45056
    .kernarg_segment_align: 8
    .kernarg_segment_size: 24
    .language:       OpenCL C
    .language_version:
      - 2
      - 0
    .max_flat_workgroup_size: 256
    .name:           _Z6k_attnPKDF16_PKfPDF16_
    .private_segment_fixed_size: 0
    .sgpr_count:     16
    .sgpr_spill_count: 0
    .symbol:         _Z6k_attnPKDF16_PKfPDF16_.kd
    .uniform_work_group_size: 1
    .uses_dynamic_stack: false
    .vgpr_count:     84
    .vgpr_spill_count: 0
    .wavefront_size: 64
  - .agpr_count:     0
    .args:
      - .actual_access:  read_only
        .address_space:  global
        .offset:         0
        .size:           8
        .value_kind:     global_buffer
      - .actual_access:  read_only
        .address_space:  global
        .offset:         8
        .size:           8
        .value_kind:     global_buffer
      - .actual_access:  write_only
        .address_space:  global
        .offset:         16
        .size:           8
        .value_kind:     global_buffer
      - .actual_access:  write_only
        .address_space:  global
        .offset:         24
        .size:           8
        .value_kind:     global_buffer
      - .actual_access:  write_only
        .address_space:  global
        .offset:         32
        .size:           8
        .value_kind:     global_buffer
      - .actual_access:  write_only
        .address_space:  global
        .offset:         40
        .size:           8
        .value_kind:     global_buffer
    .group_segment_fixed_size: 0
    .kernarg_segment_align: 8
    .kernarg_segment_size: 48
    .language:       OpenCL C
    .language_version:
      - 2
      - 0
    .max_flat_workgroup_size: 256
    .name:           _Z11k_prep_miscPKiPKfPfPDv2_fS3_S3_
    .private_segment_fixed_size: 0
    .sgpr_count:     16
    .sgpr_spill_count: 0
    .symbol:         _Z11k_prep_miscPKiPKfPfPDv2_fS3_S3_.kd
    .uniform_work_group_size: 1
    .uses_dynamic_stack: false
    .vgpr_count:     6
    .vgpr_spill_count: 0
    .wavefront_size: 64
  - .agpr_count:     0
    .args:
      - .actual_access:  read_only
        .address_space:  global
        .offset:         0
        .size:           8
        .value_kind:     global_buffer
      - .actual_access:  write_only
        .address_space:  global
        .offset:         8
        .size:           8
        .value_kind:     global_buffer
    .group_segment_fixed_size: 0
    .kernarg_segment_align: 8
    .kernarg_segment_size: 16
    .language:       OpenCL C
    .language_version:
      - 2
      - 0
    .max_flat_workgroup_size: 256
    .name:           _Z7k_cvt_xPKfPDF16_
    .private_segment_fixed_size: 0
    .sgpr_count:     14
    .sgpr_spill_count: 0
    .symbol:         _Z7k_cvt_xPKfPDF16_.kd
    .uniform_work_group_size: 1
    .uses_dynamic_stack: false
    .vgpr_count:     12
    .vgpr_spill_count: 0
    .wavefront_size: 64
  - .agpr_count:     0
    .args:
      - .offset:         0
        .size:           176
        .value_kind:     by_value
    .group_segment_fixed_size: 9216
    .kernarg_segment_align: 8
    .kernarg_segment_size: 176
    .language:       OpenCL C
    .language_version:
      - 2
      - 0
    .max_flat_workgroup_size: 256
    .name:           _Z8k_wtrans8PrepArgs
    .private_segment_fixed_size: 0
    .sgpr_count:     44
    .sgpr_spill_count: 0
    .symbol:         _Z8k_wtrans8PrepArgs.kd
    .uniform_work_group_size: 1
    .uses_dynamic_stack: false
    .vgpr_count:     18
    .vgpr_spill_count: 0
    .wavefront_size: 64
  - .agpr_count:     0
    .args:
      - .offset:         0
        .size:           176
        .value_kind:     by_value
      - .actual_access:  read_only
        .address_space:  global
        .offset:         176
        .size:           8
        .value_kind:     global_buffer
      - .actual_access:  read_only
        .address_space:  global
        .offset:         184
        .size:           8
        .value_kind:     global_buffer
    .group_segment_fixed_size: 2048
    .kernarg_segment_align: 8
    .kernarg_segment_size: 192
    .language:       OpenCL C
    .language_version:
      - 2
      - 0
    .max_flat_workgroup_size: 256
    .name:           _Z8k_colvec8PrepArgsPKfS1_
    .private_segment_fixed_size: 0
    .sgpr_count:     38
    .sgpr_spill_count: 0
    .symbol:         _Z8k_colvec8PrepArgsPKfS1_.kd
    .uniform_work_group_size: 1
    .uses_dynamic_stack: false
    .vgpr_count:     114
    .vgpr_spill_count: 0
    .wavefront_size: 64
  - .agpr_count:     0
    .args:
      - .actual_access:  read_only
        .address_space:  global
        .offset:         0
        .size:           8
        .value_kind:     global_buffer
      - .actual_access:  write_only
        .address_space:  global
        .offset:         8
        .size:           8
        .value_kind:     global_buffer
    .group_segment_fixed_size: 0
    .kernarg_segment_align: 8
    .kernarg_segment_size: 16
    .language:       OpenCL C
    .language_version:
      - 2
      - 0
    .max_flat_workgroup_size: 256
    .name:           _Z9k_rowstatPKDv2_fPS_
    .private_segment_fixed_size: 0
    .sgpr_count:     16
    .sgpr_spill_count: 0
    .symbol:         _Z9k_rowstatPKDv2_fPS_.kd
    .uniform_work_group_size: 1
    .uses_dynamic_stack: false
    .vgpr_count:     28
    .vgpr_spill_count: 0
    .wavefront_size: 64
  - .agpr_count:     0
    .args:
      - .actual_access:  read_only
        .address_space:  global
        .offset:         0
        .size:           8
        .value_kind:     global_buffer
      - .actual_access:  read_only
        .address_space:  global
        .offset:         8
        .size:           8
        .value_kind:     global_buffer
      - .actual_access:  read_only
        .address_space:  global
        .offset:         16
        .size:           8
        .value_kind:     global_buffer
      - .actual_access:  read_only
        .address_space:  global
        .offset:         24
        .size:           8
        .value_kind:     global_buffer
      - .actual_access:  write_only
        .address_space:  global
        .offset:         32
        .size:           8
        .value_kind:     global_buffer
    .group_segment_fixed_size: 0
    .kernarg_segment_align: 8
    .kernarg_segment_size: 40
    .language:       OpenCL C
    .language_version:
      - 2
      - 0
    .max_flat_workgroup_size: 256
    .name:           _Z10k_final_lnPKDF16_PKDv2_fPKfS5_Pf
    .private_segment_fixed_size: 0
    .sgpr_count:     19
    .sgpr_spill_count: 0
    .symbol:         _Z10k_final_lnPKDF16_PKDv2_fPKfS5_Pf.kd
    .uniform_work_group_size: 1
    .uses_dynamic_stack: false
    .vgpr_count:     19
    .vgpr_spill_count: 0
    .wavefront_size: 64
  - .agpr_count:     0
    .args:
      - .offset:         0
        .size:           32
        .value_kind:     by_value
      - .offset:         32
        .size:           32
        .value_kind:     by_value
      - .offset:         64
        .size:           4
        .value_kind:     hidden_block_count_x
      - .offset:         68
        .size:           4
        .value_kind:     hidden_block_count_y
      - .offset:         72
        .size:           4
        .value_kind:     hidden_block_count_z
      - .offset:         76
        .size:           2
        .value_kind:     hidden_group_size_x
      - .offset:         78
        .size:           2
        .value_kind:     hidden_group_size_y
      - .offset:         80
        .size:           2
        .value_kind:     hidden_group_size_z
      - .offset:         82
        .size:           2
        .value_kind:     hidden_remainder_x
      - .offset:         84
        .size:           2
        .value_kind:     hidden_remainder_y
      - .offset:         86
        .size:           2
        .value_kind:     hidden_remainder_z
      - .offset:         104
        .size:           8
        .value_kind:     hidden_global_offset_x
      - .offset:         112
        .size:           8
        .value_kind:     hidden_global_offset_y
      - .offset:         120
        .size:           8
        .value_kind:     hidden_global_offset_z
      - .offset:         128
        .size:           2
        .value_kind:     hidden_grid_dims
      - .offset:         184
        .size:           4
        .value_kind:     hidden_dynamic_lds_size
    .group_segment_fixed_size: 0
    .kernarg_segment_align: 8
    .kernarg_segment_size: 320
    .language:       OpenCL C
    .language_version:
      - 2
      - 0
    .max_flat_workgroup_size: 512
    .name:           _Z6k_gemmIN2pg6EpiLinILi0EEELi768EEvNS0_4GemmET_
    .private_segment_fixed_size: 0
    .sgpr_count:     88
    .sgpr_spill_count: 0
    .symbol:         _Z6k_gemmIN2pg6EpiLinILi0EEELi768EEvNS0_4GemmET_.kd
    .uniform_work_group_size: 1
    .uses_dynamic_stack: false
    .vgpr_count:     256
    .vgpr_spill_count: 0
    .wavefront_size: 64
  - .agpr_count:     0
    .args:
      - .offset:         0
        .size:           32
        .value_kind:     by_value
      - .offset:         32
        .size:           56
        .value_kind:     by_value
      - .offset:         88
        .size:           4
        .value_kind:     hidden_block_count_x
      - .offset:         92
        .size:           4
        .value_kind:     hidden_block_count_y
      - .offset:         96
        .size:           4
        .value_kind:     hidden_block_count_z
      - .offset:         100
        .size:           2
        .value_kind:     hidden_group_size_x
      - .offset:         102
        .size:           2
        .value_kind:     hidden_group_size_y
      - .offset:         104
        .size:           2
        .value_kind:     hidden_group_size_z
      - .offset:         106
        .size:           2
        .value_kind:     hidden_remainder_x
      - .offset:         108
        .size:           2
        .value_kind:     hidden_remainder_y
      - .offset:         110
        .size:           2
        .value_kind:     hidden_remainder_z
      - .offset:         128
        .size:           8
        .value_kind:     hidden_global_offset_x
      - .offset:         136
        .size:           8
        .value_kind:     hidden_global_offset_y
      - .offset:         144
        .size:           8
        .value_kind:     hidden_global_offset_z
      - .offset:         152
        .size:           2
        .value_kind:     hidden_grid_dims
      - .offset:         208
        .size:           4
        .value_kind:     hidden_dynamic_lds_size
    .group_segment_fixed_size: 0
    .kernarg_segment_align: 8
    .kernarg_segment_size: 344
    .language:       OpenCL C
    .language_version:
      - 2
      - 0
    .max_flat_workgroup_size: 512
    .name:           _Z6k_gemmIN2pg6EpiResELi768EEvNS0_4GemmET_
    .private_segment_fixed_size: 0
    .sgpr_count:     108
    .sgpr_spill_count: 0
    .symbol:         _Z6k_gemmIN2pg6EpiResELi768EEvNS0_4GemmET_.kd
    .uniform_work_group_size: 1
    .uses_dynamic_stack: false
    .vgpr_count:     256
    .vgpr_spill_count: 0
    .wavefront_size: 64
  - .agpr_count:     0
    .args:
      - .offset:         0
        .size:           32
        .value_kind:     by_value
      - .offset:         32
        .size:           32
        .value_kind:     by_value
      - .offset:         64
        .size:           4
        .value_kind:     hidden_block_count_x
      - .offset:         68
        .size:           4
        .value_kind:     hidden_block_count_y
      - .offset:         72
        .size:           4
        .value_kind:     hidden_block_count_z
      - .offset:         76
        .size:           2
        .value_kind:     hidden_group_size_x
      - .offset:         78
        .size:           2
        .value_kind:     hidden_group_size_y
      - .offset:         80
        .size:           2
        .value_kind:     hidden_group_size_z
      - .offset:         82
        .size:           2
        .value_kind:     hidden_remainder_x
      - .offset:         84
        .size:           2
        .value_kind:     hidden_remainder_y
      - .offset:         86
        .size:           2
        .value_kind:     hidden_remainder_z
      - .offset:         104
        .size:           8
        .value_kind:     hidden_global_offset_x
      - .offset:         112
        .size:           8
        .value_kind:     hidden_global_offset_y
      - .offset:         120
        .size:           8
        .value_kind:     hidden_global_offset_z
      - .offset:         128
        .size:           2
        .value_kind:     hidden_grid_dims
      - .offset:         184
        .size:           4
        .value_kind:     hidden_dynamic_lds_size
    .group_segment_fixed_size: 0
    .kernarg_segment_align: 8
    .kernarg_segment_size: 320
    .language:       OpenCL C
    .language_version:
      - 2
      - 0
    .max_flat_workgroup_size: 512
    .name:           _Z6k_gemmIN2pg6EpiLinILi1EEELi768EEvNS0_4GemmET_
    .private_segment_fixed_size: 0
    .sgpr_count:     88
    .sgpr_spill_count: 0
    .symbol:         _Z6k_gemmIN2pg6EpiLinILi1EEELi768EEvNS0_4GemmET_.kd
    .uniform_work_group_size: 1
    .uses_dynamic_stack: false
    .vgpr_count:     256
    .vgpr_spill_count: 0
    .wavefront_size: 64
  - .agpr_count:     0
    .args:
      - .offset:         0
        .size:           32
        .value_kind:     by_value
      - .offset:         32
        .size:           56
        .value_kind:     by_value
      - .offset:         88
        .size:           4
        .value_kind:     hidden_block_count_x
      - .offset:         92
        .size:           4
        .value_kind:     hidden_block_count_y
      - .offset:         96
        .size:           4
        .value_kind:     hidden_block_count_z
      - .offset:         100
        .size:           2
        .value_kind:     hidden_group_size_x
      - .offset:         102
        .size:           2
        .value_kind:     hidden_group_size_y
      - .offset:         104
        .size:           2
        .value_kind:     hidden_group_size_z
      - .offset:         106
        .size:           2
        .value_kind:     hidden_remainder_x
      - .offset:         108
        .size:           2
        .value_kind:     hidden_remainder_y
      - .offset:         110
        .size:           2
        .value_kind:     hidden_remainder_z
      - .offset:         128
        .size:           8
        .value_kind:     hidden_global_offset_x
      - .offset:         136
        .size:           8
        .value_kind:     hidden_global_offset_y
      - .offset:         144
        .size:           8
        .value_kind:     hidden_global_offset_z
      - .offset:         152
        .size:           2
        .value_kind:     hidden_grid_dims
      - .offset:         208
        .size:           4
        .value_kind:     hidden_dynamic_lds_size
    .group_segment_fixed_size: 0
    .kernarg_segment_align: 8
    .kernarg_segment_size: 344
    .language:       OpenCL C
    .language_version:
      - 2
      - 0
    .max_flat_workgroup_size: 512
    .name:           _Z6k_gemmIN2pg6EpiResELi3072EEvNS0_4GemmET_
    .private_segment_fixed_size: 0
    .sgpr_count:     108
    .sgpr_spill_count: 0
    .symbol:         _Z6k_gemmIN2pg6EpiResELi3072EEvNS0_4GemmET_.kd
    .uniform_work_group_size: 1
    .uses_dynamic_stack: false
    .vgpr_count:     256
    .vgpr_spill_count: 0
    .wavefront_size: 64
